# GEMM K-loops: first iteration of every unit peeled with constant-0 accumulate operand, the 127 accumulator-clearing v_mov per unit deleted (all 8 GEMM instances); stacked
# speedup vs baseline: 1.0047x; 1.0029x over previous
.LBB0_84:
	s_ashr_i32 s15, s14, 31
	v_cmp_lt_i64_e32 vcc, s[16:17], v[142:143]
	s_lshl_b64 s[16:17], s[14:15], 20
	s_add_u32 s16, s36, s16
	s_addc_u32 s17, s37, s17
	s_and_b64 s[22:23], vcc, exec
	s_cselect_b32 s15, s17, s25
	s_cselect_b32 s55, s16, s24
	s_ashr_i32 s13, s12, 31
	s_lshl_b64 s[22:23], s[12:13], 20
	s_add_u32 s22, s6, s22
	s_addc_u32 s23, s7, s23
	s_and_b64 s[56:57], vcc, exec
	s_cselect_b32 s13, s23, s85
	s_cselect_b32 s56, s22, s84
	s_add_u32 s24, s24, 0x80080
	s_addc_u32 s25, s25, 0
	s_add_u32 s57, s84, 0x100
	v_mov_b32_e32 v2, 0
	s_addc_u32 s58, s85, 0
	s_mov_b32 s59, -2
	ds_read_b128 v[154:157], v150
	ds_read_b128 v[158:161], v150 offset:1024
	ds_read_b128 v[162:165], v150 offset:2048
	ds_read_b128 v[166:169], v150 offset:3072
	s_add_u32 s60, s24, 0xfff80080
	s_addc_u32 s61, s25, -1
	s_cmp_eq_u32 s59, 28
	s_cselect_b32 s87, s15, s61
	s_cselect_b32 s86, s55, s60
	s_cselect_b32 s85, s13, s58
	s_cselect_b32 s84, s56, s57
	v_lshl_add_u64 v[202:203], s[24:25], 0, v[138:139]
	s_add_i32 m0, s11, 0xc000
	ds_read_b128 v[170:173], v151
	ds_read_b128 v[174:177], v151 offset:1024
	ds_read_b128 v[178:181], v151 offset:2048
	ds_read_b128 v[182:185], v151 offset:3072
	ds_read_b128 v[186:189], v151 offset:4096
	ds_read_b128 v[190:193], v151 offset:5120
	ds_read_b128 v[194:197], v151 offset:6144
	ds_read_b128 v[198:201], v151 offset:7168
	global_load_lds_dwordx4 v[202:203], off
	v_lshl_add_u64 v[202:203], s[24:25], 0, v[140:141]
	s_add_i32 m0, s11, 0xe000
	s_nop 0
	global_load_lds_dwordx4 v[202:203], off
	s_waitcnt lgkmcnt(8)
	s_barrier
	s_waitcnt lgkmcnt(0)
	s_setprio 1
	s_waitcnt lgkmcnt(0)
	v_mfma_f32_16x16x32_bf16 v[126:129], v[154:157], v[170:173], 0
	v_mfma_f32_16x16x32_bf16 v[122:125], v[162:165], v[170:173], 0
	v_mfma_f32_16x16x32_bf16 v[118:121], v[154:157], v[178:181], 0
	v_mfma_f32_16x16x32_bf16 v[114:117], v[162:165], v[178:181], 0
	v_mfma_f32_16x16x32_bf16 v[102:105], v[154:157], v[186:189], 0
	v_mfma_f32_16x16x32_bf16 v[98:101], v[162:165], v[186:189], 0
	v_mfma_f32_16x16x32_bf16 v[86:89], v[154:157], v[194:197], 0
	v_mfma_f32_16x16x32_bf16 v[82:85], v[162:165], v[194:197], 0
	v_mfma_f32_16x16x32_bf16 v[126:129], v[158:161], v[174:177], v[126:129]
	v_mfma_f32_16x16x32_bf16 v[122:125], v[166:169], v[174:177], v[122:125]
	v_mfma_f32_16x16x32_bf16 v[118:121], v[158:161], v[182:185], v[118:121]
	v_mfma_f32_16x16x32_bf16 v[114:117], v[166:169], v[182:185], v[114:117]
	v_mfma_f32_16x16x32_bf16 v[102:105], v[158:161], v[190:193], v[102:105]
	v_mfma_f32_16x16x32_bf16 v[98:101], v[166:169], v[190:193], v[98:101]
	v_mfma_f32_16x16x32_bf16 v[86:89], v[158:161], v[198:201], v[86:89]
	v_mfma_f32_16x16x32_bf16 v[82:85], v[166:169], v[198:201], v[82:85]
	s_setprio 0
	s_barrier
	s_add_i32 s60, s41, s18
	v_lshl_add_u64 v[218:219], s[84:85], 0, v[134:135]
	s_mov_b32 m0, s60
	ds_read_b128 v[202:205], v152
	ds_read_b128 v[206:209], v152 offset:1024
	ds_read_b128 v[210:213], v152 offset:2048
	ds_read_b128 v[214:217], v152 offset:3072
	global_load_lds_dwordx4 v[218:219], off
	v_lshl_add_u64 v[220:221], s[84:85], 0, v[130:131]
	s_add_i32 m0, s60, 0x2000
	s_nop 0
	global_load_lds_dwordx4 v[220:221], off
	s_barrier
	s_waitcnt lgkmcnt(0)
	s_setprio 1
	s_waitcnt lgkmcnt(0)
	v_mfma_f32_16x16x32_bf16 v[110:113], v[202:205], v[170:173], 0
	v_mfma_f32_16x16x32_bf16 v[106:109], v[210:213], v[170:173], 0
	v_mfma_f32_16x16x32_bf16 v[94:97], v[202:205], v[178:181], 0
	v_mfma_f32_16x16x32_bf16 v[90:93], v[210:213], v[178:181], 0
	v_mfma_f32_16x16x32_bf16 v[78:81], v[202:205], v[186:189], 0
	v_mfma_f32_16x16x32_bf16 v[74:77], v[210:213], v[186:189], 0
	v_mfma_f32_16x16x32_bf16 v[70:73], v[202:205], v[194:197], 0
	v_mfma_f32_16x16x32_bf16 v[66:69], v[210:213], v[194:197], 0
	v_mfma_f32_16x16x32_bf16 v[110:113], v[206:209], v[174:177], v[110:113]
	v_mfma_f32_16x16x32_bf16 v[106:109], v[214:217], v[174:177], v[106:109]
	v_mfma_f32_16x16x32_bf16 v[94:97], v[206:209], v[182:185], v[94:97]
	v_mfma_f32_16x16x32_bf16 v[90:93], v[214:217], v[182:185], v[90:93]
	v_mfma_f32_16x16x32_bf16 v[78:81], v[206:209], v[190:193], v[78:81]
	v_mfma_f32_16x16x32_bf16 v[74:77], v[214:217], v[190:193], v[74:77]
	v_mfma_f32_16x16x32_bf16 v[70:73], v[206:209], v[198:201], v[70:73]
	v_mfma_f32_16x16x32_bf16 v[66:69], v[214:217], v[198:201], v[66:69]
	s_setprio 0
	s_mov_b32 m0, s11
	v_lshl_add_u64 v[222:223], s[86:87], 0, v[136:137]
	s_barrier
	ds_read_b128 v[170:173], v151 offset:16384
	ds_read_b128 v[174:177], v151 offset:17408
	ds_read_b128 v[178:181], v151 offset:18432
	ds_read_b128 v[182:185], v151 offset:19456
	ds_read_b128 v[186:189], v151 offset:20480
	ds_read_b128 v[190:193], v151 offset:21504
	ds_read_b128 v[194:197], v151 offset:22528
	ds_read_b128 v[198:201], v151 offset:23552
	global_load_lds_dwordx4 v[222:223], off
	v_lshl_add_u64 v[224:225], s[86:87], 0, v[132:133]
	s_mov_b32 m0, s21
	s_nop 0
	global_load_lds_dwordx4 v[224:225], off
	s_barrier
	s_waitcnt lgkmcnt(0)
	s_setprio 1
	s_waitcnt lgkmcnt(0)
	v_mfma_f32_16x16x32_bf16 v[62:65], v[154:157], v[170:173], 0
	v_mfma_f32_16x16x32_bf16 v[58:61], v[162:165], v[170:173], 0
	v_mfma_f32_16x16x32_bf16 v[54:57], v[154:157], v[178:181], 0
	v_mfma_f32_16x16x32_bf16 v[50:53], v[162:165], v[178:181], 0
	v_mfma_f32_16x16x32_bf16 v[38:41], v[154:157], v[186:189], 0
	v_mfma_f32_16x16x32_bf16 v[34:37], v[162:165], v[186:189], 0
	v_mfma_f32_16x16x32_bf16 v[22:25], v[154:157], v[194:197], 0
	v_mfma_f32_16x16x32_bf16 v[18:21], v[162:165], v[194:197], 0
	v_mfma_f32_16x16x32_bf16 v[62:65], v[158:161], v[174:177], v[62:65]
	v_mfma_f32_16x16x32_bf16 v[58:61], v[166:169], v[174:177], v[58:61]
	v_mfma_f32_16x16x32_bf16 v[54:57], v[158:161], v[182:185], v[54:57]
	v_mfma_f32_16x16x32_bf16 v[50:53], v[166:169], v[182:185], v[50:53]
	v_mfma_f32_16x16x32_bf16 v[38:41], v[158:161], v[190:193], v[38:41]
	v_mfma_f32_16x16x32_bf16 v[34:37], v[166:169], v[190:193], v[34:37]
	v_mfma_f32_16x16x32_bf16 v[22:25], v[158:161], v[198:201], v[22:25]
	v_mfma_f32_16x16x32_bf16 v[18:21], v[166:169], v[198:201], v[18:21]
	s_setprio 0
	s_barrier
	s_add_u32 s60, s84, 0x80000
	s_addc_u32 s61, s85, 0
	s_add_i32 s62, s52, s18
	v_lshl_add_u64 v[154:155], s[60:61], 0, v[134:135]
	s_mov_b32 m0, s62
	s_nop 0
	global_load_lds_dwordx4 v[154:155], off
	v_lshl_add_u64 v[154:155], s[60:61], 0, v[130:131]
	s_add_i32 m0, s62, 0x2000
	s_nop 0
	global_load_lds_dwordx4 v[154:155], off
	s_waitcnt vmcnt(6)
	s_barrier
	s_setprio 1
	v_mfma_f32_16x16x32_bf16 v[46:49], v[202:205], v[170:173], 0
	v_mfma_f32_16x16x32_bf16 v[42:45], v[210:213], v[170:173], 0
	v_mfma_f32_16x16x32_bf16 v[30:33], v[202:205], v[178:181], 0
	v_mfma_f32_16x16x32_bf16 v[26:29], v[210:213], v[178:181], 0
	v_mfma_f32_16x16x32_bf16 v[14:17], v[202:205], v[186:189], 0
	v_mfma_f32_16x16x32_bf16 v[10:13], v[210:213], v[186:189], 0
	v_mfma_f32_16x16x32_bf16 v[6:9], v[202:205], v[194:197], 0
	v_mfma_f32_16x16x32_bf16 v[2:5], v[210:213], v[194:197], 0
	v_mfma_f32_16x16x32_bf16 v[46:49], v[206:209], v[174:177], v[46:49]
	v_mfma_f32_16x16x32_bf16 v[42:45], v[214:217], v[174:177], v[42:45]
	v_mfma_f32_16x16x32_bf16 v[30:33], v[206:209], v[182:185], v[30:33]
	v_mfma_f32_16x16x32_bf16 v[26:29], v[214:217], v[182:185], v[26:29]
	v_mfma_f32_16x16x32_bf16 v[14:17], v[206:209], v[190:193], v[14:17]
	v_mfma_f32_16x16x32_bf16 v[10:13], v[214:217], v[190:193], v[10:13]
	v_mfma_f32_16x16x32_bf16 v[6:9], v[206:209], v[198:201], v[6:9]
	v_mfma_f32_16x16x32_bf16 v[2:5], v[214:217], v[198:201], v[2:5]
	s_setprio 0
	s_add_i32 s62, 0, 0x18000
	v_add_u32_e32 v1, s62, v148
	s_barrier
	ds_read_b128 v[154:157], v1
	ds_read_b128 v[158:161], v1 offset:1024
	ds_read_b128 v[162:165], v1 offset:2048
	ds_read_b128 v[166:169], v1 offset:3072
	s_add_u32 s60, s86, 0x80000
	s_addc_u32 s61, s87, 0
	s_mov_b32 m0, s26
	v_lshl_add_u64 v[202:203], s[60:61], 0, v[136:137]
	ds_read_b128 v[170:173], v151 offset:32768
	ds_read_b128 v[174:177], v151 offset:33792
	ds_read_b128 v[178:181], v151 offset:34816
	ds_read_b128 v[182:185], v151 offset:35840
	ds_read_b128 v[186:189], v151 offset:36864
	ds_read_b128 v[190:193], v151 offset:37888
	ds_read_b128 v[194:197], v151 offset:38912
	ds_read_b128 v[198:201], v151 offset:39936
	global_load_lds_dwordx4 v[202:203], off
	v_lshl_add_u64 v[202:203], s[60:61], 0, v[132:133]
	s_mov_b32 m0, s27
	s_nop 0
	global_load_lds_dwordx4 v[202:203], off
	s_waitcnt lgkmcnt(8)
	s_barrier
	s_waitcnt lgkmcnt(0)
	s_setprio 1
	s_waitcnt lgkmcnt(0)
	v_mfma_f32_16x16x32_bf16 v[126:129], v[154:157], v[170:173], v[126:129]
	v_mfma_f32_16x16x32_bf16 v[122:125], v[162:165], v[170:173], v[122:125]
	v_mfma_f32_16x16x32_bf16 v[118:121], v[154:157], v[178:181], v[118:121]
	v_mfma_f32_16x16x32_bf16 v[114:117], v[162:165], v[178:181], v[114:117]
	v_mfma_f32_16x16x32_bf16 v[102:105], v[154:157], v[186:189], v[102:105]
	v_mfma_f32_16x16x32_bf16 v[98:101], v[162:165], v[186:189], v[98:101]
	v_mfma_f32_16x16x32_bf16 v[86:89], v[154:157], v[194:197], v[86:89]
	v_mfma_f32_16x16x32_bf16 v[82:85], v[162:165], v[194:197], v[82:85]
	v_mfma_f32_16x16x32_bf16 v[126:129], v[158:161], v[174:177], v[126:129]
	v_mfma_f32_16x16x32_bf16 v[122:125], v[166:169], v[174:177], v[122:125]
	v_mfma_f32_16x16x32_bf16 v[118:121], v[158:161], v[182:185], v[118:121]
	v_mfma_f32_16x16x32_bf16 v[114:117], v[166:169], v[182:185], v[114:117]
	v_mfma_f32_16x16x32_bf16 v[102:105], v[158:161], v[190:193], v[102:105]
	v_mfma_f32_16x16x32_bf16 v[98:101], v[166:169], v[190:193], v[98:101]
	v_mfma_f32_16x16x32_bf16 v[86:89], v[158:161], v[198:201], v[86:89]
	v_mfma_f32_16x16x32_bf16 v[82:85], v[166:169], v[198:201], v[82:85]
	s_setprio 0
	s_barrier
	s_add_i32 s63, 0, 0x1c000
	s_add_i32 s60, s62, s18
	v_add_u32_e32 v1, s63, v148
	v_lshl_add_u64 v[218:219], v[218:219], 0, s[8:9]
	s_mov_b32 m0, s60
	ds_read_b128 v[202:205], v1
	ds_read_b128 v[206:209], v1 offset:1024
	ds_read_b128 v[210:213], v1 offset:2048
	ds_read_b128 v[214:217], v1 offset:3072
	global_load_lds_dwordx4 v[218:219], off
	v_lshl_add_u64 v[218:219], v[220:221], 0, s[8:9]
	s_add_i32 m0, s60, 0x2000
	s_nop 0
	global_load_lds_dwordx4 v[218:219], off
	s_barrier
	s_waitcnt lgkmcnt(0)
	s_setprio 1
	s_waitcnt lgkmcnt(0)
	v_mfma_f32_16x16x32_bf16 v[110:113], v[202:205], v[170:173], v[110:113]
	v_mfma_f32_16x16x32_bf16 v[106:109], v[210:213], v[170:173], v[106:109]
	v_mfma_f32_16x16x32_bf16 v[94:97], v[202:205], v[178:181], v[94:97]
	v_mfma_f32_16x16x32_bf16 v[90:93], v[210:213], v[178:181], v[90:93]
	v_mfma_f32_16x16x32_bf16 v[78:81], v[202:205], v[186:189], v[78:81]
	v_mfma_f32_16x16x32_bf16 v[74:77], v[210:213], v[186:189], v[74:77]
	v_mfma_f32_16x16x32_bf16 v[70:73], v[202:205], v[194:197], v[70:73]
	v_mfma_f32_16x16x32_bf16 v[66:69], v[210:213], v[194:197], v[66:69]
	v_mfma_f32_16x16x32_bf16 v[110:113], v[206:209], v[174:177], v[110:113]
	v_mfma_f32_16x16x32_bf16 v[106:109], v[214:217], v[174:177], v[106:109]
	v_mfma_f32_16x16x32_bf16 v[94:97], v[206:209], v[182:185], v[94:97]
	v_mfma_f32_16x16x32_bf16 v[90:93], v[214:217], v[182:185], v[90:93]
	v_mfma_f32_16x16x32_bf16 v[78:81], v[206:209], v[190:193], v[78:81]
	v_mfma_f32_16x16x32_bf16 v[74:77], v[214:217], v[190:193], v[74:77]
	v_mfma_f32_16x16x32_bf16 v[70:73], v[206:209], v[198:201], v[70:73]
	v_mfma_f32_16x16x32_bf16 v[66:69], v[214:217], v[198:201], v[66:69]
	s_setprio 0
	s_mov_b32 m0, s34
	v_lshl_add_u64 v[218:219], v[222:223], 0, s[8:9]
	s_barrier
	ds_read_b128 v[170:173], v151 offset:49152
	ds_read_b128 v[174:177], v151 offset:50176
	ds_read_b128 v[178:181], v151 offset:51200
	ds_read_b128 v[182:185], v151 offset:52224
	ds_read_b128 v[186:189], v151 offset:53248
	ds_read_b128 v[190:193], v151 offset:54272
	ds_read_b128 v[194:197], v151 offset:55296
	ds_read_b128 v[198:201], v151 offset:56320
	global_load_lds_dwordx4 v[218:219], off
	v_lshl_add_u64 v[218:219], v[224:225], 0, s[8:9]
	s_mov_b32 m0, s35
	s_nop 0
	global_load_lds_dwordx4 v[218:219], off
	s_barrier
	s_waitcnt lgkmcnt(0)
	s_setprio 1
	s_waitcnt lgkmcnt(0)
	v_mfma_f32_16x16x32_bf16 v[62:65], v[154:157], v[170:173], v[62:65]
	v_mfma_f32_16x16x32_bf16 v[58:61], v[162:165], v[170:173], v[58:61]
	v_mfma_f32_16x16x32_bf16 v[54:57], v[154:157], v[178:181], v[54:57]
	v_mfma_f32_16x16x32_bf16 v[50:53], v[162:165], v[178:181], v[50:53]
	v_mfma_f32_16x16x32_bf16 v[38:41], v[154:157], v[186:189], v[38:41]
	v_mfma_f32_16x16x32_bf16 v[34:37], v[162:165], v[186:189], v[34:37]
	v_mfma_f32_16x16x32_bf16 v[22:25], v[154:157], v[194:197], v[22:25]
	v_mfma_f32_16x16x32_bf16 v[18:21], v[162:165], v[194:197], v[18:21]
	v_mfma_f32_16x16x32_bf16 v[62:65], v[158:161], v[174:177], v[62:65]
	v_mfma_f32_16x16x32_bf16 v[58:61], v[166:169], v[174:177], v[58:61]
	v_mfma_f32_16x16x32_bf16 v[54:57], v[158:161], v[182:185], v[54:57]
	v_mfma_f32_16x16x32_bf16 v[50:53], v[166:169], v[182:185], v[50:53]
	v_mfma_f32_16x16x32_bf16 v[38:41], v[158:161], v[190:193], v[38:41]
	v_mfma_f32_16x16x32_bf16 v[34:37], v[166:169], v[190:193], v[34:37]
	v_mfma_f32_16x16x32_bf16 v[22:25], v[158:161], v[198:201], v[22:25]
	v_mfma_f32_16x16x32_bf16 v[18:21], v[166:169], v[198:201], v[18:21]
	s_setprio 0
	s_barrier
	s_add_u32 s60, s84, 0x80080
	s_addc_u32 s61, s85, 0
	s_add_i32 s62, s63, s18
	v_lshl_add_u64 v[154:155], s[60:61], 0, v[134:135]
	s_mov_b32 m0, s62
	s_nop 0
	global_load_lds_dwordx4 v[154:155], off
	v_lshl_add_u64 v[154:155], s[60:61], 0, v[130:131]
	s_add_i32 m0, s62, 0x2000
	s_nop 0
	global_load_lds_dwordx4 v[154:155], off
	s_waitcnt vmcnt(6)
	s_barrier
	s_setprio 1
	v_mfma_f32_16x16x32_bf16 v[46:49], v[202:205], v[170:173], v[46:49]
	v_mfma_f32_16x16x32_bf16 v[42:45], v[210:213], v[170:173], v[42:45]
	v_mfma_f32_16x16x32_bf16 v[30:33], v[202:205], v[178:181], v[30:33]
	v_mfma_f32_16x16x32_bf16 v[26:29], v[210:213], v[178:181], v[26:29]
	v_mfma_f32_16x16x32_bf16 v[14:17], v[202:205], v[186:189], v[14:17]
	v_mfma_f32_16x16x32_bf16 v[10:13], v[210:213], v[186:189], v[10:13]
	v_mfma_f32_16x16x32_bf16 v[6:9], v[202:205], v[194:197], v[6:9]
	v_mfma_f32_16x16x32_bf16 v[2:5], v[210:213], v[194:197], v[2:5]
	v_mfma_f32_16x16x32_bf16 v[46:49], v[206:209], v[174:177], v[46:49]
	v_mfma_f32_16x16x32_bf16 v[42:45], v[214:217], v[174:177], v[42:45]
	v_mfma_f32_16x16x32_bf16 v[30:33], v[206:209], v[182:185], v[30:33]
	v_mfma_f32_16x16x32_bf16 v[26:29], v[214:217], v[182:185], v[26:29]
	v_mfma_f32_16x16x32_bf16 v[14:17], v[206:209], v[190:193], v[14:17]
	v_mfma_f32_16x16x32_bf16 v[10:13], v[214:217], v[190:193], v[10:13]
	v_mfma_f32_16x16x32_bf16 v[6:9], v[206:209], v[198:201], v[6:9]
	v_mfma_f32_16x16x32_bf16 v[2:5], v[214:217], v[198:201], v[2:5]
	s_setprio 0
	s_add_i32 s59, s59, 2
	s_add_u32 s24, s24, 0x100
	s_addc_u32 s25, s25, 0
	s_add_u32 s57, s57, 0x100
	s_addc_u32 s58, s58, 0
	s_cmp_gt_u32 s59, 29
	s_barrier
	s_cbranch_scc1 .Lpeel_85_after

.Lpeel_85_after:
	v_lshl_add_u32 v1, s10, 8, v147
	v_lshl_or_b32 v154, s54, 8, v149
	v_ashrrev_i32_e32 v155, 31, v154
	v_mov_b64_e32 v[156:157], s[96:97]
	v_cvt_pk_bf16_f32 v70, v70, v71
	v_cvt_pk_bf16_f32 v71, v72, v73
	v_cvt_pk_bf16_f32 v72, v66, v67
	v_add_u32_e32 v66, 0x80, v1
	v_mad_i64_i32 v[158:159], s[24:25], v1, s53, v[156:157]
	v_lshlrev_b64 v[154:155], 1, v[154:155]
	v_cvt_pk_bf16_f32 v110, v110, v111
	v_cvt_pk_bf16_f32 v111, v112, v113
	v_cvt_pk_bf16_f32 v112, v106, v107
	v_or_b32_e32 v106, 16, v1
	v_mad_i64_i32 v[66:67], s[24:25], v66, s53, v[156:157]
	v_cvt_pk_bf16_f32 v46, v46, v47
	v_cvt_pk_bf16_f32 v47, v48, v49
	v_cvt_pk_bf16_f32 v48, v42, v43
	v_add_u32_e32 v42, 0x90, v1
	v_lshl_add_u64 v[158:159], v[158:159], 0, v[154:155]
	v_cvt_pk_bf16_f32 v113, v108, v109
	v_mad_i64_i32 v[106:107], s[24:25], v106, s53, v[156:157]
	v_cvt_pk_bf16_f32 v94, v94, v95
	v_cvt_pk_bf16_f32 v95, v96, v97
	v_cvt_pk_bf16_f32 v96, v90, v91
	v_or_b32_e32 v90, 32, v1
	v_lshl_add_u64 v[66:67], v[66:67], 0, v[154:155]
	v_cvt_pk_bf16_f32 v49, v44, v45
	v_mad_i64_i32 v[42:43], s[24:25], v42, s53, v[156:157]
	v_cvt_pk_bf16_f32 v30, v30, v31
	v_cvt_pk_bf16_f32 v31, v32, v33
	v_cvt_pk_bf16_f32 v32, v26, v27
	v_add_u32_e32 v26, 0xa0, v1
	global_store_dwordx4 v[158:159], v[110:113], off offset:256
	v_cvt_pk_bf16_f32 v97, v92, v93
	v_mad_i64_i32 v[90:91], s[24:25], v90, s53, v[156:157]
	v_lshl_add_u64 v[110:111], v[106:107], 0, v[154:155]
	v_cvt_pk_bf16_f32 v78, v78, v79
	v_cvt_pk_bf16_f32 v79, v80, v81
	v_cvt_pk_bf16_f32 v80, v74, v75
	v_or_b32_e32 v74, 48, v1
	global_store_dwordx4 v[66:67], v[46:49], off offset:256
	v_cvt_pk_bf16_f32 v33, v28, v29
	v_mad_i64_i32 v[26:27], s[24:25], v26, s53, v[156:157]
	v_lshl_add_u64 v[46:47], v[42:43], 0, v[154:155]
	v_add_u32_e32 v1, 0xb0, v1
	global_store_dwordx4 v[110:111], v[94:97], off offset:256
	v_cvt_pk_bf16_f32 v81, v76, v77
	v_mad_i64_i32 v[74:75], s[24:25], v74, s53, v[156:157]
	v_lshl_add_u64 v[94:95], v[90:91], 0, v[154:155]
	global_store_dwordx4 v[46:47], v[30:33], off offset:256
	v_cvt_pk_bf16_f32 v14, v14, v15
	v_cvt_pk_bf16_f32 v15, v16, v17
	v_lshl_add_u64 v[30:31], v[26:27], 0, v[154:155]
	v_cvt_pk_bf16_f32 v16, v10, v11
	v_cvt_pk_bf16_f32 v17, v12, v13
	v_mad_i64_i32 v[10:11], s[24:25], v1, s53, v[156:157]
	v_cvt_pk_bf16_f32 v126, v126, v127
	v_cvt_pk_bf16_f32 v127, v128, v129
	v_cvt_pk_bf16_f32 v128, v122, v123
	v_cvt_pk_bf16_f32 v129, v124, v125
	v_cvt_pk_bf16_f32 v106, v118, v119
	v_cvt_pk_bf16_f32 v107, v120, v121
	v_cvt_pk_bf16_f32 v108, v114, v115
	v_cvt_pk_bf16_f32 v109, v116, v117
	v_cvt_pk_bf16_f32 v90, v102, v103
	v_cvt_pk_bf16_f32 v91, v104, v105
	v_cvt_pk_bf16_f32 v92, v98, v99
	v_cvt_pk_bf16_f32 v93, v100, v101
	global_store_dwordx4 v[94:95], v[78:81], off offset:256
	v_cvt_pk_bf16_f32 v76, v82, v83
	v_cvt_pk_bf16_f32 v77, v84, v85
	v_lshl_add_u64 v[78:79], v[74:75], 0, v[154:155]
	v_cvt_pk_bf16_f32 v74, v86, v87
	v_cvt_pk_bf16_f32 v75, v88, v89
	v_cvt_pk_bf16_f32 v73, v68, v69
	v_cvt_pk_bf16_f32 v62, v62, v63
	v_cvt_pk_bf16_f32 v63, v64, v65
	v_cvt_pk_bf16_f32 v64, v58, v59
	v_cvt_pk_bf16_f32 v65, v60, v61
	v_cvt_pk_bf16_f32 v42, v54, v55
	v_cvt_pk_bf16_f32 v43, v56, v57
	v_cvt_pk_bf16_f32 v44, v50, v51
	v_cvt_pk_bf16_f32 v45, v52, v53
	v_cvt_pk_bf16_f32 v26, v38, v39
	v_cvt_pk_bf16_f32 v27, v40, v41
	v_cvt_pk_bf16_f32 v28, v34, v35
	v_cvt_pk_bf16_f32 v29, v36, v37
	global_store_dwordx4 v[30:31], v[14:17], off offset:256
	v_cvt_pk_bf16_f32 v12, v18, v19
	v_cvt_pk_bf16_f32 v13, v20, v21
	v_lshl_add_u64 v[14:15], v[10:11], 0, v[154:155]
	v_cvt_pk_bf16_f32 v10, v22, v23
	v_cvt_pk_bf16_f32 v11, v24, v25
	v_cvt_pk_bf16_f32 v6, v6, v7
	v_cvt_pk_bf16_f32 v7, v8, v9
	v_cvt_pk_bf16_f32 v8, v2, v3
	v_cvt_pk_bf16_f32 v9, v4, v5
	s_and_b64 vcc, exec, s[0:1]
	s_mov_b32 s54, s12
	s_mov_b32 s10, s14
	s_mov_b64 s[84:85], s[22:23]
	s_mov_b64 s[24:25], s[16:17]
	v_readlane_b32 s93, v254, 9
	global_store_dwordx4 v[158:159], v[126:129], off
	global_store_dwordx4 v[110:111], v[106:109], off
	global_store_dwordx4 v[94:95], v[90:93], off
	global_store_dwordx4 v[78:79], v[74:77], off
	global_store_dwordx4 v[78:79], v[70:73], off offset:256
	global_store_dwordx4 v[66:67], v[62:65], off
	global_store_dwordx4 v[46:47], v[42:45], off
	global_store_dwordx4 v[30:31], v[26:29], off
	global_store_dwordx4 v[14:15], v[10:13], off
	global_store_dwordx4 v[14:15], v[6:9], off offset:256
	s_cbranch_vccz .LBB0_82
	s_waitcnt vmcnt(0)
	s_cmpk_gt_u32 s3, 0xff
	s_cbranch_scc1 .LBB0_89
	s_barrier

.LBB0_527:
	s_ashr_i32 s23, s22, 31
	v_cmp_lt_i64_e32 vcc, s[24:25], v[138:139]
	s_lshl_b64 s[24:25], s[22:23], 21
	v_readlane_b32 s17, v254, 38
	s_add_u32 s24, s17, s24
	s_addc_u32 s25, s66, s25
	s_and_b64 s[44:45], vcc, exec
	s_cselect_b32 s23, s25, s49
	s_cselect_b32 s56, s24, s48
	s_ashr_i32 s17, s16, 31
	s_lshl_b64 s[44:45], s[16:17], 21
	v_readlane_b32 s54, v254, 28
	v_readlane_b32 s55, v254, 29
	s_add_u32 s44, s54, s44
	s_addc_u32 s45, s55, s45
	s_and_b64 s[54:55], vcc, exec
	s_cselect_b32 s17, s45, s53
	s_cselect_b32 s57, s44, s52
	s_add_u32 s48, s48, 0x100080
	s_addc_u32 s49, s49, 0
	s_add_u32 s58, s52, 0x100
	v_mov_b32_e32 v2, 0
	s_addc_u32 s59, s53, 0
	s_mov_b32 s60, -2
	s_waitcnt vmcnt(0)
	ds_read_b128 v[142:145], v151
	ds_read_b128 v[154:157], v151 offset:1024
	ds_read_b128 v[158:161], v151 offset:2048
	ds_read_b128 v[162:165], v151 offset:3072
	s_add_u32 s52, s48, 0xfff00080
	s_addc_u32 s53, s49, -1
	s_cmp_eq_u32 s60, 60
	s_cselect_b32 s55, s23, s53
	s_cselect_b32 s54, s56, s52
	s_cselect_b32 s53, s17, s59
	s_cselect_b32 s52, s57, s58
	v_lshl_add_u64 v[146:147], s[48:49], 0, v[134:135]
	s_add_i32 m0, s19, 0xc000
	ds_read_b128 v[166:169], v152
	ds_read_b128 v[170:173], v152 offset:1024
	ds_read_b128 v[174:177], v152 offset:2048
	ds_read_b128 v[178:181], v152 offset:3072
	ds_read_b128 v[182:185], v152 offset:4096
	ds_read_b128 v[186:189], v152 offset:5120
	ds_read_b128 v[190:193], v152 offset:6144
	ds_read_b128 v[194:197], v152 offset:7168
	global_load_lds_dwordx4 v[146:147], off
	v_lshl_add_u64 v[146:147], s[48:49], 0, v[136:137]
	s_add_i32 m0, s19, 0xe000
	s_nop 0
	global_load_lds_dwordx4 v[146:147], off
	s_waitcnt lgkmcnt(8)
	s_barrier
	s_waitcnt lgkmcnt(0)
	s_setprio 1
	s_waitcnt lgkmcnt(0)
	v_mfma_f32_16x16x32_bf16 v[126:129], v[142:145], v[166:169], 0
	v_mfma_f32_16x16x32_bf16 v[122:125], v[158:161], v[166:169], 0
	v_mfma_f32_16x16x32_bf16 v[118:121], v[142:145], v[174:177], 0
	v_mfma_f32_16x16x32_bf16 v[114:117], v[158:161], v[174:177], 0
	v_mfma_f32_16x16x32_bf16 v[94:97], v[142:145], v[182:185], 0
	v_mfma_f32_16x16x32_bf16 v[90:93], v[158:161], v[182:185], 0
	v_mfma_f32_16x16x32_bf16 v[86:89], v[142:145], v[190:193], 0
	v_mfma_f32_16x16x32_bf16 v[82:85], v[158:161], v[190:193], 0
	v_mfma_f32_16x16x32_bf16 v[126:129], v[154:157], v[170:173], v[126:129]
	v_mfma_f32_16x16x32_bf16 v[122:125], v[162:165], v[170:173], v[122:125]
	v_mfma_f32_16x16x32_bf16 v[118:121], v[154:157], v[178:181], v[118:121]
	v_mfma_f32_16x16x32_bf16 v[114:117], v[162:165], v[178:181], v[114:117]
	v_mfma_f32_16x16x32_bf16 v[94:97], v[154:157], v[186:189], v[94:97]
	v_mfma_f32_16x16x32_bf16 v[90:93], v[162:165], v[186:189], v[90:93]
	v_mfma_f32_16x16x32_bf16 v[86:89], v[154:157], v[194:197], v[86:89]
	v_mfma_f32_16x16x32_bf16 v[82:85], v[162:165], v[194:197], v[82:85]
	s_setprio 0
	s_barrier
	s_add_i32 s61, s40, s18
	v_lshl_add_u64 v[146:147], s[52:53], 0, v[130:131]
	s_mov_b32 m0, s61
	ds_read_b128 v[198:201], v153
	ds_read_b128 v[202:205], v153 offset:1024
	ds_read_b128 v[206:209], v153 offset:2048
	ds_read_b128 v[210:213], v153 offset:3072
	global_load_lds_dwordx4 v[146:147], off
	v_lshl_add_u64 v[214:215], s[52:53], 0, v[132:133]
	s_add_i32 m0, s61, 0x2000
	s_nop 0
	global_load_lds_dwordx4 v[214:215], off
	s_barrier
	s_waitcnt lgkmcnt(0)
	s_setprio 1
	s_waitcnt lgkmcnt(0)
	v_mfma_f32_16x16x32_bf16 v[110:113], v[198:201], v[166:169], 0
	v_mfma_f32_16x16x32_bf16 v[106:109], v[206:209], v[166:169], 0
	v_mfma_f32_16x16x32_bf16 v[102:105], v[198:201], v[174:177], 0
	v_mfma_f32_16x16x32_bf16 v[98:101], v[206:209], v[174:177], 0
	v_mfma_f32_16x16x32_bf16 v[78:81], v[198:201], v[182:185], 0
	v_mfma_f32_16x16x32_bf16 v[74:77], v[206:209], v[182:185], 0
	v_mfma_f32_16x16x32_bf16 v[70:73], v[198:201], v[190:193], 0
	v_mfma_f32_16x16x32_bf16 v[66:69], v[206:209], v[190:193], 0
	v_mfma_f32_16x16x32_bf16 v[110:113], v[202:205], v[170:173], v[110:113]
	v_mfma_f32_16x16x32_bf16 v[106:109], v[210:213], v[170:173], v[106:109]
	v_mfma_f32_16x16x32_bf16 v[102:105], v[202:205], v[178:181], v[102:105]
	v_mfma_f32_16x16x32_bf16 v[98:101], v[210:213], v[178:181], v[98:101]
	v_mfma_f32_16x16x32_bf16 v[78:81], v[202:205], v[186:189], v[78:81]
	v_mfma_f32_16x16x32_bf16 v[74:77], v[210:213], v[186:189], v[74:77]
	v_mfma_f32_16x16x32_bf16 v[70:73], v[202:205], v[194:197], v[70:73]
	v_mfma_f32_16x16x32_bf16 v[66:69], v[210:213], v[194:197], v[66:69]
	s_setprio 0
	s_mov_b32 m0, s19
	v_lshl_add_u64 v[216:217], s[54:55], 0, v[130:131]
	s_barrier
	ds_read_b128 v[166:169], v152 offset:16384
	ds_read_b128 v[170:173], v152 offset:17408
	ds_read_b128 v[174:177], v152 offset:18432
	ds_read_b128 v[178:181], v152 offset:19456
	ds_read_b128 v[182:185], v152 offset:20480
	ds_read_b128 v[186:189], v152 offset:21504
	ds_read_b128 v[190:193], v152 offset:22528
	ds_read_b128 v[194:197], v152 offset:23552
	global_load_lds_dwordx4 v[216:217], off
	v_lshl_add_u64 v[218:219], s[54:55], 0, v[132:133]
	s_mov_b32 m0, s20
	s_nop 0
	global_load_lds_dwordx4 v[218:219], off
	s_barrier
	s_waitcnt lgkmcnt(0)
	s_setprio 1
	s_waitcnt lgkmcnt(0)
	v_mfma_f32_16x16x32_bf16 v[62:65], v[142:145], v[166:169], 0
	v_mfma_f32_16x16x32_bf16 v[58:61], v[158:161], v[166:169], 0
	v_mfma_f32_16x16x32_bf16 v[54:57], v[142:145], v[174:177], 0
	v_mfma_f32_16x16x32_bf16 v[50:53], v[158:161], v[174:177], 0
	v_mfma_f32_16x16x32_bf16 v[30:33], v[142:145], v[182:185], 0
	v_mfma_f32_16x16x32_bf16 v[26:29], v[158:161], v[182:185], 0
	v_mfma_f32_16x16x32_bf16 v[22:25], v[142:145], v[190:193], 0
	v_mfma_f32_16x16x32_bf16 v[18:21], v[158:161], v[190:193], 0
	v_mfma_f32_16x16x32_bf16 v[62:65], v[154:157], v[170:173], v[62:65]
	v_mfma_f32_16x16x32_bf16 v[58:61], v[162:165], v[170:173], v[58:61]
	v_mfma_f32_16x16x32_bf16 v[54:57], v[154:157], v[178:181], v[54:57]
	v_mfma_f32_16x16x32_bf16 v[50:53], v[162:165], v[178:181], v[50:53]
	v_mfma_f32_16x16x32_bf16 v[30:33], v[154:157], v[186:189], v[30:33]
	v_mfma_f32_16x16x32_bf16 v[26:29], v[162:165], v[186:189], v[26:29]
	v_mfma_f32_16x16x32_bf16 v[22:25], v[154:157], v[194:197], v[22:25]
	v_mfma_f32_16x16x32_bf16 v[18:21], v[162:165], v[194:197], v[18:21]
	s_setprio 0
	s_barrier
	s_add_u32 s62, s52, 0x100000
	s_addc_u32 s63, s53, 0
	s_add_i32 s61, s41, s18
	v_lshl_add_u64 v[142:143], s[62:63], 0, v[130:131]
	s_mov_b32 m0, s61
	s_nop 0
	global_load_lds_dwordx4 v[142:143], off
	v_lshl_add_u64 v[142:143], s[62:63], 0, v[132:133]
	s_add_i32 m0, s61, 0x2000
	s_nop 0
	global_load_lds_dwordx4 v[142:143], off
	s_waitcnt vmcnt(6)
	s_barrier
	s_setprio 1
	v_mfma_f32_16x16x32_bf16 v[46:49], v[198:201], v[166:169], 0
	v_mfma_f32_16x16x32_bf16 v[42:45], v[206:209], v[166:169], 0
	v_mfma_f32_16x16x32_bf16 v[38:41], v[198:201], v[174:177], 0
	v_mfma_f32_16x16x32_bf16 v[34:37], v[206:209], v[174:177], 0
	v_mfma_f32_16x16x32_bf16 v[14:17], v[198:201], v[182:185], 0
	v_mfma_f32_16x16x32_bf16 v[10:13], v[206:209], v[182:185], 0
	v_mfma_f32_16x16x32_bf16 v[6:9], v[198:201], v[190:193], 0
	v_mfma_f32_16x16x32_bf16 v[2:5], v[206:209], v[190:193], 0
	v_mfma_f32_16x16x32_bf16 v[46:49], v[202:205], v[170:173], v[46:49]
	v_mfma_f32_16x16x32_bf16 v[42:45], v[210:213], v[170:173], v[42:45]
	v_mfma_f32_16x16x32_bf16 v[38:41], v[202:205], v[178:181], v[38:41]
	v_mfma_f32_16x16x32_bf16 v[34:37], v[210:213], v[178:181], v[34:37]
	v_mfma_f32_16x16x32_bf16 v[14:17], v[202:205], v[186:189], v[14:17]
	v_mfma_f32_16x16x32_bf16 v[10:13], v[210:213], v[186:189], v[10:13]
	v_mfma_f32_16x16x32_bf16 v[6:9], v[202:205], v[194:197], v[6:9]
	v_mfma_f32_16x16x32_bf16 v[2:5], v[210:213], v[194:197], v[2:5]
	s_setprio 0
	s_add_i32 s61, 0, 0x18000
	v_add_u32_e32 v1, s61, v149
	s_barrier
	ds_read_b128 v[142:145], v1
	ds_read_b128 v[154:157], v1 offset:1024
	ds_read_b128 v[158:161], v1 offset:2048
	ds_read_b128 v[162:165], v1 offset:3072
	s_add_u32 s54, s54, 0x100000
	s_addc_u32 s55, s55, 0
	s_mov_b32 m0, s21
	v_lshl_add_u64 v[198:199], s[54:55], 0, v[130:131]
	ds_read_b128 v[166:169], v152 offset:32768
	ds_read_b128 v[170:173], v152 offset:33792
	ds_read_b128 v[174:177], v152 offset:34816
	ds_read_b128 v[178:181], v152 offset:35840
	ds_read_b128 v[182:185], v152 offset:36864
	ds_read_b128 v[186:189], v152 offset:37888
	ds_read_b128 v[190:193], v152 offset:38912
	ds_read_b128 v[194:197], v152 offset:39936
	global_load_lds_dwordx4 v[198:199], off
	v_lshl_add_u64 v[198:199], s[54:55], 0, v[132:133]
	s_mov_b32 m0, s26
	s_nop 0
	global_load_lds_dwordx4 v[198:199], off
	s_waitcnt lgkmcnt(8)
	s_barrier
	s_waitcnt lgkmcnt(0)
	s_setprio 1
	s_waitcnt lgkmcnt(0)
	v_mfma_f32_16x16x32_bf16 v[126:129], v[142:145], v[166:169], v[126:129]
	v_mfma_f32_16x16x32_bf16 v[122:125], v[158:161], v[166:169], v[122:125]
	v_mfma_f32_16x16x32_bf16 v[118:121], v[142:145], v[174:177], v[118:121]
	v_mfma_f32_16x16x32_bf16 v[114:117], v[158:161], v[174:177], v[114:117]
	v_mfma_f32_16x16x32_bf16 v[94:97], v[142:145], v[182:185], v[94:97]
	v_mfma_f32_16x16x32_bf16 v[90:93], v[158:161], v[182:185], v[90:93]
	v_mfma_f32_16x16x32_bf16 v[86:89], v[142:145], v[190:193], v[86:89]
	v_mfma_f32_16x16x32_bf16 v[82:85], v[158:161], v[190:193], v[82:85]
	v_mfma_f32_16x16x32_bf16 v[126:129], v[154:157], v[170:173], v[126:129]
	v_mfma_f32_16x16x32_bf16 v[122:125], v[162:165], v[170:173], v[122:125]
	v_mfma_f32_16x16x32_bf16 v[118:121], v[154:157], v[178:181], v[118:121]
	v_mfma_f32_16x16x32_bf16 v[114:117], v[162:165], v[178:181], v[114:117]
	v_mfma_f32_16x16x32_bf16 v[94:97], v[154:157], v[186:189], v[94:97]
	v_mfma_f32_16x16x32_bf16 v[90:93], v[162:165], v[186:189], v[90:93]
	v_mfma_f32_16x16x32_bf16 v[86:89], v[154:157], v[194:197], v[86:89]
	v_mfma_f32_16x16x32_bf16 v[82:85], v[162:165], v[194:197], v[82:85]
	s_setprio 0
	s_barrier
	s_add_i32 s54, 0, 0x1c000
	s_add_i32 s55, s61, s18
	v_add_u32_e32 v1, s54, v149
	v_lshl_add_u64 v[146:147], v[146:147], 0, s[8:9]
	s_mov_b32 m0, s55
	ds_read_b128 v[198:201], v1
	ds_read_b128 v[202:205], v1 offset:1024
	ds_read_b128 v[206:209], v1 offset:2048
	ds_read_b128 v[210:213], v1 offset:3072
	global_load_lds_dwordx4 v[146:147], off
	v_lshl_add_u64 v[146:147], v[214:215], 0, s[8:9]
	s_add_i32 m0, s55, 0x2000
	s_nop 0
	global_load_lds_dwordx4 v[146:147], off
	s_barrier
	s_waitcnt lgkmcnt(0)
	s_setprio 1
	s_waitcnt lgkmcnt(0)
	v_mfma_f32_16x16x32_bf16 v[110:113], v[198:201], v[166:169], v[110:113]
	v_mfma_f32_16x16x32_bf16 v[106:109], v[206:209], v[166:169], v[106:109]
	v_mfma_f32_16x16x32_bf16 v[102:105], v[198:201], v[174:177], v[102:105]
	v_mfma_f32_16x16x32_bf16 v[98:101], v[206:209], v[174:177], v[98:101]
	v_mfma_f32_16x16x32_bf16 v[78:81], v[198:201], v[182:185], v[78:81]
	v_mfma_f32_16x16x32_bf16 v[74:77], v[206:209], v[182:185], v[74:77]
	v_mfma_f32_16x16x32_bf16 v[70:73], v[198:201], v[190:193], v[70:73]
	v_mfma_f32_16x16x32_bf16 v[66:69], v[206:209], v[190:193], v[66:69]
	v_mfma_f32_16x16x32_bf16 v[110:113], v[202:205], v[170:173], v[110:113]
	v_mfma_f32_16x16x32_bf16 v[106:109], v[210:213], v[170:173], v[106:109]
	v_mfma_f32_16x16x32_bf16 v[102:105], v[202:205], v[178:181], v[102:105]
	v_mfma_f32_16x16x32_bf16 v[98:101], v[210:213], v[178:181], v[98:101]
	v_mfma_f32_16x16x32_bf16 v[78:81], v[202:205], v[186:189], v[78:81]
	v_mfma_f32_16x16x32_bf16 v[74:77], v[210:213], v[186:189], v[74:77]
	v_mfma_f32_16x16x32_bf16 v[70:73], v[202:205], v[194:197], v[70:73]
	v_mfma_f32_16x16x32_bf16 v[66:69], v[210:213], v[194:197], v[66:69]
	s_setprio 0
	s_mov_b32 m0, s33
	v_lshl_add_u64 v[146:147], v[216:217], 0, s[8:9]
	s_barrier
	ds_read_b128 v[166:169], v152 offset:49152
	ds_read_b128 v[170:173], v152 offset:50176
	ds_read_b128 v[174:177], v152 offset:51200
	ds_read_b128 v[178:181], v152 offset:52224
	ds_read_b128 v[182:185], v152 offset:53248
	ds_read_b128 v[186:189], v152 offset:54272
	ds_read_b128 v[190:193], v152 offset:55296
	ds_read_b128 v[194:197], v152 offset:56320
	global_load_lds_dwordx4 v[146:147], off
	v_lshl_add_u64 v[146:147], v[218:219], 0, s[8:9]
	s_mov_b32 m0, s34
	s_nop 0
	global_load_lds_dwordx4 v[146:147], off
	s_barrier
	s_waitcnt lgkmcnt(0)
	s_setprio 1
	s_waitcnt lgkmcnt(0)
	v_mfma_f32_16x16x32_bf16 v[62:65], v[142:145], v[166:169], v[62:65]
	v_mfma_f32_16x16x32_bf16 v[58:61], v[158:161], v[166:169], v[58:61]
	v_mfma_f32_16x16x32_bf16 v[54:57], v[142:145], v[174:177], v[54:57]
	v_mfma_f32_16x16x32_bf16 v[50:53], v[158:161], v[174:177], v[50:53]
	v_mfma_f32_16x16x32_bf16 v[30:33], v[142:145], v[182:185], v[30:33]
	v_mfma_f32_16x16x32_bf16 v[26:29], v[158:161], v[182:185], v[26:29]
	v_mfma_f32_16x16x32_bf16 v[22:25], v[142:145], v[190:193], v[22:25]
	v_mfma_f32_16x16x32_bf16 v[18:21], v[158:161], v[190:193], v[18:21]
	v_mfma_f32_16x16x32_bf16 v[62:65], v[154:157], v[170:173], v[62:65]
	v_mfma_f32_16x16x32_bf16 v[58:61], v[162:165], v[170:173], v[58:61]
	v_mfma_f32_16x16x32_bf16 v[54:57], v[154:157], v[178:181], v[54:57]
	v_mfma_f32_16x16x32_bf16 v[50:53], v[162:165], v[178:181], v[50:53]
	v_mfma_f32_16x16x32_bf16 v[30:33], v[154:157], v[186:189], v[30:33]
	v_mfma_f32_16x16x32_bf16 v[26:29], v[162:165], v[186:189], v[26:29]
	v_mfma_f32_16x16x32_bf16 v[22:25], v[154:157], v[194:197], v[22:25]
	v_mfma_f32_16x16x32_bf16 v[18:21], v[162:165], v[194:197], v[18:21]
	s_setprio 0
	s_barrier
	s_add_u32 s52, s52, 0x100080
	s_addc_u32 s53, s53, 0
	s_add_i32 s54, s54, s18
	v_lshl_add_u64 v[142:143], s[52:53], 0, v[130:131]
	s_mov_b32 m0, s54
	s_nop 0
	global_load_lds_dwordx4 v[142:143], off
	v_lshl_add_u64 v[142:143], s[52:53], 0, v[132:133]
	s_add_i32 m0, s54, 0x2000
	s_nop 0
	global_load_lds_dwordx4 v[142:143], off
	s_waitcnt vmcnt(6)
	s_barrier
	s_setprio 1
	v_mfma_f32_16x16x32_bf16 v[46:49], v[198:201], v[166:169], v[46:49]
	v_mfma_f32_16x16x32_bf16 v[42:45], v[206:209], v[166:169], v[42:45]
	v_mfma_f32_16x16x32_bf16 v[38:41], v[198:201], v[174:177], v[38:41]
	v_mfma_f32_16x16x32_bf16 v[34:37], v[206:209], v[174:177], v[34:37]
	v_mfma_f32_16x16x32_bf16 v[14:17], v[198:201], v[182:185], v[14:17]
	v_mfma_f32_16x16x32_bf16 v[10:13], v[206:209], v[182:185], v[10:13]
	v_mfma_f32_16x16x32_bf16 v[6:9], v[198:201], v[190:193], v[6:9]
	v_mfma_f32_16x16x32_bf16 v[2:5], v[206:209], v[190:193], v[2:5]
	v_mfma_f32_16x16x32_bf16 v[46:49], v[202:205], v[170:173], v[46:49]
	v_mfma_f32_16x16x32_bf16 v[42:45], v[210:213], v[170:173], v[42:45]
	v_mfma_f32_16x16x32_bf16 v[38:41], v[202:205], v[178:181], v[38:41]
	v_mfma_f32_16x16x32_bf16 v[34:37], v[210:213], v[178:181], v[34:37]
	v_mfma_f32_16x16x32_bf16 v[14:17], v[202:205], v[186:189], v[14:17]
	v_mfma_f32_16x16x32_bf16 v[10:13], v[210:213], v[186:189], v[10:13]
	v_mfma_f32_16x16x32_bf16 v[6:9], v[202:205], v[194:197], v[6:9]
	v_mfma_f32_16x16x32_bf16 v[2:5], v[210:213], v[194:197], v[2:5]
	s_setprio 0
	s_add_i32 s60, s60, 2
	s_add_u32 s48, s48, 0x100
	s_addc_u32 s49, s49, 0
	s_add_u32 s58, s58, 0x100
	s_addc_u32 s59, s59, 0
	s_cmp_gt_u32 s60, 61
	s_barrier
	s_cbranch_scc1 .Lpeel_528_after

.Lpeel_528_after:
	v_lshl_add_u32 v186, s46, 8, v148
	v_lshl_or_b32 v142, s47, 8, v150
	v_ashrrev_i32_e32 v143, 31, v142
	v_or_b32_e32 v170, 16, v186
	v_lshlrev_b64 v[146:147], 2, v[142:143]
	v_ashrrev_i32_e32 v187, 31, v186
	v_ashrrev_i32_e32 v171, 31, v170
	v_lshl_add_u64 v[142:143], s[68:69], 0, v[146:147]
	v_lshlrev_b64 v[144:145], 13, v[186:187]
	v_lshlrev_b64 v[188:189], 13, v[170:171]
	v_lshl_add_u64 v[166:167], v[142:143], 0, v[144:145]
	v_lshl_add_u64 v[182:183], v[142:143], 0, v[188:189]
	global_load_dwordx4 v[154:157], v[166:167], off
	global_load_dwordx4 v[158:161], v[166:167], off offset:64
	global_load_dwordx4 v[162:165], v[166:167], off offset:512
	s_nop 0
	global_load_dwordx4 v[166:169], v[166:167], off offset:576
	s_nop 0
	global_load_dwordx4 v[170:173], v[182:183], off
	global_load_dwordx4 v[174:177], v[182:183], off offset:64
	global_load_dwordx4 v[178:181], v[182:183], off offset:512
	s_nop 0
	global_load_dwordx4 v[182:185], v[182:183], off offset:576
	v_lshl_add_u64 v[146:147], s[50:51], 0, v[146:147]
	v_or_b32_e32 v190, 32, v186
	v_lshl_add_u64 v[192:193], v[146:147], 0, v[144:145]
	v_ashrrev_i32_e32 v191, 31, v190
	v_lshl_add_u64 v[188:189], v[146:147], 0, v[188:189]
	v_lshlrev_b64 v[190:191], 13, v[190:191]
	v_lshl_add_u64 v[194:195], v[142:143], 0, v[190:191]
	s_and_b64 vcc, exec, s[0:1]
	s_mov_b32 s47, s16
	s_mov_b32 s46, s22
	s_mov_b64 s[52:53], s[44:45]
	s_mov_b64 s[48:49], s[24:25]
	v_readlane_b32 s93, v254, 9
	s_waitcnt vmcnt(0)
	v_pk_add_f32 v[128:129], v[128:129], v[156:157]
	v_pk_add_f32 v[126:127], v[126:127], v[154:155]
	v_pk_add_f32 v[110:111], v[110:111], v[162:163]
	v_pk_add_f32 v[124:125], v[124:125], v[160:161]
	v_pk_add_f32 v[122:123], v[122:123], v[158:159]
	v_pk_add_f32 v[112:113], v[112:113], v[164:165]
	v_pk_add_f32 v[108:109], v[108:109], v[168:169]
	v_pk_add_f32 v[106:107], v[106:107], v[166:167]
	v_pk_add_f32 v[120:121], v[120:121], v[172:173]
	v_pk_add_f32 v[118:119], v[118:119], v[170:171]
	v_pk_add_f32 v[116:117], v[116:117], v[176:177]
	v_pk_add_f32 v[114:115], v[114:115], v[174:175]
	v_pk_add_f32 v[104:105], v[104:105], v[180:181]
	v_pk_add_f32 v[102:103], v[102:103], v[178:179]
	v_pk_add_f32 v[100:101], v[100:101], v[184:185]
	v_pk_add_f32 v[98:99], v[98:99], v[182:183]
	global_store_dwordx4 v[192:193], v[126:129], off
	global_store_dwordx4 v[192:193], v[122:125], off offset:64
	global_store_dwordx4 v[192:193], v[110:113], off offset:512
	global_store_dwordx4 v[192:193], v[106:109], off offset:576
	global_store_dwordx4 v[188:189], v[118:121], off
	global_store_dwordx4 v[188:189], v[114:117], off offset:64
	global_store_dwordx4 v[188:189], v[102:105], off offset:512
	global_store_dwordx4 v[188:189], v[98:101], off offset:576
	v_or_b32_e32 v110, 48, v186
	v_ashrrev_i32_e32 v111, 31, v110
	v_lshlrev_b64 v[154:155], 13, v[110:111]
	global_load_dwordx4 v[98:101], v[194:195], off
	global_load_dwordx4 v[102:105], v[194:195], off offset:64
	v_lshl_add_u64 v[126:127], v[142:143], 0, v[154:155]
	global_load_dwordx4 v[106:109], v[194:195], off offset:512
	global_load_dwordx4 v[110:113], v[194:195], off offset:576
	global_load_dwordx4 v[114:117], v[126:127], off
	global_load_dwordx4 v[118:121], v[126:127], off offset:64
	global_load_dwordx4 v[122:125], v[126:127], off offset:512
	s_nop 0
	global_load_dwordx4 v[126:129], v[126:127], off offset:576
	v_lshl_add_u64 v[156:157], v[144:145], 0, s[6:7]
	v_lshl_add_u64 v[158:159], v[146:147], 0, v[190:191]
	v_lshl_add_u64 v[154:155], v[146:147], 0, v[154:155]
	v_lshl_add_u64 v[160:161], v[142:143], 0, v[156:157]
	s_waitcnt vmcnt(0)
	v_pk_add_f32 v[96:97], v[96:97], v[100:101]
	v_pk_add_f32 v[94:95], v[94:95], v[98:99]
	v_lshl_add_u64 v[98:99], v[144:145], 0, s[10:11]
	v_pk_add_f32 v[92:93], v[92:93], v[104:105]
	v_pk_add_f32 v[90:91], v[90:91], v[102:103]
	v_pk_add_f32 v[80:81], v[80:81], v[108:109]
	v_pk_add_f32 v[78:79], v[78:79], v[106:107]
	v_pk_add_f32 v[76:77], v[76:77], v[112:113]
	v_pk_add_f32 v[74:75], v[74:75], v[110:111]
	v_pk_add_f32 v[88:89], v[88:89], v[116:117]
	v_pk_add_f32 v[86:87], v[86:87], v[114:115]
	v_pk_add_f32 v[84:85], v[84:85], v[120:121]
	v_pk_add_f32 v[82:83], v[82:83], v[118:119]
	v_pk_add_f32 v[72:73], v[72:73], v[124:125]
	v_pk_add_f32 v[70:71], v[70:71], v[122:123]
	v_pk_add_f32 v[68:69], v[68:69], v[128:129]
	v_pk_add_f32 v[66:67], v[66:67], v[126:127]
	global_store_dwordx4 v[158:159], v[94:97], off
	global_store_dwordx4 v[158:159], v[90:93], off offset:64
	global_store_dwordx4 v[158:159], v[78:81], off offset:512
	global_store_dwordx4 v[158:159], v[74:77], off offset:576
	global_store_dwordx4 v[154:155], v[86:89], off
	global_store_dwordx4 v[154:155], v[82:85], off offset:64
	global_store_dwordx4 v[154:155], v[70:73], off offset:512
	global_store_dwordx4 v[154:155], v[66:69], off offset:576
	v_lshl_add_u64 v[94:95], v[142:143], 0, v[98:99]
	global_load_dwordx4 v[66:69], v[160:161], off
	global_load_dwordx4 v[70:73], v[160:161], off offset:64
	global_load_dwordx4 v[74:77], v[160:161], off offset:512
	global_load_dwordx4 v[78:81], v[160:161], off offset:576
	global_load_dwordx4 v[82:85], v[94:95], off
	global_load_dwordx4 v[86:89], v[94:95], off offset:64
	global_load_dwordx4 v[90:93], v[94:95], off offset:512
	s_nop 0
	global_load_dwordx4 v[94:97], v[94:95], off offset:576
	v_lshl_add_u64 v[100:101], v[144:145], 0, s[12:13]
	v_lshl_add_u64 v[102:103], v[146:147], 0, v[156:157]
	v_lshl_add_u64 v[98:99], v[146:147], 0, v[98:99]
	v_lshl_add_u64 v[104:105], v[142:143], 0, v[100:101]
	s_waitcnt vmcnt(0)
	v_pk_add_f32 v[64:65], v[64:65], v[68:69]
	v_pk_add_f32 v[62:63], v[62:63], v[66:67]
	v_lshl_add_u64 v[66:67], v[144:145], 0, s[14:15]
	v_pk_add_f32 v[60:61], v[60:61], v[72:73]
	v_pk_add_f32 v[58:59], v[58:59], v[70:71]
	v_pk_add_f32 v[48:49], v[48:49], v[76:77]
	v_pk_add_f32 v[46:47], v[46:47], v[74:75]
	v_pk_add_f32 v[44:45], v[44:45], v[80:81]
	v_pk_add_f32 v[42:43], v[42:43], v[78:79]
	v_pk_add_f32 v[56:57], v[56:57], v[84:85]
	v_pk_add_f32 v[54:55], v[54:55], v[82:83]
	v_pk_add_f32 v[52:53], v[52:53], v[88:89]
	v_pk_add_f32 v[50:51], v[50:51], v[86:87]
	v_pk_add_f32 v[40:41], v[40:41], v[92:93]
	v_pk_add_f32 v[38:39], v[38:39], v[90:91]
	v_pk_add_f32 v[36:37], v[36:37], v[96:97]
	v_pk_add_f32 v[34:35], v[34:35], v[94:95]
	global_store_dwordx4 v[102:103], v[62:65], off
	global_store_dwordx4 v[102:103], v[58:61], off offset:64
	global_store_dwordx4 v[102:103], v[46:49], off offset:512
	global_store_dwordx4 v[102:103], v[42:45], off offset:576
	global_store_dwordx4 v[98:99], v[54:57], off
	global_store_dwordx4 v[98:99], v[50:53], off offset:64
	global_store_dwordx4 v[98:99], v[38:41], off offset:512
	global_store_dwordx4 v[98:99], v[34:37], off offset:576
	v_lshl_add_u64 v[62:63], v[142:143], 0, v[66:67]
	global_load_dwordx4 v[34:37], v[104:105], off
	global_load_dwordx4 v[38:41], v[104:105], off offset:64
	global_load_dwordx4 v[42:45], v[104:105], off offset:512
	global_load_dwordx4 v[46:49], v[104:105], off offset:576
	global_load_dwordx4 v[50:53], v[62:63], off
	global_load_dwordx4 v[54:57], v[62:63], off offset:64
	global_load_dwordx4 v[58:61], v[62:63], off offset:512
	s_nop 0
	global_load_dwordx4 v[62:65], v[62:63], off offset:576
	v_lshl_add_u64 v[68:69], v[146:147], 0, v[100:101]
	v_lshl_add_u64 v[66:67], v[146:147], 0, v[66:67]
	s_waitcnt vmcnt(0)
	v_pk_add_f32 v[32:33], v[32:33], v[36:37]
	v_pk_add_f32 v[30:31], v[30:31], v[34:35]
	v_pk_add_f32 v[28:29], v[28:29], v[40:41]
	v_pk_add_f32 v[26:27], v[26:27], v[38:39]
	v_pk_add_f32 v[16:17], v[16:17], v[44:45]
	v_pk_add_f32 v[14:15], v[14:15], v[42:43]
	v_pk_add_f32 v[12:13], v[12:13], v[48:49]
	v_pk_add_f32 v[10:11], v[10:11], v[46:47]
	v_pk_add_f32 v[24:25], v[24:25], v[52:53]
	v_pk_add_f32 v[22:23], v[22:23], v[50:51]
	v_pk_add_f32 v[20:21], v[20:21], v[56:57]
	v_pk_add_f32 v[18:19], v[18:19], v[54:55]
	v_pk_add_f32 v[8:9], v[8:9], v[60:61]
	v_pk_add_f32 v[6:7], v[6:7], v[58:59]
	v_pk_add_f32 v[4:5], v[4:5], v[64:65]
	v_pk_add_f32 v[2:3], v[2:3], v[62:63]
	global_store_dwordx4 v[68:69], v[30:33], off
	global_store_dwordx4 v[68:69], v[26:29], off offset:64
	global_store_dwordx4 v[68:69], v[14:17], off offset:512
	global_store_dwordx4 v[68:69], v[10:13], off offset:576
	global_store_dwordx4 v[66:67], v[22:25], off
	global_store_dwordx4 v[66:67], v[18:21], off offset:64
	global_store_dwordx4 v[66:67], v[6:9], off offset:512
	global_store_dwordx4 v[66:67], v[2:5], off offset:576
	s_cbranch_vccz .LBB0_521
	s_waitcnt vmcnt(0)
	s_cmpk_gt_u32 s2, 0xff
	s_cbranch_scc1 .LBB0_532
	s_barrier

.LBB0_810:
	s_ashr_i32 s9, s8, 31
	s_lshl_b64 s[10:11], s[8:9], 20
	v_readlane_b32 s9, v254, 34
	s_add_u32 s10, s9, s10
	v_readlane_b32 s9, v254, 35
	s_addc_u32 s11, s9, s11
	s_and_b64 s[14:15], s[14:15], exec
	s_cselect_b32 s9, s11, s13
	s_cselect_b32 s59, s10, s12
	v_mov_b32_e32 v139, v135
	v_mov_b32_e32 v141, v135
	s_add_u32 s60, s12, 0x100
	v_mov_b32_e32 v2, 0
	v_lshl_add_u64 v[142:143], s[6:7], 0, v[140:141]
	v_lshl_add_u64 v[144:145], s[6:7], 0, v[138:139]
	s_addc_u32 s61, s13, 0
	s_mov_b32 s62, -2
	s_mov_b64 s[12:13], 0
	s_add_u32 s14, s28, s12
	s_addc_u32 s15, s29, s13
	s_add_u32 s16, s14, 0x2a300100
	ds_read_b128 v[160:163], v152
	ds_read_b128 v[164:167], v152 offset:1024
	ds_read_b128 v[168:171], v152 offset:2048
	ds_read_b128 v[172:175], v152 offset:3072
	s_addc_u32 s17, s15, 0
	s_add_u32 s63, s60, s12
	s_addc_u32 s64, s61, s13
	s_cmpk_eq_i32 s12, 0xf00
	s_cselect_b64 vcc, -1, 0
	s_and_b64 s[14:15], vcc, exec
	v_cndmask_b32_e32 v134, v137, v155, vcc
	v_cndmask_b32_e32 v216, v136, v156, vcc
	v_cndmask_b32_e32 v1, v138, v157, vcc
	v_cndmask_b32_e32 v139, v140, v158, vcc
	s_cselect_b32 s17, s37, s17
	s_cselect_b32 s16, s36, s16
	s_cselect_b32 s15, s9, s64
	s_cselect_b32 s14, s59, s63
	v_lshl_add_u64 v[208:209], v[144:145], 0, s[12:13]
	s_add_i32 m0, s26, 0xc000
	ds_read_b128 v[176:179], v153
	ds_read_b128 v[180:183], v153 offset:1024
	ds_read_b128 v[184:187], v153 offset:2048
	ds_read_b128 v[188:191], v153 offset:3072
	ds_read_b128 v[192:195], v153 offset:4096
	ds_read_b128 v[196:199], v153 offset:5120
	ds_read_b128 v[200:203], v153 offset:6144
	ds_read_b128 v[204:207], v153 offset:7168
	global_load_lds_dwordx4 v[208:209], off
	v_lshl_add_u64 v[208:209], v[142:143], 0, s[12:13]
	s_add_i32 m0, s26, 0xe000
	s_nop 0
	global_load_lds_dwordx4 v[208:209], off
	s_waitcnt lgkmcnt(8)
	s_barrier
	s_waitcnt lgkmcnt(0)
	s_setprio 1
	s_waitcnt lgkmcnt(0)
	v_mfma_f32_16x16x32_bf16 v[126:129], v[160:163], v[176:179], 0
	v_mfma_f32_16x16x32_bf16 v[122:125], v[168:171], v[176:179], 0
	v_mfma_f32_16x16x32_bf16 v[110:113], v[160:163], v[184:187], 0
	v_mfma_f32_16x16x32_bf16 v[106:109], v[168:171], v[184:187], 0
	v_mfma_f32_16x16x32_bf16 v[94:97], v[160:163], v[192:195], 0
	v_mfma_f32_16x16x32_bf16 v[90:93], v[168:171], v[192:195], 0
	v_mfma_f32_16x16x32_bf16 v[78:81], v[160:163], v[200:203], 0
	v_mfma_f32_16x16x32_bf16 v[74:77], v[168:171], v[200:203], 0
	v_mfma_f32_16x16x32_bf16 v[126:129], v[164:167], v[180:183], v[126:129]
	v_mfma_f32_16x16x32_bf16 v[122:125], v[172:175], v[180:183], v[122:125]
	v_mfma_f32_16x16x32_bf16 v[110:113], v[164:167], v[188:191], v[110:113]
	v_mfma_f32_16x16x32_bf16 v[106:109], v[172:175], v[188:191], v[106:109]
	v_mfma_f32_16x16x32_bf16 v[94:97], v[164:167], v[196:199], v[94:97]
	v_mfma_f32_16x16x32_bf16 v[90:93], v[172:175], v[196:199], v[90:93]
	v_mfma_f32_16x16x32_bf16 v[78:81], v[164:167], v[204:207], v[78:81]
	v_mfma_f32_16x16x32_bf16 v[74:77], v[172:175], v[204:207], v[74:77]
	s_setprio 0
	s_barrier
	s_add_i32 s63, s41, s25
	v_lshl_add_u64 v[228:229], s[14:15], 0, v[132:133]
	s_mov_b32 m0, s63
	ds_read_b128 v[208:211], v154
	ds_read_b128 v[212:215], v154 offset:1024
	ds_read_b128 v[220:223], v154 offset:2048
	ds_read_b128 v[224:227], v154 offset:3072
	global_load_lds_dwordx4 v[228:229], off
	v_lshl_add_u64 v[230:231], s[14:15], 0, v[130:131]
	s_add_i32 m0, s63, 0x2000
	s_nop 0
	global_load_lds_dwordx4 v[230:231], off
	s_barrier
	s_waitcnt lgkmcnt(0)
	s_setprio 1
	s_waitcnt lgkmcnt(0)
	v_mfma_f32_16x16x32_bf16 v[118:121], v[208:211], v[176:179], 0
	v_mfma_f32_16x16x32_bf16 v[114:117], v[220:223], v[176:179], 0
	v_mfma_f32_16x16x32_bf16 v[102:105], v[208:211], v[184:187], 0
	v_mfma_f32_16x16x32_bf16 v[98:101], v[220:223], v[184:187], 0
	v_mfma_f32_16x16x32_bf16 v[86:89], v[208:211], v[192:195], 0
	v_mfma_f32_16x16x32_bf16 v[82:85], v[220:223], v[192:195], 0
	v_mfma_f32_16x16x32_bf16 v[70:73], v[208:211], v[200:203], 0
	v_mfma_f32_16x16x32_bf16 v[66:69], v[220:223], v[200:203], 0
	v_mfma_f32_16x16x32_bf16 v[118:121], v[212:215], v[180:183], v[118:121]
	v_mfma_f32_16x16x32_bf16 v[114:117], v[224:227], v[180:183], v[114:117]
	v_mfma_f32_16x16x32_bf16 v[102:105], v[212:215], v[188:191], v[102:105]
	v_mfma_f32_16x16x32_bf16 v[98:101], v[224:227], v[188:191], v[98:101]
	v_mfma_f32_16x16x32_bf16 v[86:89], v[212:215], v[196:199], v[86:89]
	v_mfma_f32_16x16x32_bf16 v[82:85], v[224:227], v[196:199], v[82:85]
	v_mfma_f32_16x16x32_bf16 v[70:73], v[212:215], v[204:207], v[70:73]
	v_mfma_f32_16x16x32_bf16 v[66:69], v[224:227], v[204:207], v[66:69]
	s_setprio 0
	s_mov_b32 m0, s26
	s_barrier
	ds_read_b128 v[176:179], v153 offset:16384
	ds_read_b128 v[180:183], v153 offset:17408
	ds_read_b128 v[184:187], v153 offset:18432
	ds_read_b128 v[188:191], v153 offset:19456
	ds_read_b128 v[192:195], v153 offset:20480
	ds_read_b128 v[196:199], v153 offset:21504
	ds_read_b128 v[200:203], v153 offset:22528
	ds_read_b128 v[204:207], v153 offset:23552
	global_load_lds_dwordx4 v134, s[16:17]
	s_mov_b32 m0, s27
	v_mov_b32_e32 v217, v135
	global_load_lds_dwordx4 v216, s[16:17]
	s_barrier
	s_waitcnt lgkmcnt(0)
	v_lshl_add_u64 v[232:233], s[16:17], 0, v[134:135]
	v_lshl_add_u64 v[216:217], s[16:17], 0, v[216:217]
	s_setprio 1
	s_waitcnt lgkmcnt(0)
	v_mfma_f32_16x16x32_bf16 v[62:65], v[160:163], v[176:179], 0
	v_mfma_f32_16x16x32_bf16 v[58:61], v[168:171], v[176:179], 0
	v_mfma_f32_16x16x32_bf16 v[46:49], v[160:163], v[184:187], 0
	v_mfma_f32_16x16x32_bf16 v[42:45], v[168:171], v[184:187], 0
	v_mfma_f32_16x16x32_bf16 v[30:33], v[160:163], v[192:195], 0
	v_mfma_f32_16x16x32_bf16 v[26:29], v[168:171], v[192:195], 0
	v_mfma_f32_16x16x32_bf16 v[14:17], v[160:163], v[200:203], 0
	v_mfma_f32_16x16x32_bf16 v[10:13], v[168:171], v[200:203], 0
	v_mfma_f32_16x16x32_bf16 v[62:65], v[164:167], v[180:183], v[62:65]
	v_mfma_f32_16x16x32_bf16 v[58:61], v[172:175], v[180:183], v[58:61]
	v_mfma_f32_16x16x32_bf16 v[46:49], v[164:167], v[188:191], v[46:49]
	v_mfma_f32_16x16x32_bf16 v[42:45], v[172:175], v[188:191], v[42:45]
	v_mfma_f32_16x16x32_bf16 v[30:33], v[164:167], v[196:199], v[30:33]
	v_mfma_f32_16x16x32_bf16 v[26:29], v[172:175], v[196:199], v[26:29]
	v_mfma_f32_16x16x32_bf16 v[14:17], v[164:167], v[204:207], v[14:17]
	v_mfma_f32_16x16x32_bf16 v[10:13], v[172:175], v[204:207], v[10:13]
	s_setprio 0
	s_barrier
	s_add_u32 s64, s14, 0x80000
	s_addc_u32 s65, s15, 0
	s_add_i32 s63, s48, s25
	v_lshl_add_u64 v[160:161], s[64:65], 0, v[132:133]
	s_mov_b32 m0, s63
	s_nop 0
	global_load_lds_dwordx4 v[160:161], off
	v_lshl_add_u64 v[160:161], s[64:65], 0, v[130:131]
	s_add_i32 m0, s63, 0x2000
	s_nop 0
	global_load_lds_dwordx4 v[160:161], off
	s_waitcnt vmcnt(6)
	s_barrier
	s_setprio 1
	v_mfma_f32_16x16x32_bf16 v[54:57], v[208:211], v[176:179], 0
	v_mfma_f32_16x16x32_bf16 v[50:53], v[220:223], v[176:179], 0
	v_mfma_f32_16x16x32_bf16 v[38:41], v[208:211], v[184:187], 0
	v_mfma_f32_16x16x32_bf16 v[34:37], v[220:223], v[184:187], 0
	v_mfma_f32_16x16x32_bf16 v[22:25], v[208:211], v[192:195], 0
	v_mfma_f32_16x16x32_bf16 v[18:21], v[220:223], v[192:195], 0
	v_mfma_f32_16x16x32_bf16 v[6:9], v[208:211], v[200:203], 0
	v_mfma_f32_16x16x32_bf16 v[2:5], v[220:223], v[200:203], 0
	v_mfma_f32_16x16x32_bf16 v[54:57], v[212:215], v[180:183], v[54:57]
	v_mfma_f32_16x16x32_bf16 v[50:53], v[224:227], v[180:183], v[50:53]
	v_mfma_f32_16x16x32_bf16 v[38:41], v[212:215], v[188:191], v[38:41]
	v_mfma_f32_16x16x32_bf16 v[34:37], v[224:227], v[188:191], v[34:37]
	v_mfma_f32_16x16x32_bf16 v[22:25], v[212:215], v[196:199], v[22:25]
	v_mfma_f32_16x16x32_bf16 v[18:21], v[224:227], v[196:199], v[18:21]
	v_mfma_f32_16x16x32_bf16 v[6:9], v[212:215], v[204:207], v[6:9]
	v_mfma_f32_16x16x32_bf16 v[2:5], v[224:227], v[204:207], v[2:5]
	s_setprio 0
	s_add_i32 s63, 0, 0x18000
	v_add_u32_e32 v134, s63, v150
	s_barrier
	ds_read_b128 v[160:163], v134
	ds_read_b128 v[164:167], v134 offset:1024
	ds_read_b128 v[168:171], v134 offset:2048
	ds_read_b128 v[172:175], v134 offset:3072
	s_mov_b32 m0, s33
	ds_read_b128 v[176:179], v153 offset:32768
	ds_read_b128 v[180:183], v153 offset:33792
	ds_read_b128 v[184:187], v153 offset:34816
	ds_read_b128 v[188:191], v153 offset:35840
	ds_read_b128 v[192:195], v153 offset:36864
	ds_read_b128 v[196:199], v153 offset:37888
	ds_read_b128 v[200:203], v153 offset:38912
	ds_read_b128 v[204:207], v153 offset:39936
	global_load_lds_dwordx4 v1, s[16:17]
	s_mov_b32 m0, s34
	s_nop 0
	global_load_lds_dwordx4 v139, s[16:17]
	s_waitcnt lgkmcnt(8)
	s_barrier
	s_waitcnt lgkmcnt(0)
	s_setprio 1
	s_waitcnt lgkmcnt(0)
	v_mfma_f32_16x16x32_bf16 v[126:129], v[160:163], v[176:179], v[126:129]
	v_mfma_f32_16x16x32_bf16 v[122:125], v[168:171], v[176:179], v[122:125]
	v_mfma_f32_16x16x32_bf16 v[110:113], v[160:163], v[184:187], v[110:113]
	v_mfma_f32_16x16x32_bf16 v[106:109], v[168:171], v[184:187], v[106:109]
	v_mfma_f32_16x16x32_bf16 v[94:97], v[160:163], v[192:195], v[94:97]
	v_mfma_f32_16x16x32_bf16 v[90:93], v[168:171], v[192:195], v[90:93]
	v_mfma_f32_16x16x32_bf16 v[78:81], v[160:163], v[200:203], v[78:81]
	v_mfma_f32_16x16x32_bf16 v[74:77], v[168:171], v[200:203], v[74:77]
	v_mfma_f32_16x16x32_bf16 v[126:129], v[164:167], v[180:183], v[126:129]
	v_mfma_f32_16x16x32_bf16 v[122:125], v[172:175], v[180:183], v[122:125]
	v_mfma_f32_16x16x32_bf16 v[110:113], v[164:167], v[188:191], v[110:113]
	v_mfma_f32_16x16x32_bf16 v[106:109], v[172:175], v[188:191], v[106:109]
	v_mfma_f32_16x16x32_bf16 v[94:97], v[164:167], v[196:199], v[94:97]
	v_mfma_f32_16x16x32_bf16 v[90:93], v[172:175], v[196:199], v[90:93]
	v_mfma_f32_16x16x32_bf16 v[78:81], v[164:167], v[204:207], v[78:81]
	v_mfma_f32_16x16x32_bf16 v[74:77], v[172:175], v[204:207], v[74:77]
	s_setprio 0
	s_barrier
	s_add_i32 s16, 0, 0x1c000
	s_add_i32 s17, s63, s25
	v_add_u32_e32 v1, s16, v150
	v_lshl_add_u64 v[228:229], v[228:229], 0, s[0:1]
	s_mov_b32 m0, s17
	ds_read_b128 v[208:211], v1
	ds_read_b128 v[212:215], v1 offset:1024
	ds_read_b128 v[220:223], v1 offset:2048
	ds_read_b128 v[224:227], v1 offset:3072
	global_load_lds_dwordx4 v[228:229], off
	v_lshl_add_u64 v[228:229], v[230:231], 0, s[0:1]
	s_add_i32 m0, s17, 0x2000
	s_nop 0
	global_load_lds_dwordx4 v[228:229], off
	s_barrier
	s_waitcnt lgkmcnt(0)
	s_setprio 1
	s_waitcnt lgkmcnt(0)
	v_mfma_f32_16x16x32_bf16 v[118:121], v[208:211], v[176:179], v[118:121]
	v_mfma_f32_16x16x32_bf16 v[114:117], v[220:223], v[176:179], v[114:117]
	v_mfma_f32_16x16x32_bf16 v[102:105], v[208:211], v[184:187], v[102:105]
	v_mfma_f32_16x16x32_bf16 v[98:101], v[220:223], v[184:187], v[98:101]
	v_mfma_f32_16x16x32_bf16 v[86:89], v[208:211], v[192:195], v[86:89]
	v_mfma_f32_16x16x32_bf16 v[82:85], v[220:223], v[192:195], v[82:85]
	v_mfma_f32_16x16x32_bf16 v[70:73], v[208:211], v[200:203], v[70:73]
	v_mfma_f32_16x16x32_bf16 v[66:69], v[220:223], v[200:203], v[66:69]
	v_mfma_f32_16x16x32_bf16 v[118:121], v[212:215], v[180:183], v[118:121]
	v_mfma_f32_16x16x32_bf16 v[114:117], v[224:227], v[180:183], v[114:117]
	v_mfma_f32_16x16x32_bf16 v[102:105], v[212:215], v[188:191], v[102:105]
	v_mfma_f32_16x16x32_bf16 v[98:101], v[224:227], v[188:191], v[98:101]
	v_mfma_f32_16x16x32_bf16 v[86:89], v[212:215], v[196:199], v[86:89]
	v_mfma_f32_16x16x32_bf16 v[82:85], v[224:227], v[196:199], v[82:85]
	v_mfma_f32_16x16x32_bf16 v[70:73], v[212:215], v[204:207], v[70:73]
	v_mfma_f32_16x16x32_bf16 v[66:69], v[224:227], v[204:207], v[66:69]
	s_setprio 0
	s_mov_b32 m0, s35
	v_lshl_add_u64 v[228:229], v[232:233], 0, s[0:1]
	s_barrier
	ds_read_b128 v[176:179], v153 offset:49152
	ds_read_b128 v[180:183], v153 offset:50176
	ds_read_b128 v[184:187], v153 offset:51200
	ds_read_b128 v[188:191], v153 offset:52224
	ds_read_b128 v[192:195], v153 offset:53248
	ds_read_b128 v[196:199], v153 offset:54272
	ds_read_b128 v[200:203], v153 offset:55296
	ds_read_b128 v[204:207], v153 offset:56320
	global_load_lds_dwordx4 v[228:229], off
	v_lshl_add_u64 v[216:217], v[216:217], 0, s[0:1]
	s_mov_b32 m0, s40
	s_nop 0
	global_load_lds_dwordx4 v[216:217], off
	s_barrier
	s_waitcnt lgkmcnt(0)
	s_setprio 1
	s_waitcnt lgkmcnt(0)
	v_mfma_f32_16x16x32_bf16 v[62:65], v[160:163], v[176:179], v[62:65]
	v_mfma_f32_16x16x32_bf16 v[58:61], v[168:171], v[176:179], v[58:61]
	v_mfma_f32_16x16x32_bf16 v[46:49], v[160:163], v[184:187], v[46:49]
	v_mfma_f32_16x16x32_bf16 v[42:45], v[168:171], v[184:187], v[42:45]
	v_mfma_f32_16x16x32_bf16 v[30:33], v[160:163], v[192:195], v[30:33]
	v_mfma_f32_16x16x32_bf16 v[26:29], v[168:171], v[192:195], v[26:29]
	v_mfma_f32_16x16x32_bf16 v[14:17], v[160:163], v[200:203], v[14:17]
	v_mfma_f32_16x16x32_bf16 v[10:13], v[168:171], v[200:203], v[10:13]
	v_mfma_f32_16x16x32_bf16 v[62:65], v[164:167], v[180:183], v[62:65]
	v_mfma_f32_16x16x32_bf16 v[58:61], v[172:175], v[180:183], v[58:61]
	v_mfma_f32_16x16x32_bf16 v[46:49], v[164:167], v[188:191], v[46:49]
	v_mfma_f32_16x16x32_bf16 v[42:45], v[172:175], v[188:191], v[42:45]
	v_mfma_f32_16x16x32_bf16 v[30:33], v[164:167], v[196:199], v[30:33]
	v_mfma_f32_16x16x32_bf16 v[26:29], v[172:175], v[196:199], v[26:29]
	v_mfma_f32_16x16x32_bf16 v[14:17], v[164:167], v[204:207], v[14:17]
	v_mfma_f32_16x16x32_bf16 v[10:13], v[172:175], v[204:207], v[10:13]
	s_setprio 0
	s_barrier
	s_add_u32 s14, s14, 0x80080
	s_addc_u32 s15, s15, 0
	s_add_i32 s16, s16, s25
	v_lshl_add_u64 v[160:161], s[14:15], 0, v[132:133]
	s_mov_b32 m0, s16
	s_nop 0
	global_load_lds_dwordx4 v[160:161], off
	v_lshl_add_u64 v[160:161], s[14:15], 0, v[130:131]
	s_add_i32 m0, s16, 0x2000
	s_nop 0
	global_load_lds_dwordx4 v[160:161], off
	s_waitcnt vmcnt(6)
	s_barrier
	s_setprio 1
	v_mfma_f32_16x16x32_bf16 v[54:57], v[208:211], v[176:179], v[54:57]
	v_mfma_f32_16x16x32_bf16 v[50:53], v[220:223], v[176:179], v[50:53]
	v_mfma_f32_16x16x32_bf16 v[38:41], v[208:211], v[184:187], v[38:41]
	v_mfma_f32_16x16x32_bf16 v[34:37], v[220:223], v[184:187], v[34:37]
	v_mfma_f32_16x16x32_bf16 v[22:25], v[208:211], v[192:195], v[22:25]
	v_mfma_f32_16x16x32_bf16 v[18:21], v[220:223], v[192:195], v[18:21]
	v_mfma_f32_16x16x32_bf16 v[6:9], v[208:211], v[200:203], v[6:9]
	v_mfma_f32_16x16x32_bf16 v[2:5], v[220:223], v[200:203], v[2:5]
	v_mfma_f32_16x16x32_bf16 v[54:57], v[212:215], v[180:183], v[54:57]
	v_mfma_f32_16x16x32_bf16 v[50:53], v[224:227], v[180:183], v[50:53]
	v_mfma_f32_16x16x32_bf16 v[38:41], v[212:215], v[188:191], v[38:41]
	v_mfma_f32_16x16x32_bf16 v[34:37], v[224:227], v[188:191], v[34:37]
	v_mfma_f32_16x16x32_bf16 v[22:25], v[212:215], v[196:199], v[22:25]
	v_mfma_f32_16x16x32_bf16 v[18:21], v[224:227], v[196:199], v[18:21]
	v_mfma_f32_16x16x32_bf16 v[6:9], v[212:215], v[204:207], v[6:9]
	v_mfma_f32_16x16x32_bf16 v[2:5], v[224:227], v[204:207], v[2:5]
	s_setprio 0
	s_add_i32 s62, s62, 2
	s_add_u32 s12, s12, 0x100
	s_addc_u32 s13, s13, 0
	s_cmp_gt_u32 s62, 29
	s_barrier
	s_cbranch_scc1 .Lpeel_811_after

.Lpeel_811_after:
	v_mul_f32_e32 v1, 0xbfb8aa3b, v126
	v_exp_f32_e32 v1, v1
	v_mul_f32_e32 v136, 0xbfb8aa3b, v127
	v_exp_f32_e32 v136, v136
	v_lshl_or_b32 v138, s57, 7, v151
	v_add_f32_e32 v1, 1.0, v1
	v_rcp_f32_e32 v140, v1
	v_add_f32_e32 v1, 1.0, v136
	v_rcp_f32_e32 v141, v1
	v_mul_f32_e32 v1, 0xbfb8aa3b, v128
	v_exp_f32_e32 v1, v1
	v_lshl_add_u32 v134, s58, 8, v149
	v_pk_mul_f32 v[126:127], v[126:127], v[140:141]
	v_mul_f32_e32 v140, 0xbfb8aa3b, v129
	v_exp_f32_e32 v140, v140
	v_add_f32_e32 v1, 1.0, v1
	v_pk_mul_f32 v[118:119], v[126:127], v[118:119]
	v_rcp_f32_e32 v126, v1
	v_add_f32_e32 v1, 1.0, v140
	v_rcp_f32_e32 v127, v1
	v_mul_f32_e32 v1, 0xbfb8aa3b, v122
	v_exp_f32_e32 v1, v1
	v_mul_f32_e32 v140, 0xbfb8aa3b, v123
	v_exp_f32_e32 v140, v140
	v_pk_mul_f32 v[126:127], v[128:129], v[126:127]
	v_add_f32_e32 v1, 1.0, v1
	v_mul_f32_e32 v129, 0xbfb8aa3b, v124
	v_rcp_f32_e32 v128, v1
	v_add_f32_e32 v1, 1.0, v140
	v_exp_f32_e32 v140, v129
	v_mul_f32_e32 v129, 0xbfb8aa3b, v125
	v_exp_f32_e32 v141, v129
	v_rcp_f32_e32 v129, v1
	v_add_f32_e32 v1, 1.0, v140
	v_rcp_f32_e32 v140, v1
	v_add_f32_e32 v1, 1.0, v141
	v_rcp_f32_e32 v141, v1
	v_pk_mul_f32 v[122:123], v[122:123], v[128:129]
	v_pk_mul_f32 v[120:121], v[126:127], v[120:121]
	v_pk_mul_f32 v[122:123], v[122:123], v[114:115]
	v_pk_mul_f32 v[114:115], v[124:125], v[140:141]
	v_mul_f32_e32 v1, 0xbfb8aa3b, v110
	v_pk_mul_f32 v[124:125], v[114:115], v[116:117]
	v_cvt_pk_bf16_f32 v117, v120, v121
	v_exp_f32_e32 v1, v1
	v_mul_f32_e32 v120, 0xbfb8aa3b, v111
	v_exp_f32_e32 v120, v120
	v_ashrrev_i32_e32 v139, 31, v138
	v_mov_b64_e32 v[136:137], s[44:45]
	v_mad_i64_i32 v[142:143], s[12:13], v134, s49, v[136:137]
	v_lshlrev_b64 v[114:115], 1, v[138:139]
	v_lshl_add_u64 v[126:127], v[142:143], 0, v[114:115]
	v_cvt_pk_bf16_f32 v116, v118, v119
	v_cvt_pk_bf16_f32 v118, v122, v123
	v_cvt_pk_bf16_f32 v119, v124, v125
	v_add_f32_e32 v1, 1.0, v1
	global_store_dwordx4 v[126:127], v[116:119], off
	s_cmp_eq_u32 s54, s20
	v_mov_b32_e32 v138, v157
	v_rcp_f32_e32 v116, v1
	v_add_f32_e32 v1, 1.0, v120
	v_rcp_f32_e32 v117, v1
	v_or_b32_e32 v1, 16, v134
	v_mad_i64_i32 v[118:119], s[12:13], v1, s49, v[136:137]
	v_mul_f32_e32 v1, 0xbfb8aa3b, v112
	v_pk_mul_f32 v[110:111], v[110:111], v[116:117]
	v_exp_f32_e32 v1, v1
	v_mul_f32_e32 v116, 0xbfb8aa3b, v113
	v_exp_f32_e32 v116, v116
	v_pk_mul_f32 v[102:103], v[110:111], v[102:103]
	v_add_f32_e32 v1, 1.0, v1
	v_rcp_f32_e32 v110, v1
	v_add_f32_e32 v1, 1.0, v116
	v_rcp_f32_e32 v111, v1
	v_mul_f32_e32 v1, 0xbfb8aa3b, v106
	v_exp_f32_e32 v1, v1
	v_mul_f32_e32 v116, 0xbfb8aa3b, v107
	v_exp_f32_e32 v116, v116
	v_pk_mul_f32 v[110:111], v[112:113], v[110:111]
	v_add_f32_e32 v1, 1.0, v1
	v_mul_f32_e32 v113, 0xbfb8aa3b, v108
	v_rcp_f32_e32 v112, v1
	v_add_f32_e32 v1, 1.0, v116
	v_exp_f32_e32 v116, v113
	v_mul_f32_e32 v113, 0xbfb8aa3b, v109
	v_exp_f32_e32 v117, v113
	v_rcp_f32_e32 v113, v1
	v_add_f32_e32 v1, 1.0, v116
	v_rcp_f32_e32 v116, v1
	v_add_f32_e32 v1, 1.0, v117
	v_rcp_f32_e32 v117, v1
	v_pk_mul_f32 v[106:107], v[106:107], v[112:113]
	v_mul_f32_e32 v1, 0xbfb8aa3b, v94
	v_pk_mul_f32 v[106:107], v[106:107], v[98:99]
	v_pk_mul_f32 v[98:99], v[108:109], v[116:117]
	v_exp_f32_e32 v1, v1
	v_pk_mul_f32 v[108:109], v[98:99], v[100:101]
	v_cvt_pk_bf16_f32 v98, v102, v103
	v_mul_f32_e32 v102, 0xbfb8aa3b, v95
	v_exp_f32_e32 v102, v102
	v_pk_mul_f32 v[104:105], v[110:111], v[104:105]
	v_lshl_add_u64 v[110:111], v[118:119], 0, v[114:115]
	v_cvt_pk_bf16_f32 v99, v104, v105
	v_cvt_pk_bf16_f32 v100, v106, v107
	v_cvt_pk_bf16_f32 v101, v108, v109
	v_add_f32_e32 v1, 1.0, v1
	global_store_dwordx4 v[110:111], v[98:101], off
	v_mov_b32_e32 v140, v158
	s_mov_b32 s57, s56
	v_rcp_f32_e32 v98, v1
	v_add_f32_e32 v1, 1.0, v102
	v_rcp_f32_e32 v99, v1
	v_or_b32_e32 v1, 32, v134
	v_mad_i64_i32 v[100:101], s[12:13], v1, s49, v[136:137]
	v_mul_f32_e32 v1, 0xbfb8aa3b, v96
	v_pk_mul_f32 v[94:95], v[94:95], v[98:99]
	v_exp_f32_e32 v1, v1
	v_mul_f32_e32 v98, 0xbfb8aa3b, v97
	v_exp_f32_e32 v98, v98
	v_pk_mul_f32 v[86:87], v[94:95], v[86:87]
	v_add_f32_e32 v1, 1.0, v1
	v_rcp_f32_e32 v94, v1
	v_add_f32_e32 v1, 1.0, v98
	v_rcp_f32_e32 v95, v1
	v_mul_f32_e32 v1, 0xbfb8aa3b, v90
	v_exp_f32_e32 v1, v1
	v_mul_f32_e32 v98, 0xbfb8aa3b, v91
	v_exp_f32_e32 v98, v98
	v_pk_mul_f32 v[94:95], v[96:97], v[94:95]
	v_add_f32_e32 v1, 1.0, v1
	v_mul_f32_e32 v97, 0xbfb8aa3b, v92
	v_rcp_f32_e32 v96, v1
	v_add_f32_e32 v1, 1.0, v98
	v_exp_f32_e32 v98, v97
	v_mul_f32_e32 v97, 0xbfb8aa3b, v93
	v_exp_f32_e32 v99, v97
	v_rcp_f32_e32 v97, v1
	v_add_f32_e32 v1, 1.0, v98
	v_rcp_f32_e32 v98, v1
	v_add_f32_e32 v1, 1.0, v99
	v_rcp_f32_e32 v99, v1
	v_pk_mul_f32 v[90:91], v[90:91], v[96:97]
	v_mul_f32_e32 v1, 0xbfb8aa3b, v78
	v_pk_mul_f32 v[90:91], v[90:91], v[82:83]
	v_pk_mul_f32 v[82:83], v[92:93], v[98:99]
	v_exp_f32_e32 v1, v1
	v_pk_mul_f32 v[92:93], v[82:83], v[84:85]
	v_cvt_pk_bf16_f32 v82, v86, v87
	v_mul_f32_e32 v86, 0xbfb8aa3b, v79
	v_exp_f32_e32 v86, v86
	v_pk_mul_f32 v[88:89], v[94:95], v[88:89]
	v_lshl_add_u64 v[94:95], v[100:101], 0, v[114:115]
	v_cvt_pk_bf16_f32 v83, v88, v89
	v_cvt_pk_bf16_f32 v84, v90, v91
	v_cvt_pk_bf16_f32 v85, v92, v93
	v_add_f32_e32 v1, 1.0, v1
	global_store_dwordx4 v[94:95], v[82:85], off
	s_mov_b32 s58, s55
	s_nop 0
	v_rcp_f32_e32 v82, v1
	v_add_f32_e32 v1, 1.0, v86
	v_rcp_f32_e32 v83, v1
	v_or_b32_e32 v1, 48, v134
	v_mad_i64_i32 v[84:85], s[12:13], v1, s49, v[136:137]
	v_mul_f32_e32 v1, 0xbfb8aa3b, v80
	v_pk_mul_f32 v[78:79], v[78:79], v[82:83]
	v_exp_f32_e32 v1, v1
	v_mul_f32_e32 v82, 0xbfb8aa3b, v81
	v_exp_f32_e32 v82, v82
	v_pk_mul_f32 v[70:71], v[78:79], v[70:71]
	v_add_f32_e32 v1, 1.0, v1
	v_rcp_f32_e32 v78, v1
	v_add_f32_e32 v1, 1.0, v82
	v_rcp_f32_e32 v79, v1
	v_mul_f32_e32 v1, 0xbfb8aa3b, v74
	v_exp_f32_e32 v1, v1
	v_mul_f32_e32 v82, 0xbfb8aa3b, v75
	v_exp_f32_e32 v82, v82
	v_pk_mul_f32 v[78:79], v[80:81], v[78:79]
	v_add_f32_e32 v1, 1.0, v1
	v_mul_f32_e32 v81, 0xbfb8aa3b, v76
	v_rcp_f32_e32 v80, v1
	v_add_f32_e32 v1, 1.0, v82
	v_exp_f32_e32 v82, v81
	v_mul_f32_e32 v81, 0xbfb8aa3b, v77
	v_exp_f32_e32 v83, v81
	v_rcp_f32_e32 v81, v1
	v_add_f32_e32 v1, 1.0, v82
	v_rcp_f32_e32 v82, v1
	v_add_f32_e32 v1, 1.0, v83
	v_rcp_f32_e32 v83, v1
	v_pk_mul_f32 v[74:75], v[74:75], v[80:81]
	v_mul_f32_e32 v1, 0xbfb8aa3b, v62
	v_pk_mul_f32 v[74:75], v[74:75], v[66:67]
	v_pk_mul_f32 v[66:67], v[76:77], v[82:83]
	v_exp_f32_e32 v1, v1
	v_pk_mul_f32 v[76:77], v[66:67], v[68:69]
	v_cvt_pk_bf16_f32 v66, v70, v71
	v_mul_f32_e32 v70, 0xbfb8aa3b, v63
	v_exp_f32_e32 v70, v70
	v_pk_mul_f32 v[72:73], v[78:79], v[72:73]
	v_lshl_add_u64 v[78:79], v[84:85], 0, v[114:115]
	v_cvt_pk_bf16_f32 v67, v72, v73
	v_cvt_pk_bf16_f32 v68, v74, v75
	v_cvt_pk_bf16_f32 v69, v76, v77
	v_add_f32_e32 v1, 1.0, v1
	global_store_dwordx4 v[78:79], v[66:69], off
	s_nop 1
	v_rcp_f32_e32 v66, v1
	v_add_f32_e32 v1, 1.0, v70
	v_rcp_f32_e32 v67, v1
	v_add_u32_e32 v1, 0x80, v134
	v_mad_i64_i32 v[68:69], s[12:13], v1, s49, v[136:137]
	v_mul_f32_e32 v1, 0xbfb8aa3b, v64
	v_pk_mul_f32 v[62:63], v[62:63], v[66:67]
	v_exp_f32_e32 v1, v1
	v_mul_f32_e32 v66, 0xbfb8aa3b, v65
	v_exp_f32_e32 v66, v66
	v_pk_mul_f32 v[54:55], v[62:63], v[54:55]
	v_add_f32_e32 v1, 1.0, v1
	v_rcp_f32_e32 v62, v1
	v_add_f32_e32 v1, 1.0, v66
	v_rcp_f32_e32 v63, v1
	v_mul_f32_e32 v1, 0xbfb8aa3b, v58
	v_exp_f32_e32 v1, v1
	v_mul_f32_e32 v66, 0xbfb8aa3b, v59
	v_exp_f32_e32 v66, v66
	v_pk_mul_f32 v[62:63], v[64:65], v[62:63]
	v_add_f32_e32 v1, 1.0, v1
	v_mul_f32_e32 v65, 0xbfb8aa3b, v60
	v_rcp_f32_e32 v64, v1
	v_add_f32_e32 v1, 1.0, v66
	v_exp_f32_e32 v66, v65
	v_mul_f32_e32 v65, 0xbfb8aa3b, v61
	v_exp_f32_e32 v67, v65
	v_rcp_f32_e32 v65, v1
	v_add_f32_e32 v1, 1.0, v66
	v_rcp_f32_e32 v66, v1
	v_add_f32_e32 v1, 1.0, v67
	v_rcp_f32_e32 v67, v1
	v_pk_mul_f32 v[58:59], v[58:59], v[64:65]
	v_mul_f32_e32 v1, 0xbfb8aa3b, v46
	v_pk_mul_f32 v[58:59], v[58:59], v[50:51]
	v_pk_mul_f32 v[50:51], v[60:61], v[66:67]
	v_exp_f32_e32 v1, v1
	v_pk_mul_f32 v[60:61], v[50:51], v[52:53]
	v_cvt_pk_bf16_f32 v50, v54, v55
	v_mul_f32_e32 v54, 0xbfb8aa3b, v47
	v_exp_f32_e32 v54, v54
	v_pk_mul_f32 v[56:57], v[62:63], v[56:57]
	v_lshl_add_u64 v[62:63], v[68:69], 0, v[114:115]
	v_cvt_pk_bf16_f32 v51, v56, v57
	v_cvt_pk_bf16_f32 v52, v58, v59
	v_cvt_pk_bf16_f32 v53, v60, v61
	v_add_f32_e32 v1, 1.0, v1
	global_store_dwordx4 v[62:63], v[50:53], off
	s_nop 1
	v_rcp_f32_e32 v50, v1
	v_add_f32_e32 v1, 1.0, v54
	v_rcp_f32_e32 v51, v1
	v_add_u32_e32 v1, 0x90, v134
	v_mad_i64_i32 v[52:53], s[12:13], v1, s49, v[136:137]
	v_mul_f32_e32 v1, 0xbfb8aa3b, v48
	v_pk_mul_f32 v[46:47], v[46:47], v[50:51]
	v_exp_f32_e32 v1, v1
	v_mul_f32_e32 v50, 0xbfb8aa3b, v49
	v_exp_f32_e32 v50, v50
	v_pk_mul_f32 v[38:39], v[46:47], v[38:39]
	v_add_f32_e32 v1, 1.0, v1
	v_rcp_f32_e32 v46, v1
	v_add_f32_e32 v1, 1.0, v50
	v_rcp_f32_e32 v47, v1
	v_mul_f32_e32 v1, 0xbfb8aa3b, v42
	v_exp_f32_e32 v1, v1
	v_mul_f32_e32 v50, 0xbfb8aa3b, v43
	v_exp_f32_e32 v50, v50
	v_pk_mul_f32 v[46:47], v[48:49], v[46:47]
	v_add_f32_e32 v1, 1.0, v1
	v_mul_f32_e32 v49, 0xbfb8aa3b, v44
	v_rcp_f32_e32 v48, v1
	v_add_f32_e32 v1, 1.0, v50
	v_exp_f32_e32 v50, v49
	v_mul_f32_e32 v49, 0xbfb8aa3b, v45
	v_exp_f32_e32 v51, v49
	v_rcp_f32_e32 v49, v1
	v_add_f32_e32 v1, 1.0, v50
	v_rcp_f32_e32 v50, v1
	v_add_f32_e32 v1, 1.0, v51
	v_rcp_f32_e32 v51, v1
	v_pk_mul_f32 v[42:43], v[42:43], v[48:49]
	v_mul_f32_e32 v1, 0xbfb8aa3b, v30
	v_pk_mul_f32 v[42:43], v[42:43], v[34:35]
	v_pk_mul_f32 v[34:35], v[44:45], v[50:51]
	v_exp_f32_e32 v1, v1
	v_pk_mul_f32 v[44:45], v[34:35], v[36:37]
	v_cvt_pk_bf16_f32 v34, v38, v39
	v_mul_f32_e32 v38, 0xbfb8aa3b, v31
	v_exp_f32_e32 v38, v38
	v_pk_mul_f32 v[40:41], v[46:47], v[40:41]
	v_lshl_add_u64 v[46:47], v[52:53], 0, v[114:115]
	v_cvt_pk_bf16_f32 v35, v40, v41
	v_cvt_pk_bf16_f32 v36, v42, v43
	v_cvt_pk_bf16_f32 v37, v44, v45
	v_add_f32_e32 v1, 1.0, v1
	global_store_dwordx4 v[46:47], v[34:37], off
	s_nop 1
	v_rcp_f32_e32 v34, v1
	v_add_f32_e32 v1, 1.0, v38
	v_rcp_f32_e32 v35, v1
	v_add_u32_e32 v1, 0xa0, v134
	v_mad_i64_i32 v[36:37], s[12:13], v1, s49, v[136:137]
	v_mul_f32_e32 v1, 0xbfb8aa3b, v32
	v_pk_mul_f32 v[30:31], v[30:31], v[34:35]
	v_exp_f32_e32 v1, v1
	v_mul_f32_e32 v34, 0xbfb8aa3b, v33
	v_exp_f32_e32 v34, v34
	v_pk_mul_f32 v[22:23], v[30:31], v[22:23]
	v_add_f32_e32 v1, 1.0, v1
	v_rcp_f32_e32 v30, v1
	v_add_f32_e32 v1, 1.0, v34
	v_rcp_f32_e32 v31, v1
	v_mul_f32_e32 v1, 0xbfb8aa3b, v26
	v_exp_f32_e32 v1, v1
	v_mul_f32_e32 v34, 0xbfb8aa3b, v27
	v_exp_f32_e32 v34, v34
	v_pk_mul_f32 v[30:31], v[32:33], v[30:31]
	v_add_f32_e32 v1, 1.0, v1
	v_mul_f32_e32 v33, 0xbfb8aa3b, v28
	v_rcp_f32_e32 v32, v1
	v_add_f32_e32 v1, 1.0, v34
	v_exp_f32_e32 v34, v33
	v_mul_f32_e32 v33, 0xbfb8aa3b, v29
	v_exp_f32_e32 v35, v33
	v_rcp_f32_e32 v33, v1
	v_add_f32_e32 v1, 1.0, v34
	v_rcp_f32_e32 v34, v1
	v_add_f32_e32 v1, 1.0, v35
	v_rcp_f32_e32 v35, v1
	v_pk_mul_f32 v[26:27], v[26:27], v[32:33]
	v_mul_f32_e32 v1, 0xbfb8aa3b, v14
	v_pk_mul_f32 v[26:27], v[26:27], v[18:19]
	v_pk_mul_f32 v[18:19], v[28:29], v[34:35]
	v_exp_f32_e32 v1, v1
	v_pk_mul_f32 v[28:29], v[18:19], v[20:21]
	v_cvt_pk_bf16_f32 v18, v22, v23
	v_mul_f32_e32 v22, 0xbfb8aa3b, v15
	v_exp_f32_e32 v22, v22
	v_pk_mul_f32 v[24:25], v[30:31], v[24:25]
	v_lshl_add_u64 v[30:31], v[36:37], 0, v[114:115]
	v_cvt_pk_bf16_f32 v19, v24, v25
	v_cvt_pk_bf16_f32 v20, v26, v27
	v_cvt_pk_bf16_f32 v21, v28, v29
	v_add_f32_e32 v1, 1.0, v1
	global_store_dwordx4 v[30:31], v[18:21], off
	s_nop 1
	v_rcp_f32_e32 v18, v1
	v_add_f32_e32 v1, 1.0, v22
	v_rcp_f32_e32 v19, v1
	v_add_u32_e32 v1, 0xb0, v134
	v_mad_i64_i32 v[20:21], s[12:13], v1, s49, v[136:137]
	v_mul_f32_e32 v1, 0xbfb8aa3b, v16
	v_pk_mul_f32 v[14:15], v[14:15], v[18:19]
	v_exp_f32_e32 v1, v1
	v_mul_f32_e32 v18, 0xbfb8aa3b, v17
	v_exp_f32_e32 v18, v18
	v_pk_mul_f32 v[6:7], v[14:15], v[6:7]
	v_add_f32_e32 v1, 1.0, v1
	v_rcp_f32_e32 v14, v1
	v_add_f32_e32 v1, 1.0, v18
	v_rcp_f32_e32 v15, v1
	v_mul_f32_e32 v1, 0xbfb8aa3b, v10
	v_exp_f32_e32 v1, v1
	v_mul_f32_e32 v18, 0xbfb8aa3b, v11
	v_exp_f32_e32 v18, v18
	v_pk_mul_f32 v[14:15], v[16:17], v[14:15]
	v_add_f32_e32 v1, 1.0, v1
	v_mul_f32_e32 v17, 0xbfb8aa3b, v12
	v_rcp_f32_e32 v16, v1
	v_add_f32_e32 v1, 1.0, v18
	v_exp_f32_e32 v18, v17
	v_mul_f32_e32 v17, 0xbfb8aa3b, v13
	v_exp_f32_e32 v19, v17
	v_rcp_f32_e32 v17, v1
	v_add_f32_e32 v1, 1.0, v18
	v_rcp_f32_e32 v18, v1
	v_add_f32_e32 v1, 1.0, v19
	v_rcp_f32_e32 v19, v1
	v_pk_mul_f32 v[10:11], v[10:11], v[16:17]
	v_pk_mul_f32 v[8:9], v[14:15], v[8:9]
	v_pk_mul_f32 v[10:11], v[10:11], v[2:3]
	v_pk_mul_f32 v[2:3], v[12:13], v[18:19]
	v_lshl_add_u64 v[14:15], v[20:21], 0, v[114:115]
	v_pk_mul_f32 v[12:13], v[2:3], v[4:5]
	v_cvt_pk_bf16_f32 v2, v6, v7
	v_cvt_pk_bf16_f32 v3, v8, v9
	v_cvt_pk_bf16_f32 v4, v10, v11
	v_cvt_pk_bf16_f32 v5, v12, v13
	v_mov_b32_e32 v137, v155
	v_mov_b32_e32 v136, v156
	s_mov_b64 s[12:13], s[10:11]
	s_mov_b32 s10, s54
	global_store_dwordx4 v[14:15], v[2:5], off
	s_cbranch_scc0 .LBB0_786
	s_waitcnt vmcnt(0)
	s_cmpk_gt_u32 s24, 0xff
	v_readlane_b32 s93, v254, 9
	s_cbranch_scc1 .LBB0_815
	s_barrier

.LBB0_916:
	s_add_u32 s14, s14, 0x30080
	s_addc_u32 s15, s15, 0
	s_add_u32 s65, s16, 0x100
	v_mov_b32_e32 v2, 0
	s_addc_u32 s66, s17, 0
	s_mov_b32 s67, -2
	ds_read_b128 v[148:151], v145
	ds_read_b128 v[152:155], v145 offset:1024
	ds_read_b128 v[156:159], v145 offset:2048
	ds_read_b128 v[160:163], v145 offset:3072
	s_add_u32 s16, s14, 0xfffd0080
	s_addc_u32 s17, s15, -1
	s_cmp_eq_u32 s67, 8
	s_cselect_b32 s19, s13, s17
	s_cselect_b32 s18, s12, s16
	s_cselect_b32 s17, s1, s66
	s_cselect_b32 s16, s0, s65
	v_lshl_add_u64 v[196:197], s[14:15], 0, v[138:139]
	s_add_i32 m0, s33, 0xc000
	ds_read_b128 v[164:167], v146
	ds_read_b128 v[168:171], v146 offset:1024
	ds_read_b128 v[172:175], v146 offset:2048
	ds_read_b128 v[176:179], v146 offset:3072
	ds_read_b128 v[180:183], v146 offset:4096
	ds_read_b128 v[184:187], v146 offset:5120
	ds_read_b128 v[188:191], v146 offset:6144
	ds_read_b128 v[192:195], v146 offset:7168
	global_load_lds_dwordx4 v[196:197], off
	v_lshl_add_u64 v[196:197], s[14:15], 0, v[140:141]
	s_add_i32 m0, s33, 0xe000
	s_nop 0
	global_load_lds_dwordx4 v[196:197], off
	s_waitcnt lgkmcnt(8)
	s_barrier
	s_waitcnt lgkmcnt(0)
	s_setprio 1
	s_waitcnt lgkmcnt(0)
	v_mfma_f32_16x16x32_bf16 v[126:129], v[148:151], v[164:167], 0
	v_mfma_f32_16x16x32_bf16 v[122:125], v[156:159], v[164:167], 0
	v_mfma_f32_16x16x32_bf16 v[118:121], v[148:151], v[172:175], 0
	v_mfma_f32_16x16x32_bf16 v[114:117], v[156:159], v[172:175], 0
	v_mfma_f32_16x16x32_bf16 v[102:105], v[148:151], v[180:183], 0
	v_mfma_f32_16x16x32_bf16 v[98:101], v[156:159], v[180:183], 0
	v_mfma_f32_16x16x32_bf16 v[86:89], v[148:151], v[188:191], 0
	v_mfma_f32_16x16x32_bf16 v[82:85], v[156:159], v[188:191], 0
	v_mfma_f32_16x16x32_bf16 v[126:129], v[152:155], v[168:171], v[126:129]
	v_mfma_f32_16x16x32_bf16 v[122:125], v[160:163], v[168:171], v[122:125]
	v_mfma_f32_16x16x32_bf16 v[118:121], v[152:155], v[176:179], v[118:121]
	v_mfma_f32_16x16x32_bf16 v[114:117], v[160:163], v[176:179], v[114:117]
	v_mfma_f32_16x16x32_bf16 v[102:105], v[152:155], v[184:187], v[102:105]
	v_mfma_f32_16x16x32_bf16 v[98:101], v[160:163], v[184:187], v[98:101]
	v_mfma_f32_16x16x32_bf16 v[86:89], v[152:155], v[192:195], v[86:89]
	v_mfma_f32_16x16x32_bf16 v[82:85], v[160:163], v[192:195], v[82:85]
	s_setprio 0
	s_barrier
	s_add_i32 s68, s55, s27
	v_lshl_add_u64 v[212:213], s[16:17], 0, v[134:135]
	s_mov_b32 m0, s68
	ds_read_b128 v[196:199], v147
	ds_read_b128 v[200:203], v147 offset:1024
	ds_read_b128 v[204:207], v147 offset:2048
	ds_read_b128 v[208:211], v147 offset:3072
	global_load_lds_dwordx4 v[212:213], off
	v_lshl_add_u64 v[214:215], s[16:17], 0, v[130:131]
	s_add_i32 m0, s68, 0x2000
	s_nop 0
	global_load_lds_dwordx4 v[214:215], off
	s_barrier
	s_waitcnt lgkmcnt(0)
	s_setprio 1
	s_waitcnt lgkmcnt(0)
	v_mfma_f32_16x16x32_bf16 v[110:113], v[196:199], v[164:167], 0
	v_mfma_f32_16x16x32_bf16 v[106:109], v[204:207], v[164:167], 0
	v_mfma_f32_16x16x32_bf16 v[94:97], v[196:199], v[172:175], 0
	v_mfma_f32_16x16x32_bf16 v[90:93], v[204:207], v[172:175], 0
	v_mfma_f32_16x16x32_bf16 v[78:81], v[196:199], v[180:183], 0
	v_mfma_f32_16x16x32_bf16 v[74:77], v[204:207], v[180:183], 0
	v_mfma_f32_16x16x32_bf16 v[70:73], v[196:199], v[188:191], 0
	v_mfma_f32_16x16x32_bf16 v[66:69], v[204:207], v[188:191], 0
	v_mfma_f32_16x16x32_bf16 v[110:113], v[200:203], v[168:171], v[110:113]
	v_mfma_f32_16x16x32_bf16 v[106:109], v[208:211], v[168:171], v[106:109]
	v_mfma_f32_16x16x32_bf16 v[94:97], v[200:203], v[176:179], v[94:97]
	v_mfma_f32_16x16x32_bf16 v[90:93], v[208:211], v[176:179], v[90:93]
	v_mfma_f32_16x16x32_bf16 v[78:81], v[200:203], v[184:187], v[78:81]
	v_mfma_f32_16x16x32_bf16 v[74:77], v[208:211], v[184:187], v[74:77]
	v_mfma_f32_16x16x32_bf16 v[70:73], v[200:203], v[192:195], v[70:73]
	v_mfma_f32_16x16x32_bf16 v[66:69], v[208:211], v[192:195], v[66:69]
	s_setprio 0
	s_mov_b32 m0, s33
	v_lshl_add_u64 v[216:217], s[18:19], 0, v[136:137]
	s_barrier
	ds_read_b128 v[164:167], v146 offset:16384
	ds_read_b128 v[168:171], v146 offset:17408
	ds_read_b128 v[172:175], v146 offset:18432
	ds_read_b128 v[176:179], v146 offset:19456
	ds_read_b128 v[180:183], v146 offset:20480
	ds_read_b128 v[184:187], v146 offset:21504
	ds_read_b128 v[188:191], v146 offset:22528
	ds_read_b128 v[192:195], v146 offset:23552
	global_load_lds_dwordx4 v[216:217], off
	v_lshl_add_u64 v[220:221], s[18:19], 0, v[132:133]
	s_mov_b32 m0, s34
	s_nop 0
	global_load_lds_dwordx4 v[220:221], off
	s_barrier
	s_waitcnt lgkmcnt(0)
	s_setprio 1
	s_waitcnt lgkmcnt(0)
	v_mfma_f32_16x16x32_bf16 v[62:65], v[148:151], v[164:167], 0
	v_mfma_f32_16x16x32_bf16 v[58:61], v[156:159], v[164:167], 0
	v_mfma_f32_16x16x32_bf16 v[54:57], v[148:151], v[172:175], 0
	v_mfma_f32_16x16x32_bf16 v[50:53], v[156:159], v[172:175], 0
	v_mfma_f32_16x16x32_bf16 v[38:41], v[148:151], v[180:183], 0
	v_mfma_f32_16x16x32_bf16 v[34:37], v[156:159], v[180:183], 0
	v_mfma_f32_16x16x32_bf16 v[22:25], v[148:151], v[188:191], 0
	v_mfma_f32_16x16x32_bf16 v[18:21], v[156:159], v[188:191], 0
	v_mfma_f32_16x16x32_bf16 v[62:65], v[152:155], v[168:171], v[62:65]
	v_mfma_f32_16x16x32_bf16 v[58:61], v[160:163], v[168:171], v[58:61]
	v_mfma_f32_16x16x32_bf16 v[54:57], v[152:155], v[176:179], v[54:57]
	v_mfma_f32_16x16x32_bf16 v[50:53], v[160:163], v[176:179], v[50:53]
	v_mfma_f32_16x16x32_bf16 v[38:41], v[152:155], v[184:187], v[38:41]
	v_mfma_f32_16x16x32_bf16 v[34:37], v[160:163], v[184:187], v[34:37]
	v_mfma_f32_16x16x32_bf16 v[22:25], v[152:155], v[192:195], v[22:25]
	v_mfma_f32_16x16x32_bf16 v[18:21], v[160:163], v[192:195], v[18:21]
	s_setprio 0
	s_barrier
	s_add_u32 s68, s16, 0x30000
	s_addc_u32 s69, s17, 0
	s_add_i32 s72, s56, s27
	v_lshl_add_u64 v[148:149], s[68:69], 0, v[134:135]
	s_mov_b32 m0, s72
	s_nop 0
	global_load_lds_dwordx4 v[148:149], off
	v_lshl_add_u64 v[148:149], s[68:69], 0, v[130:131]
	s_add_i32 m0, s72, 0x2000
	s_nop 0
	global_load_lds_dwordx4 v[148:149], off
	s_waitcnt vmcnt(6)
	s_barrier
	s_setprio 1
	v_mfma_f32_16x16x32_bf16 v[46:49], v[196:199], v[164:167], 0
	v_mfma_f32_16x16x32_bf16 v[42:45], v[204:207], v[164:167], 0
	v_mfma_f32_16x16x32_bf16 v[30:33], v[196:199], v[172:175], 0
	v_mfma_f32_16x16x32_bf16 v[26:29], v[204:207], v[172:175], 0
	v_mfma_f32_16x16x32_bf16 v[14:17], v[196:199], v[180:183], 0
	v_mfma_f32_16x16x32_bf16 v[10:13], v[204:207], v[180:183], 0
	v_mfma_f32_16x16x32_bf16 v[6:9], v[196:199], v[188:191], 0
	v_mfma_f32_16x16x32_bf16 v[2:5], v[204:207], v[188:191], 0
	v_mfma_f32_16x16x32_bf16 v[46:49], v[200:203], v[168:171], v[46:49]
	v_mfma_f32_16x16x32_bf16 v[42:45], v[208:211], v[168:171], v[42:45]
	v_mfma_f32_16x16x32_bf16 v[30:33], v[200:203], v[176:179], v[30:33]
	v_mfma_f32_16x16x32_bf16 v[26:29], v[208:211], v[176:179], v[26:29]
	v_mfma_f32_16x16x32_bf16 v[14:17], v[200:203], v[184:187], v[14:17]
	v_mfma_f32_16x16x32_bf16 v[10:13], v[208:211], v[184:187], v[10:13]
	v_mfma_f32_16x16x32_bf16 v[6:9], v[200:203], v[192:195], v[6:9]
	v_mfma_f32_16x16x32_bf16 v[2:5], v[208:211], v[192:195], v[2:5]
	s_setprio 0
	s_add_i32 s68, 0, 0x18000
	v_add_u32_e32 v1, s68, v143
	s_barrier
	ds_read_b128 v[148:151], v1
	ds_read_b128 v[152:155], v1 offset:1024
	ds_read_b128 v[156:159], v1 offset:2048
	ds_read_b128 v[160:163], v1 offset:3072
	s_add_u32 s18, s18, 0x30000
	s_addc_u32 s19, s19, 0
	s_mov_b32 m0, s35
	v_lshl_add_u64 v[196:197], s[18:19], 0, v[136:137]
	ds_read_b128 v[164:167], v146 offset:32768
	ds_read_b128 v[168:171], v146 offset:33792
	ds_read_b128 v[172:175], v146 offset:34816
	ds_read_b128 v[176:179], v146 offset:35840
	ds_read_b128 v[180:183], v146 offset:36864
	ds_read_b128 v[184:187], v146 offset:37888
	ds_read_b128 v[188:191], v146 offset:38912
	ds_read_b128 v[192:195], v146 offset:39936
	global_load_lds_dwordx4 v[196:197], off
	v_lshl_add_u64 v[196:197], s[18:19], 0, v[132:133]
	s_mov_b32 m0, s40
	s_nop 0
	global_load_lds_dwordx4 v[196:197], off
	s_waitcnt lgkmcnt(8)
	s_barrier
	s_waitcnt lgkmcnt(0)
	s_setprio 1
	s_waitcnt lgkmcnt(0)
	v_mfma_f32_16x16x32_bf16 v[126:129], v[148:151], v[164:167], v[126:129]
	v_mfma_f32_16x16x32_bf16 v[122:125], v[156:159], v[164:167], v[122:125]
	v_mfma_f32_16x16x32_bf16 v[118:121], v[148:151], v[172:175], v[118:121]
	v_mfma_f32_16x16x32_bf16 v[114:117], v[156:159], v[172:175], v[114:117]
	v_mfma_f32_16x16x32_bf16 v[102:105], v[148:151], v[180:183], v[102:105]
	v_mfma_f32_16x16x32_bf16 v[98:101], v[156:159], v[180:183], v[98:101]
	v_mfma_f32_16x16x32_bf16 v[86:89], v[148:151], v[188:191], v[86:89]
	v_mfma_f32_16x16x32_bf16 v[82:85], v[156:159], v[188:191], v[82:85]
	v_mfma_f32_16x16x32_bf16 v[126:129], v[152:155], v[168:171], v[126:129]
	v_mfma_f32_16x16x32_bf16 v[122:125], v[160:163], v[168:171], v[122:125]
	v_mfma_f32_16x16x32_bf16 v[118:121], v[152:155], v[176:179], v[118:121]
	v_mfma_f32_16x16x32_bf16 v[114:117], v[160:163], v[176:179], v[114:117]
	v_mfma_f32_16x16x32_bf16 v[102:105], v[152:155], v[184:187], v[102:105]
	v_mfma_f32_16x16x32_bf16 v[98:101], v[160:163], v[184:187], v[98:101]
	v_mfma_f32_16x16x32_bf16 v[86:89], v[152:155], v[192:195], v[86:89]
	v_mfma_f32_16x16x32_bf16 v[82:85], v[160:163], v[192:195], v[82:85]
	s_setprio 0
	s_barrier
	s_add_i32 s18, 0, 0x1c000
	s_add_i32 s19, s68, s27
	v_add_u32_e32 v1, s18, v143
	v_lshl_add_u64 v[212:213], v[212:213], 0, s[6:7]
	s_mov_b32 m0, s19
	ds_read_b128 v[196:199], v1
	ds_read_b128 v[200:203], v1 offset:1024
	ds_read_b128 v[204:207], v1 offset:2048
	ds_read_b128 v[208:211], v1 offset:3072
	global_load_lds_dwordx4 v[212:213], off
	v_lshl_add_u64 v[212:213], v[214:215], 0, s[6:7]
	s_add_i32 m0, s19, 0x2000
	s_nop 0
	global_load_lds_dwordx4 v[212:213], off
	s_barrier
	s_waitcnt lgkmcnt(0)
	s_setprio 1
	s_waitcnt lgkmcnt(0)
	v_mfma_f32_16x16x32_bf16 v[110:113], v[196:199], v[164:167], v[110:113]
	v_mfma_f32_16x16x32_bf16 v[106:109], v[204:207], v[164:167], v[106:109]
	v_mfma_f32_16x16x32_bf16 v[94:97], v[196:199], v[172:175], v[94:97]
	v_mfma_f32_16x16x32_bf16 v[90:93], v[204:207], v[172:175], v[90:93]
	v_mfma_f32_16x16x32_bf16 v[78:81], v[196:199], v[180:183], v[78:81]
	v_mfma_f32_16x16x32_bf16 v[74:77], v[204:207], v[180:183], v[74:77]
	v_mfma_f32_16x16x32_bf16 v[70:73], v[196:199], v[188:191], v[70:73]
	v_mfma_f32_16x16x32_bf16 v[66:69], v[204:207], v[188:191], v[66:69]
	v_mfma_f32_16x16x32_bf16 v[110:113], v[200:203], v[168:171], v[110:113]
	v_mfma_f32_16x16x32_bf16 v[106:109], v[208:211], v[168:171], v[106:109]
	v_mfma_f32_16x16x32_bf16 v[94:97], v[200:203], v[176:179], v[94:97]
	v_mfma_f32_16x16x32_bf16 v[90:93], v[208:211], v[176:179], v[90:93]
	v_mfma_f32_16x16x32_bf16 v[78:81], v[200:203], v[184:187], v[78:81]
	v_mfma_f32_16x16x32_bf16 v[74:77], v[208:211], v[184:187], v[74:77]
	v_mfma_f32_16x16x32_bf16 v[70:73], v[200:203], v[192:195], v[70:73]
	v_mfma_f32_16x16x32_bf16 v[66:69], v[208:211], v[192:195], v[66:69]
	s_setprio 0
	s_mov_b32 m0, s41
	v_lshl_add_u64 v[212:213], v[216:217], 0, s[6:7]
	s_barrier
	ds_read_b128 v[164:167], v146 offset:49152
	ds_read_b128 v[168:171], v146 offset:50176
	ds_read_b128 v[172:175], v146 offset:51200
	ds_read_b128 v[176:179], v146 offset:52224
	ds_read_b128 v[180:183], v146 offset:53248
	ds_read_b128 v[184:187], v146 offset:54272
	ds_read_b128 v[188:191], v146 offset:55296
	ds_read_b128 v[192:195], v146 offset:56320
	global_load_lds_dwordx4 v[212:213], off
	v_lshl_add_u64 v[212:213], v[220:221], 0, s[6:7]
	s_mov_b32 m0, s54
	s_nop 0
	global_load_lds_dwordx4 v[212:213], off
	s_barrier
	s_waitcnt lgkmcnt(0)
	s_setprio 1
	s_waitcnt lgkmcnt(0)
	v_mfma_f32_16x16x32_bf16 v[62:65], v[148:151], v[164:167], v[62:65]
	v_mfma_f32_16x16x32_bf16 v[58:61], v[156:159], v[164:167], v[58:61]
	v_mfma_f32_16x16x32_bf16 v[54:57], v[148:151], v[172:175], v[54:57]
	v_mfma_f32_16x16x32_bf16 v[50:53], v[156:159], v[172:175], v[50:53]
	v_mfma_f32_16x16x32_bf16 v[38:41], v[148:151], v[180:183], v[38:41]
	v_mfma_f32_16x16x32_bf16 v[34:37], v[156:159], v[180:183], v[34:37]
	v_mfma_f32_16x16x32_bf16 v[22:25], v[148:151], v[188:191], v[22:25]
	v_mfma_f32_16x16x32_bf16 v[18:21], v[156:159], v[188:191], v[18:21]
	v_mfma_f32_16x16x32_bf16 v[62:65], v[152:155], v[168:171], v[62:65]
	v_mfma_f32_16x16x32_bf16 v[58:61], v[160:163], v[168:171], v[58:61]
	v_mfma_f32_16x16x32_bf16 v[54:57], v[152:155], v[176:179], v[54:57]
	v_mfma_f32_16x16x32_bf16 v[50:53], v[160:163], v[176:179], v[50:53]
	v_mfma_f32_16x16x32_bf16 v[38:41], v[152:155], v[184:187], v[38:41]
	v_mfma_f32_16x16x32_bf16 v[34:37], v[160:163], v[184:187], v[34:37]
	v_mfma_f32_16x16x32_bf16 v[22:25], v[152:155], v[192:195], v[22:25]
	v_mfma_f32_16x16x32_bf16 v[18:21], v[160:163], v[192:195], v[18:21]
	s_setprio 0
	s_barrier
	s_add_u32 s16, s16, 0x30080
	s_addc_u32 s17, s17, 0
	s_add_i32 s18, s18, s27
	v_lshl_add_u64 v[148:149], s[16:17], 0, v[134:135]
	s_mov_b32 m0, s18
	s_nop 0
	global_load_lds_dwordx4 v[148:149], off
	v_lshl_add_u64 v[148:149], s[16:17], 0, v[130:131]
	s_add_i32 m0, s18, 0x2000
	s_nop 0
	global_load_lds_dwordx4 v[148:149], off
	s_waitcnt vmcnt(6)
	s_barrier
	s_setprio 1
	v_mfma_f32_16x16x32_bf16 v[46:49], v[196:199], v[164:167], v[46:49]
	v_mfma_f32_16x16x32_bf16 v[42:45], v[204:207], v[164:167], v[42:45]
	v_mfma_f32_16x16x32_bf16 v[30:33], v[196:199], v[172:175], v[30:33]
	v_mfma_f32_16x16x32_bf16 v[26:29], v[204:207], v[172:175], v[26:29]
	v_mfma_f32_16x16x32_bf16 v[14:17], v[196:199], v[180:183], v[14:17]
	v_mfma_f32_16x16x32_bf16 v[10:13], v[204:207], v[180:183], v[10:13]
	v_mfma_f32_16x16x32_bf16 v[6:9], v[196:199], v[188:191], v[6:9]
	v_mfma_f32_16x16x32_bf16 v[2:5], v[204:207], v[188:191], v[2:5]
	v_mfma_f32_16x16x32_bf16 v[46:49], v[200:203], v[168:171], v[46:49]
	v_mfma_f32_16x16x32_bf16 v[42:45], v[208:211], v[168:171], v[42:45]
	v_mfma_f32_16x16x32_bf16 v[30:33], v[200:203], v[176:179], v[30:33]
	v_mfma_f32_16x16x32_bf16 v[26:29], v[208:211], v[176:179], v[26:29]
	v_mfma_f32_16x16x32_bf16 v[14:17], v[200:203], v[184:187], v[14:17]
	v_mfma_f32_16x16x32_bf16 v[10:13], v[208:211], v[184:187], v[10:13]
	v_mfma_f32_16x16x32_bf16 v[6:9], v[200:203], v[192:195], v[6:9]
	v_mfma_f32_16x16x32_bf16 v[2:5], v[208:211], v[192:195], v[2:5]
	s_setprio 0
	s_add_i32 s67, s67, 2
	s_add_u32 s14, s14, 0x100
	s_addc_u32 s15, s15, 0
	s_add_u32 s65, s65, 0x100
	s_addc_u32 s66, s66, 0
	s_cmp_gt_u32 s67, 9
	s_barrier
	s_cbranch_scc1 .Lpeel_917_after

.Lpeel_917_after:
	v_lshl_add_u32 v148, s60, 8, v142
	v_lshl_or_b32 v150, s61, 8, v144
	v_ashrrev_i32_e32 v149, 31, v148
	v_ashrrev_i32_e32 v151, 31, v150
	v_lshlrev_b64 v[152:153], 12, v[148:149]
	v_lshl_add_u64 v[152:153], s[48:49], 0, v[152:153]
	v_lshlrev_b64 v[150:151], 1, v[150:151]
	v_lshl_add_u64 v[152:153], v[152:153], 0, v[150:151]
	s_mov_b64 s[14:15], 0x80000
	v_cvt_pk_bf16_f32 v70, v70, v71
	v_cvt_pk_bf16_f32 v71, v72, v73
	v_cvt_pk_bf16_f32 v72, v66, v67
	v_lshl_add_u64 v[66:67], v[152:153], 0, s[14:15]
	s_mov_b32 s14, 0x80000
	v_cvt_pk_bf16_f32 v62, v62, v63
	v_cvt_pk_bf16_f32 v63, v64, v65
	v_cvt_pk_bf16_f32 v64, v58, v59
	v_add_co_u32_e32 v58, vcc, s14, v152
	v_cvt_pk_bf16_f32 v46, v46, v47
	v_cvt_pk_bf16_f32 v47, v48, v49
	v_cvt_pk_bf16_f32 v48, v42, v43
	v_cvt_pk_bf16_f32 v49, v44, v45
	s_mov_b64 s[14:15], 0x90000
	v_cvt_pk_bf16_f32 v110, v110, v111
	v_cvt_pk_bf16_f32 v111, v112, v113
	v_cvt_pk_bf16_f32 v112, v106, v107
	v_or_b32_e32 v106, 16, v148
	v_addc_co_u32_e32 v59, vcc, 0, v153, vcc
	global_store_dwordx4 v[66:67], v[46:49], off offset:256
	v_ashrrev_i32_e32 v107, 31, v106
	v_cvt_pk_bf16_f32 v94, v94, v95
	v_lshl_add_u64 v[46:47], v[152:153], 0, s[14:15]
	s_mov_b32 s14, 0x90000
	v_cvt_pk_bf16_f32 v95, v96, v97
	v_cvt_pk_bf16_f32 v96, v90, v91
	v_or_b32_e32 v90, 32, v148
	v_add_co_u32_e32 v48, vcc, s14, v152
	v_lshlrev_b64 v[106:107], 12, v[106:107]
	v_ashrrev_i32_e32 v91, 31, v90
	v_cvt_pk_bf16_f32 v78, v78, v79
	v_cvt_pk_bf16_f32 v79, v80, v81
	v_cvt_pk_bf16_f32 v80, v74, v75
	v_or_b32_e32 v74, 48, v148
	v_addc_co_u32_e32 v49, vcc, 0, v153, vcc
	v_cvt_pk_bf16_f32 v30, v30, v31
	v_cvt_pk_bf16_f32 v31, v32, v33
	v_cvt_pk_bf16_f32 v32, v26, v27
	v_cvt_pk_bf16_f32 v33, v28, v29
	v_cvt_pk_bf16_f32 v113, v108, v109
	v_lshl_add_u64 v[106:107], s[48:49], 0, v[106:107]
	v_lshlrev_b64 v[90:91], 12, v[90:91]
	v_ashrrev_i32_e32 v75, 31, v74
	global_store_dwordx4 v[46:47], v[30:33], off offset:256
	global_store_dwordx4 v[152:153], v[110:113], off offset:256
	v_cvt_pk_bf16_f32 v97, v92, v93
	v_add_co_u32_e32 v32, vcc, s57, v152
	v_lshl_add_u64 v[110:111], v[106:107], 0, v[150:151]
	v_lshl_add_u64 v[90:91], s[48:49], 0, v[90:91]
	v_lshlrev_b64 v[74:75], 12, v[74:75]
	v_lshl_add_u64 v[30:31], v[152:153], 0, s[8:9]
	v_addc_co_u32_e32 v33, vcc, 0, v153, vcc
	v_cvt_pk_bf16_f32 v14, v14, v15
	v_cvt_pk_bf16_f32 v15, v16, v17
	v_cvt_pk_bf16_f32 v16, v10, v11
	v_cvt_pk_bf16_f32 v17, v12, v13
	global_store_dwordx4 v[110:111], v[94:97], off offset:256
	v_cvt_pk_bf16_f32 v81, v76, v77
	v_lshl_add_u64 v[74:75], s[48:49], 0, v[74:75]
	v_lshl_add_u64 v[94:95], v[90:91], 0, v[150:151]
	global_store_dwordx4 v[30:31], v[14:17], off offset:256
	v_cvt_pk_bf16_f32 v126, v126, v127
	v_cvt_pk_bf16_f32 v127, v128, v129
	v_add_co_u32_e32 v16, vcc, s58, v152
	v_cvt_pk_bf16_f32 v128, v122, v123
	v_cvt_pk_bf16_f32 v129, v124, v125
	v_cvt_pk_bf16_f32 v106, v118, v119
	v_cvt_pk_bf16_f32 v107, v120, v121
	v_cvt_pk_bf16_f32 v108, v114, v115
	v_cvt_pk_bf16_f32 v109, v116, v117
	v_cvt_pk_bf16_f32 v90, v102, v103
	v_cvt_pk_bf16_f32 v91, v104, v105
	v_cvt_pk_bf16_f32 v92, v98, v99
	v_cvt_pk_bf16_f32 v93, v100, v101
	global_store_dwordx4 v[94:95], v[78:81], off offset:256
	v_cvt_pk_bf16_f32 v76, v82, v83
	v_cvt_pk_bf16_f32 v77, v84, v85
	v_lshl_add_u64 v[78:79], v[74:75], 0, v[150:151]
	v_cvt_pk_bf16_f32 v74, v86, v87
	v_cvt_pk_bf16_f32 v75, v88, v89
	v_cvt_pk_bf16_f32 v73, v68, v69
	v_cvt_pk_bf16_f32 v65, v60, v61
	v_cvt_pk_bf16_f32 v42, v54, v55
	v_cvt_pk_bf16_f32 v43, v56, v57
	v_cvt_pk_bf16_f32 v44, v50, v51
	v_cvt_pk_bf16_f32 v45, v52, v53
	v_cvt_pk_bf16_f32 v26, v38, v39
	v_cvt_pk_bf16_f32 v27, v40, v41
	v_cvt_pk_bf16_f32 v28, v34, v35
	v_cvt_pk_bf16_f32 v29, v36, v37
	v_lshl_add_u64 v[14:15], v[152:153], 0, s[10:11]
	v_cvt_pk_bf16_f32 v10, v22, v23
	v_cvt_pk_bf16_f32 v11, v24, v25
	v_cvt_pk_bf16_f32 v12, v18, v19
	v_cvt_pk_bf16_f32 v13, v20, v21
	v_addc_co_u32_e32 v17, vcc, 0, v153, vcc
	v_cvt_pk_bf16_f32 v6, v6, v7
	v_cvt_pk_bf16_f32 v7, v8, v9
	v_cvt_pk_bf16_f32 v8, v2, v3
	v_cvt_pk_bf16_f32 v9, v4, v5
	s_cmp_eq_u32 s59, s23
	s_mov_b32 s61, s63
	s_mov_b32 s60, s62
	s_mov_b64 s[16:17], s[0:1]
	s_mov_b64 s[14:15], s[12:13]
	s_mov_b32 s18, s59
	global_store_dwordx4 v[152:153], v[126:129], off
	global_store_dwordx4 v[110:111], v[106:109], off
	global_store_dwordx4 v[94:95], v[90:93], off
	global_store_dwordx4 v[78:79], v[74:77], off
	global_store_dwordx4 v[78:79], v[70:73], off offset:256
	global_store_dwordx4 v[58:59], v[62:65], off
	global_store_dwordx4 v[48:49], v[42:45], off
	global_store_dwordx4 v[32:33], v[26:29], off
	global_store_dwordx4 v[16:17], v[10:13], off
	global_store_dwordx4 v[14:15], v[6:9], off offset:256
	s_cbranch_scc0 .LBB0_890
	s_waitcnt vmcnt(0)
	s_cmpk_gt_u32 s26, 0xff
	v_readlane_b32 s93, v254, 9
	s_cbranch_scc1 .LBB0_921
	s_barrier

.LBB0_1036:
	v_mov_b64_e32 v[2:3], 0x600
	s_ashr_i32 s17, s16, 31
	v_cmp_lt_i64_e32 vcc, s[18:19], v[2:3]
	s_lshl_b64 s[18:19], s[16:17], 20
	s_add_u32 s18, s36, s18
	s_addc_u32 s19, s37, s19
	s_and_b64 s[20:21], vcc, exec
	s_cselect_b32 s17, s19, s5
	s_cselect_b32 s63, s18, s4
	s_ashr_i32 s15, s14, 31
	s_lshl_b64 s[20:21], s[14:15], 20
	v_readlane_b32 s54, v254, 30
	v_readlane_b32 s55, v254, 31
	s_add_u32 s20, s54, s20
	s_addc_u32 s21, s55, s21
	s_and_b64 s[54:55], vcc, exec
	s_cselect_b32 s15, s21, s9
	s_cselect_b32 s64, s20, s8
	s_add_u32 s4, s4, 0x80080
	s_addc_u32 s5, s5, 0
	s_add_u32 s65, s8, 0x100
	v_mov_b32_e32 v2, 0
	s_addc_u32 s66, s9, 0
	s_mov_b32 s67, -2
	s_waitcnt vmcnt(0)
	ds_read_b128 v[130:133], v192
	ds_read_b128 v[134:137], v192 offset:1024
	ds_read_b128 v[200:203], v192 offset:2048
	ds_read_b128 v[204:207], v192 offset:3072
	s_add_u32 s8, s4, 0xfff80080
	s_addc_u32 s9, s5, -1
	s_cmp_eq_u32 s67, 28
	s_cselect_b32 s55, s17, s9
	s_cselect_b32 s54, s63, s8
	s_cselect_b32 s9, s15, s66
	s_cselect_b32 s8, s64, s65
	v_lshl_add_u64 v[150:151], s[4:5], 0, v[146:147]
	s_add_i32 m0, s23, 0xc000
	ds_read_b128 v[208:211], v193
	ds_read_b128 v[212:215], v193 offset:1024
	ds_read_b128 v[220:223], v193 offset:2048
	ds_read_b128 v[224:227], v193 offset:3072
	ds_read_b128 v[228:231], v193 offset:4096
	ds_read_b128 v[232:235], v193 offset:5120
	ds_read_b128 v[236:239], v193 offset:6144
	ds_read_b128 v[240:243], v193 offset:7168
	global_load_lds_dwordx4 v[150:151], off
	v_lshl_add_u64 v[150:151], s[4:5], 0, v[148:149]
	s_add_i32 m0, s23, 0xe000
	s_nop 0
	global_load_lds_dwordx4 v[150:151], off
	s_waitcnt lgkmcnt(8)
	s_barrier
	s_waitcnt lgkmcnt(0)
	s_setprio 1
	s_waitcnt lgkmcnt(0)
	v_mfma_f32_16x16x32_bf16 v[126:129], v[130:133], v[208:211], 0
	v_mfma_f32_16x16x32_bf16 v[122:125], v[200:203], v[208:211], 0
	v_mfma_f32_16x16x32_bf16 v[110:113], v[130:133], v[220:223], 0
	v_mfma_f32_16x16x32_bf16 v[106:109], v[200:203], v[220:223], 0
	v_mfma_f32_16x16x32_bf16 v[94:97], v[130:133], v[228:231], 0
	v_mfma_f32_16x16x32_bf16 v[90:93], v[200:203], v[228:231], 0
	v_mfma_f32_16x16x32_bf16 v[78:81], v[130:133], v[236:239], 0
	v_mfma_f32_16x16x32_bf16 v[74:77], v[200:203], v[236:239], 0
	v_mfma_f32_16x16x32_bf16 v[126:129], v[134:137], v[212:215], v[126:129]
	v_mfma_f32_16x16x32_bf16 v[122:125], v[204:207], v[212:215], v[122:125]
	v_mfma_f32_16x16x32_bf16 v[110:113], v[134:137], v[224:227], v[110:113]
	v_mfma_f32_16x16x32_bf16 v[106:109], v[204:207], v[224:227], v[106:109]
	v_mfma_f32_16x16x32_bf16 v[94:97], v[134:137], v[232:235], v[94:97]
	v_mfma_f32_16x16x32_bf16 v[90:93], v[204:207], v[232:235], v[90:93]
	v_mfma_f32_16x16x32_bf16 v[78:81], v[134:137], v[240:243], v[78:81]
	v_mfma_f32_16x16x32_bf16 v[74:77], v[204:207], v[240:243], v[74:77]
	s_setprio 0
	s_barrier
	s_add_i32 s68, s58, s3
	v_lshl_add_u64 v[186:187], s[8:9], 0, v[140:141]
	s_mov_b32 m0, s68
	ds_read_b128 v[244:247], v194
	ds_read_b128 v[248:251], v194 offset:1024
	ds_read_b128 v[150:153], v194 offset:2048
	ds_read_b128 v[176:179], v194 offset:3072
	global_load_lds_dwordx4 v[186:187], off
	v_lshl_add_u64 v[216:217], s[8:9], 0, v[144:145]
	s_add_i32 m0, s68, 0x2000
	s_nop 0
	global_load_lds_dwordx4 v[216:217], off
	s_barrier
	s_waitcnt lgkmcnt(0)
	s_setprio 1
	s_waitcnt lgkmcnt(0)
	v_mfma_f32_16x16x32_bf16 v[118:121], v[244:247], v[208:211], 0
	v_mfma_f32_16x16x32_bf16 v[114:117], v[150:153], v[208:211], 0
	v_mfma_f32_16x16x32_bf16 v[102:105], v[244:247], v[220:223], 0
	v_mfma_f32_16x16x32_bf16 v[98:101], v[150:153], v[220:223], 0
	v_mfma_f32_16x16x32_bf16 v[86:89], v[244:247], v[228:231], 0
	v_mfma_f32_16x16x32_bf16 v[82:85], v[150:153], v[228:231], 0
	v_mfma_f32_16x16x32_bf16 v[70:73], v[244:247], v[236:239], 0
	v_mfma_f32_16x16x32_bf16 v[66:69], v[150:153], v[236:239], 0
	v_mfma_f32_16x16x32_bf16 v[118:121], v[248:251], v[212:215], v[118:121]
	v_mfma_f32_16x16x32_bf16 v[114:117], v[176:179], v[212:215], v[114:117]
	v_mfma_f32_16x16x32_bf16 v[102:105], v[248:251], v[224:227], v[102:105]
	v_mfma_f32_16x16x32_bf16 v[98:101], v[176:179], v[224:227], v[98:101]
	v_mfma_f32_16x16x32_bf16 v[86:89], v[248:251], v[232:235], v[86:89]
	v_mfma_f32_16x16x32_bf16 v[82:85], v[176:179], v[232:235], v[82:85]
	v_mfma_f32_16x16x32_bf16 v[70:73], v[248:251], v[240:243], v[70:73]
	v_mfma_f32_16x16x32_bf16 v[66:69], v[176:179], v[240:243], v[66:69]
	s_setprio 0
	s_mov_b32 m0, s23
	v_lshl_add_u64 v[252:253], s[54:55], 0, v[138:139]
	s_barrier
	ds_read_b128 v[208:211], v193 offset:16384
	ds_read_b128 v[212:215], v193 offset:17408
	ds_read_b128 v[220:223], v193 offset:18432
	ds_read_b128 v[224:227], v193 offset:19456
	ds_read_b128 v[228:231], v193 offset:20480
	ds_read_b128 v[232:235], v193 offset:21504
	ds_read_b128 v[236:239], v193 offset:22528
	ds_read_b128 v[240:243], v193 offset:23552
	global_load_lds_dwordx4 v[252:253], off
	v_lshl_add_u64 v[160:161], s[54:55], 0, v[142:143]
	s_mov_b32 m0, s25
	s_nop 0
	global_load_lds_dwordx4 v[160:161], off
	s_barrier
	s_waitcnt lgkmcnt(0)
	s_setprio 1
	s_waitcnt lgkmcnt(0)
	v_mfma_f32_16x16x32_bf16 v[62:65], v[130:133], v[208:211], 0
	v_mfma_f32_16x16x32_bf16 v[58:61], v[200:203], v[208:211], 0
	v_mfma_f32_16x16x32_bf16 v[46:49], v[130:133], v[220:223], 0
	v_mfma_f32_16x16x32_bf16 v[42:45], v[200:203], v[220:223], 0
	v_mfma_f32_16x16x32_bf16 v[30:33], v[130:133], v[228:231], 0
	v_mfma_f32_16x16x32_bf16 v[26:29], v[200:203], v[228:231], 0
	v_mfma_f32_16x16x32_bf16 v[14:17], v[130:133], v[236:239], 0
	v_mfma_f32_16x16x32_bf16 v[10:13], v[200:203], v[236:239], 0
	v_mfma_f32_16x16x32_bf16 v[62:65], v[134:137], v[212:215], v[62:65]
	v_mfma_f32_16x16x32_bf16 v[58:61], v[204:207], v[212:215], v[58:61]
	v_mfma_f32_16x16x32_bf16 v[46:49], v[134:137], v[224:227], v[46:49]
	v_mfma_f32_16x16x32_bf16 v[42:45], v[204:207], v[224:227], v[42:45]
	v_mfma_f32_16x16x32_bf16 v[30:33], v[134:137], v[232:235], v[30:33]
	v_mfma_f32_16x16x32_bf16 v[26:29], v[204:207], v[232:235], v[26:29]
	v_mfma_f32_16x16x32_bf16 v[14:17], v[134:137], v[240:243], v[14:17]
	v_mfma_f32_16x16x32_bf16 v[10:13], v[204:207], v[240:243], v[10:13]
	s_setprio 0
	s_barrier
	s_add_u32 s68, s8, 0x80000
	s_addc_u32 s69, s9, 0
	s_add_i32 s72, s59, s3
	v_lshl_add_u64 v[130:131], s[68:69], 0, v[140:141]
	s_mov_b32 m0, s72
	s_nop 0
	global_load_lds_dwordx4 v[130:131], off
	v_lshl_add_u64 v[130:131], s[68:69], 0, v[144:145]
	s_add_i32 m0, s72, 0x2000
	s_nop 0
	global_load_lds_dwordx4 v[130:131], off
	s_waitcnt vmcnt(6)
	s_barrier
	s_setprio 1
	v_mfma_f32_16x16x32_bf16 v[54:57], v[244:247], v[208:211], 0
	v_mfma_f32_16x16x32_bf16 v[50:53], v[150:153], v[208:211], 0
	v_mfma_f32_16x16x32_bf16 v[38:41], v[244:247], v[220:223], 0
	v_mfma_f32_16x16x32_bf16 v[34:37], v[150:153], v[220:223], 0
	v_mfma_f32_16x16x32_bf16 v[22:25], v[244:247], v[228:231], 0
	v_mfma_f32_16x16x32_bf16 v[18:21], v[150:153], v[228:231], 0
	v_mfma_f32_16x16x32_bf16 v[6:9], v[244:247], v[236:239], 0
	v_mfma_f32_16x16x32_bf16 v[2:5], v[150:153], v[236:239], 0
	v_mfma_f32_16x16x32_bf16 v[54:57], v[248:251], v[212:215], v[54:57]
	v_mfma_f32_16x16x32_bf16 v[50:53], v[176:179], v[212:215], v[50:53]
	v_mfma_f32_16x16x32_bf16 v[38:41], v[248:251], v[224:227], v[38:41]
	v_mfma_f32_16x16x32_bf16 v[34:37], v[176:179], v[224:227], v[34:37]
	v_mfma_f32_16x16x32_bf16 v[22:25], v[248:251], v[232:235], v[22:25]
	v_mfma_f32_16x16x32_bf16 v[18:21], v[176:179], v[232:235], v[18:21]
	v_mfma_f32_16x16x32_bf16 v[6:9], v[248:251], v[240:243], v[6:9]
	v_mfma_f32_16x16x32_bf16 v[2:5], v[176:179], v[240:243], v[2:5]
	s_setprio 0
	s_add_i32 s68, 0, 0x18000
	v_add_u32_e32 v154, s68, v157
	s_barrier
	ds_read_b128 v[130:133], v154
	ds_read_b128 v[134:137], v154 offset:1024
	ds_read_b128 v[150:153], v154 offset:2048
	ds_read_b128 v[176:179], v154 offset:3072
	s_add_u32 s54, s54, 0x80000
	s_addc_u32 s55, s55, 0
	s_mov_b32 m0, s26
	v_lshl_add_u64 v[236:237], s[54:55], 0, v[138:139]
	ds_read_b128 v[200:203], v193 offset:32768
	ds_read_b128 v[204:207], v193 offset:33792
	ds_read_b128 v[208:211], v193 offset:34816
	ds_read_b128 v[212:215], v193 offset:35840
	ds_read_b128 v[220:223], v193 offset:36864
	ds_read_b128 v[224:227], v193 offset:37888
	ds_read_b128 v[228:231], v193 offset:38912
	ds_read_b128 v[232:235], v193 offset:39936
	global_load_lds_dwordx4 v[236:237], off
	v_lshl_add_u64 v[236:237], s[54:55], 0, v[142:143]
	s_mov_b32 m0, s33
	s_nop 0
	global_load_lds_dwordx4 v[236:237], off
	s_waitcnt lgkmcnt(8)
	s_barrier
	s_waitcnt lgkmcnt(0)
	s_setprio 1
	s_waitcnt lgkmcnt(0)
	v_mfma_f32_16x16x32_bf16 v[126:129], v[130:133], v[200:203], v[126:129]
	v_mfma_f32_16x16x32_bf16 v[122:125], v[150:153], v[200:203], v[122:125]
	v_mfma_f32_16x16x32_bf16 v[110:113], v[130:133], v[208:211], v[110:113]
	v_mfma_f32_16x16x32_bf16 v[106:109], v[150:153], v[208:211], v[106:109]
	v_mfma_f32_16x16x32_bf16 v[94:97], v[130:133], v[220:223], v[94:97]
	v_mfma_f32_16x16x32_bf16 v[90:93], v[150:153], v[220:223], v[90:93]
	v_mfma_f32_16x16x32_bf16 v[78:81], v[130:133], v[228:231], v[78:81]
	v_mfma_f32_16x16x32_bf16 v[74:77], v[150:153], v[228:231], v[74:77]
	v_mfma_f32_16x16x32_bf16 v[126:129], v[134:137], v[204:207], v[126:129]
	v_mfma_f32_16x16x32_bf16 v[122:125], v[176:179], v[204:207], v[122:125]
	v_mfma_f32_16x16x32_bf16 v[110:113], v[134:137], v[212:215], v[110:113]
	v_mfma_f32_16x16x32_bf16 v[106:109], v[176:179], v[212:215], v[106:109]
	v_mfma_f32_16x16x32_bf16 v[94:97], v[134:137], v[224:227], v[94:97]
	v_mfma_f32_16x16x32_bf16 v[90:93], v[176:179], v[224:227], v[90:93]
	v_mfma_f32_16x16x32_bf16 v[78:81], v[134:137], v[232:235], v[78:81]
	v_mfma_f32_16x16x32_bf16 v[74:77], v[176:179], v[232:235], v[74:77]
	s_setprio 0
	s_barrier
	s_add_i32 s54, 0, 0x1c000
	s_add_i32 s55, s68, s3
	v_add_u32_e32 v154, s54, v157
	v_lshl_add_u64 v[186:187], v[186:187], 0, s[12:13]
	s_mov_b32 m0, s55
	ds_read_b128 v[236:239], v154
	ds_read_b128 v[240:243], v154 offset:1024
	ds_read_b128 v[244:247], v154 offset:2048
	ds_read_b128 v[248:251], v154 offset:3072
	global_load_lds_dwordx4 v[186:187], off
	v_lshl_add_u64 v[186:187], v[216:217], 0, s[12:13]
	s_add_i32 m0, s55, 0x2000
	s_nop 0
	global_load_lds_dwordx4 v[186:187], off
	s_barrier
	s_waitcnt lgkmcnt(0)
	s_setprio 1
	s_waitcnt lgkmcnt(0)
	v_mfma_f32_16x16x32_bf16 v[118:121], v[236:239], v[200:203], v[118:121]
	v_mfma_f32_16x16x32_bf16 v[114:117], v[244:247], v[200:203], v[114:117]
	v_mfma_f32_16x16x32_bf16 v[102:105], v[236:239], v[208:211], v[102:105]
	v_mfma_f32_16x16x32_bf16 v[98:101], v[244:247], v[208:211], v[98:101]
	v_mfma_f32_16x16x32_bf16 v[86:89], v[236:239], v[220:223], v[86:89]
	v_mfma_f32_16x16x32_bf16 v[82:85], v[244:247], v[220:223], v[82:85]
	v_mfma_f32_16x16x32_bf16 v[70:73], v[236:239], v[228:231], v[70:73]
	v_mfma_f32_16x16x32_bf16 v[66:69], v[244:247], v[228:231], v[66:69]
	v_mfma_f32_16x16x32_bf16 v[118:121], v[240:243], v[204:207], v[118:121]
	v_mfma_f32_16x16x32_bf16 v[114:117], v[248:251], v[204:207], v[114:117]
	v_mfma_f32_16x16x32_bf16 v[102:105], v[240:243], v[212:215], v[102:105]
	v_mfma_f32_16x16x32_bf16 v[98:101], v[248:251], v[212:215], v[98:101]
	v_mfma_f32_16x16x32_bf16 v[86:89], v[240:243], v[224:227], v[86:89]
	v_mfma_f32_16x16x32_bf16 v[82:85], v[248:251], v[224:227], v[82:85]
	v_mfma_f32_16x16x32_bf16 v[70:73], v[240:243], v[232:235], v[70:73]
	v_mfma_f32_16x16x32_bf16 v[66:69], v[248:251], v[232:235], v[66:69]
	s_setprio 0
	s_mov_b32 m0, s35
	v_lshl_add_u64 v[186:187], v[252:253], 0, s[12:13]
	s_barrier
	ds_read_b128 v[200:203], v193 offset:49152
	ds_read_b128 v[204:207], v193 offset:50176
	ds_read_b128 v[208:211], v193 offset:51200
	ds_read_b128 v[212:215], v193 offset:52224
	ds_read_b128 v[220:223], v193 offset:53248
	ds_read_b128 v[224:227], v193 offset:54272
	ds_read_b128 v[228:231], v193 offset:55296
	ds_read_b128 v[232:235], v193 offset:56320
	global_load_lds_dwordx4 v[186:187], off
	v_lshl_add_u64 v[160:161], v[160:161], 0, s[12:13]
	s_mov_b32 m0, s40
	s_nop 0
	global_load_lds_dwordx4 v[160:161], off
	s_barrier
	s_waitcnt lgkmcnt(0)
	s_setprio 1
	s_waitcnt lgkmcnt(0)
	v_mfma_f32_16x16x32_bf16 v[62:65], v[130:133], v[200:203], v[62:65]
	v_mfma_f32_16x16x32_bf16 v[58:61], v[150:153], v[200:203], v[58:61]
	v_mfma_f32_16x16x32_bf16 v[46:49], v[130:133], v[208:211], v[46:49]
	v_mfma_f32_16x16x32_bf16 v[42:45], v[150:153], v[208:211], v[42:45]
	v_mfma_f32_16x16x32_bf16 v[30:33], v[130:133], v[220:223], v[30:33]
	v_mfma_f32_16x16x32_bf16 v[26:29], v[150:153], v[220:223], v[26:29]
	v_mfma_f32_16x16x32_bf16 v[14:17], v[130:133], v[228:231], v[14:17]
	v_mfma_f32_16x16x32_bf16 v[10:13], v[150:153], v[228:231], v[10:13]
	v_mfma_f32_16x16x32_bf16 v[62:65], v[134:137], v[204:207], v[62:65]
	v_mfma_f32_16x16x32_bf16 v[58:61], v[176:179], v[204:207], v[58:61]
	v_mfma_f32_16x16x32_bf16 v[46:49], v[134:137], v[212:215], v[46:49]
	v_mfma_f32_16x16x32_bf16 v[42:45], v[176:179], v[212:215], v[42:45]
	v_mfma_f32_16x16x32_bf16 v[30:33], v[134:137], v[224:227], v[30:33]
	v_mfma_f32_16x16x32_bf16 v[26:29], v[176:179], v[224:227], v[26:29]
	v_mfma_f32_16x16x32_bf16 v[14:17], v[134:137], v[232:235], v[14:17]
	v_mfma_f32_16x16x32_bf16 v[10:13], v[176:179], v[232:235], v[10:13]
	s_setprio 0
	s_barrier
	s_add_u32 s8, s8, 0x80080
	s_addc_u32 s9, s9, 0
	s_add_i32 s54, s54, s3
	v_lshl_add_u64 v[130:131], s[8:9], 0, v[140:141]
	s_mov_b32 m0, s54
	s_nop 0
	global_load_lds_dwordx4 v[130:131], off
	v_lshl_add_u64 v[130:131], s[8:9], 0, v[144:145]
	s_add_i32 m0, s54, 0x2000
	s_nop 0
	global_load_lds_dwordx4 v[130:131], off
	s_waitcnt vmcnt(6)
	s_barrier
	s_setprio 1
	v_mfma_f32_16x16x32_bf16 v[54:57], v[236:239], v[200:203], v[54:57]
	v_mfma_f32_16x16x32_bf16 v[50:53], v[244:247], v[200:203], v[50:53]
	v_mfma_f32_16x16x32_bf16 v[38:41], v[236:239], v[208:211], v[38:41]
	v_mfma_f32_16x16x32_bf16 v[34:37], v[244:247], v[208:211], v[34:37]
	v_mfma_f32_16x16x32_bf16 v[22:25], v[236:239], v[220:223], v[22:25]
	v_mfma_f32_16x16x32_bf16 v[18:21], v[244:247], v[220:223], v[18:21]
	v_mfma_f32_16x16x32_bf16 v[6:9], v[236:239], v[228:231], v[6:9]
	v_mfma_f32_16x16x32_bf16 v[2:5], v[244:247], v[228:231], v[2:5]
	v_mfma_f32_16x16x32_bf16 v[54:57], v[240:243], v[204:207], v[54:57]
	v_mfma_f32_16x16x32_bf16 v[50:53], v[248:251], v[204:207], v[50:53]
	v_mfma_f32_16x16x32_bf16 v[38:41], v[240:243], v[212:215], v[38:41]
	v_mfma_f32_16x16x32_bf16 v[34:37], v[248:251], v[212:215], v[34:37]
	v_mfma_f32_16x16x32_bf16 v[22:25], v[240:243], v[224:227], v[22:25]
	v_mfma_f32_16x16x32_bf16 v[18:21], v[248:251], v[224:227], v[18:21]
	v_mfma_f32_16x16x32_bf16 v[6:9], v[240:243], v[232:235], v[6:9]
	v_mfma_f32_16x16x32_bf16 v[2:5], v[248:251], v[232:235], v[2:5]
	s_setprio 0
	s_add_i32 s67, s67, 2
	s_add_u32 s4, s4, 0x100
	s_addc_u32 s5, s5, 0
	s_add_u32 s65, s65, 0x100
	s_addc_u32 s66, s66, 0
	s_cmp_gt_u32 s67, 29
	s_barrier
	s_cbranch_scc1 .Lpeel_1037_after

.Lpeel_1037_after:
	s_add_i32 s4, s22, -16
	v_mov_b32_e32 v133, 1.0
	s_cmp_lt_u32 s4, -8
	s_cselect_b64 s[54:55], -1, 0
	s_cmp_gt_u32 s4, -9
	v_mov_b32_e32 v132, 1.0
	v_mov_b32_e32 v131, 1.0
	v_mov_b32_e32 v130, v133
	v_mov_b32_e32 v137, 1.0
	v_mov_b32_e32 v136, 1.0
	v_mov_b32_e32 v135, 1.0
	v_mov_b32_e32 v134, v133
	s_cbranch_scc1 .LBB0_1072
	v_and_b32_e32 v131, 64, v198
	v_xor_b32_e32 v130, 16, v198
	v_add_u32_e32 v131, 64, v131
	v_xor_b32_e32 v134, 32, v198
	v_cmp_lt_i32_e32 vcc, v130, v131
	v_cmp_lt_i32_e64 s[4:5], v134, v131
	s_nop 1
	v_cndmask_b32_e32 v130, v198, v130, vcc
	v_cndmask_b32_e64 v131, v198, v134, s[4:5]
	v_lshlrev_b32_e32 v130, 2, v130
	v_lshlrev_b32_e32 v131, 2, v131
	v_mul_f32_e32 v220, v127, v127
	v_mul_f32_e32 v236, v129, v129
	v_fmac_f32_e32 v220, v126, v126
	v_fmac_f32_e32 v236, v128, v128
	v_add_f32_e32 v220, v220, v236
	v_mul_f32_e32 v236, v123, v123
	v_fmac_f32_e32 v236, v122, v122
	v_add_f32_e32 v220, v220, v236
	v_mul_f32_e32 v236, v125, v125
	v_fmac_f32_e32 v236, v124, v124
	v_add_f32_e32 v220, v236, v220
	v_mul_f32_e32 v221, v119, v119
	v_mul_f32_e32 v237, v121, v121
	v_fmac_f32_e32 v221, v118, v118
	v_fmac_f32_e32 v237, v120, v120
	v_add_f32_e32 v221, v221, v237
	v_mul_f32_e32 v237, v115, v115
	v_fmac_f32_e32 v237, v114, v114
	v_add_f32_e32 v221, v221, v237
	v_mul_f32_e32 v237, v117, v117
	v_fmac_f32_e32 v237, v116, v116
	v_add_f32_e32 v221, v237, v221
	v_mul_f32_e32 v222, v111, v111
	v_mul_f32_e32 v238, v113, v113
	v_fmac_f32_e32 v222, v110, v110
	v_fmac_f32_e32 v238, v112, v112
	v_add_f32_e32 v222, v222, v238
	v_mul_f32_e32 v238, v107, v107
	v_fmac_f32_e32 v238, v106, v106
	v_add_f32_e32 v222, v222, v238
	v_mul_f32_e32 v238, v109, v109
	v_fmac_f32_e32 v238, v108, v108
	v_add_f32_e32 v222, v238, v222
	v_mul_f32_e32 v223, v103, v103
	v_mul_f32_e32 v239, v105, v105
	v_fmac_f32_e32 v223, v102, v102
	v_fmac_f32_e32 v239, v104, v104
	v_add_f32_e32 v223, v223, v239
	v_mul_f32_e32 v239, v99, v99
	v_fmac_f32_e32 v239, v98, v98
	v_add_f32_e32 v223, v223, v239
	v_mul_f32_e32 v239, v101, v101
	v_fmac_f32_e32 v239, v100, v100
	v_add_f32_e32 v223, v239, v223
	v_mul_f32_e32 v224, v95, v95
	v_mul_f32_e32 v240, v97, v97
	v_fmac_f32_e32 v224, v94, v94
	v_fmac_f32_e32 v240, v96, v96
	v_add_f32_e32 v224, v224, v240
	v_mul_f32_e32 v240, v91, v91
	v_fmac_f32_e32 v240, v90, v90
	v_add_f32_e32 v224, v224, v240
	v_mul_f32_e32 v240, v93, v93
	v_fmac_f32_e32 v240, v92, v92
	v_add_f32_e32 v224, v240, v224
	v_mul_f32_e32 v225, v87, v87
	v_mul_f32_e32 v241, v89, v89
	v_fmac_f32_e32 v225, v86, v86
	v_fmac_f32_e32 v241, v88, v88
	v_add_f32_e32 v225, v225, v241
	v_mul_f32_e32 v241, v83, v83
	v_fmac_f32_e32 v241, v82, v82
	v_add_f32_e32 v225, v225, v241
	v_mul_f32_e32 v241, v85, v85
	v_fmac_f32_e32 v241, v84, v84
	v_add_f32_e32 v225, v241, v225
	v_mul_f32_e32 v226, v79, v79
	v_mul_f32_e32 v242, v81, v81
	v_fmac_f32_e32 v226, v78, v78
	v_fmac_f32_e32 v242, v80, v80
	v_add_f32_e32 v226, v226, v242
	v_mul_f32_e32 v242, v75, v75
	v_fmac_f32_e32 v242, v74, v74
	v_add_f32_e32 v226, v226, v242
	v_mul_f32_e32 v242, v77, v77
	v_fmac_f32_e32 v242, v76, v76
	v_add_f32_e32 v226, v242, v226
	v_mul_f32_e32 v227, v71, v71
	v_mul_f32_e32 v243, v73, v73
	v_fmac_f32_e32 v227, v70, v70
	v_fmac_f32_e32 v243, v72, v72
	v_add_f32_e32 v227, v227, v243
	v_mul_f32_e32 v243, v67, v67
	v_fmac_f32_e32 v243, v66, v66
	v_add_f32_e32 v227, v227, v243
	v_mul_f32_e32 v243, v69, v69
	v_fmac_f32_e32 v243, v68, v68
	v_add_f32_e32 v227, v243, v227
	v_mul_f32_e32 v228, v63, v63
	v_mul_f32_e32 v244, v65, v65
	v_fmac_f32_e32 v228, v62, v62
	v_fmac_f32_e32 v244, v64, v64
	v_add_f32_e32 v228, v228, v244
	v_mul_f32_e32 v244, v59, v59
	v_fmac_f32_e32 v244, v58, v58
	v_add_f32_e32 v228, v228, v244
	v_mul_f32_e32 v244, v61, v61
	v_fmac_f32_e32 v244, v60, v60
	v_add_f32_e32 v228, v244, v228
	v_mul_f32_e32 v229, v55, v55
	v_mul_f32_e32 v245, v57, v57
	v_fmac_f32_e32 v229, v54, v54
	v_fmac_f32_e32 v245, v56, v56
	v_add_f32_e32 v229, v229, v245
	v_mul_f32_e32 v245, v51, v51
	v_fmac_f32_e32 v245, v50, v50
	v_add_f32_e32 v229, v229, v245
	v_mul_f32_e32 v245, v53, v53
	v_fmac_f32_e32 v245, v52, v52
	v_add_f32_e32 v229, v245, v229
	v_mul_f32_e32 v230, v47, v47
	v_mul_f32_e32 v246, v49, v49
	v_fmac_f32_e32 v230, v46, v46
	v_fmac_f32_e32 v246, v48, v48
	v_add_f32_e32 v230, v230, v246
	v_mul_f32_e32 v246, v43, v43
	v_fmac_f32_e32 v246, v42, v42
	v_add_f32_e32 v230, v230, v246
	v_mul_f32_e32 v246, v45, v45
	v_fmac_f32_e32 v246, v44, v44
	v_add_f32_e32 v230, v246, v230
	v_mul_f32_e32 v231, v39, v39
	v_mul_f32_e32 v247, v41, v41
	v_fmac_f32_e32 v231, v38, v38
	v_fmac_f32_e32 v247, v40, v40
	v_add_f32_e32 v231, v231, v247
	v_mul_f32_e32 v247, v35, v35
	v_fmac_f32_e32 v247, v34, v34
	v_add_f32_e32 v231, v231, v247
	v_mul_f32_e32 v247, v37, v37
	v_fmac_f32_e32 v247, v36, v36
	v_add_f32_e32 v231, v247, v231
	v_mul_f32_e32 v232, v31, v31
	v_mul_f32_e32 v248, v33, v33
	v_fmac_f32_e32 v232, v30, v30
	v_fmac_f32_e32 v248, v32, v32
	v_add_f32_e32 v232, v232, v248
	v_mul_f32_e32 v248, v27, v27
	v_fmac_f32_e32 v248, v26, v26
	v_add_f32_e32 v232, v232, v248
	v_mul_f32_e32 v248, v29, v29
	v_fmac_f32_e32 v248, v28, v28
	v_add_f32_e32 v232, v248, v232
	v_mul_f32_e32 v233, v23, v23
	v_mul_f32_e32 v249, v25, v25
	v_fmac_f32_e32 v233, v22, v22
	v_fmac_f32_e32 v249, v24, v24
	v_add_f32_e32 v233, v233, v249
	v_mul_f32_e32 v249, v19, v19
	v_fmac_f32_e32 v249, v18, v18
	v_add_f32_e32 v233, v233, v249
	v_mul_f32_e32 v249, v21, v21
	v_fmac_f32_e32 v249, v20, v20
	v_add_f32_e32 v233, v249, v233
	v_mul_f32_e32 v234, v15, v15
	v_mul_f32_e32 v250, v17, v17
	v_fmac_f32_e32 v234, v14, v14
	v_fmac_f32_e32 v250, v16, v16
	v_add_f32_e32 v234, v234, v250
	v_mul_f32_e32 v250, v11, v11
	v_fmac_f32_e32 v250, v10, v10
	v_add_f32_e32 v234, v234, v250
	v_mul_f32_e32 v250, v13, v13
	v_fmac_f32_e32 v250, v12, v12
	v_add_f32_e32 v234, v250, v234
	v_mul_f32_e32 v235, v7, v7
	v_mul_f32_e32 v251, v9, v9
	v_fmac_f32_e32 v235, v6, v6
	v_fmac_f32_e32 v251, v8, v8
	v_add_f32_e32 v235, v235, v251
	v_mul_f32_e32 v251, v3, v3
	v_fmac_f32_e32 v251, v2, v2
	v_add_f32_e32 v235, v235, v251
	v_mul_f32_e32 v251, v5, v5
	v_fmac_f32_e32 v251, v4, v4
	v_add_f32_e32 v235, v251, v235
	ds_bpermute_b32 v236, v130, v220
	ds_bpermute_b32 v237, v130, v221
	ds_bpermute_b32 v238, v130, v222
	ds_bpermute_b32 v239, v130, v223
	ds_bpermute_b32 v240, v130, v224
	ds_bpermute_b32 v241, v130, v225
	ds_bpermute_b32 v242, v130, v226
	ds_bpermute_b32 v243, v130, v227
	s_waitcnt lgkmcnt(7)
	v_add_f32_e32 v220, v220, v236
	s_waitcnt lgkmcnt(6)
	v_add_f32_e32 v221, v221, v237
	s_waitcnt lgkmcnt(5)
	v_add_f32_e32 v222, v222, v238
	s_waitcnt lgkmcnt(4)
	v_add_f32_e32 v223, v223, v239
	s_waitcnt lgkmcnt(3)
	v_add_f32_e32 v224, v224, v240
	s_waitcnt lgkmcnt(2)
	v_add_f32_e32 v225, v225, v241
	s_waitcnt lgkmcnt(1)
	v_add_f32_e32 v226, v226, v242
	s_waitcnt lgkmcnt(0)
	v_add_f32_e32 v227, v227, v243
	ds_bpermute_b32 v244, v130, v228
	ds_bpermute_b32 v245, v130, v229
	ds_bpermute_b32 v246, v130, v230
	ds_bpermute_b32 v247, v130, v231
	ds_bpermute_b32 v248, v130, v232
	ds_bpermute_b32 v249, v130, v233
	ds_bpermute_b32 v250, v130, v234
	ds_bpermute_b32 v251, v130, v235
	s_waitcnt lgkmcnt(7)
	v_add_f32_e32 v228, v228, v244
	s_waitcnt lgkmcnt(6)
	v_add_f32_e32 v229, v229, v245
	s_waitcnt lgkmcnt(5)
	v_add_f32_e32 v230, v230, v246
	s_waitcnt lgkmcnt(4)
	v_add_f32_e32 v231, v231, v247
	s_waitcnt lgkmcnt(3)
	v_add_f32_e32 v232, v232, v248
	s_waitcnt lgkmcnt(2)
	v_add_f32_e32 v233, v233, v249
	s_waitcnt lgkmcnt(1)
	v_add_f32_e32 v234, v234, v250
	s_waitcnt lgkmcnt(0)
	v_add_f32_e32 v235, v235, v251
	ds_bpermute_b32 v236, v131, v220
	ds_bpermute_b32 v237, v131, v221
	ds_bpermute_b32 v238, v131, v222
	ds_bpermute_b32 v239, v131, v223
	ds_bpermute_b32 v240, v131, v224
	ds_bpermute_b32 v241, v131, v225
	ds_bpermute_b32 v242, v131, v226
	ds_bpermute_b32 v243, v131, v227
	s_waitcnt lgkmcnt(7)
	v_add_f32_e32 v220, v220, v236
	s_waitcnt lgkmcnt(6)
	v_add_f32_e32 v221, v221, v237
	s_waitcnt lgkmcnt(5)
	v_add_f32_e32 v222, v222, v238
	s_waitcnt lgkmcnt(4)
	v_add_f32_e32 v223, v223, v239
	s_waitcnt lgkmcnt(3)
	v_add_f32_e32 v224, v224, v240
	s_waitcnt lgkmcnt(2)
	v_add_f32_e32 v225, v225, v241
	s_waitcnt lgkmcnt(1)
	v_add_f32_e32 v226, v226, v242
	s_waitcnt lgkmcnt(0)
	v_add_f32_e32 v227, v227, v243
	ds_bpermute_b32 v244, v131, v228
	ds_bpermute_b32 v245, v131, v229
	ds_bpermute_b32 v246, v131, v230
	ds_bpermute_b32 v247, v131, v231
	ds_bpermute_b32 v248, v131, v232
	ds_bpermute_b32 v249, v131, v233
	ds_bpermute_b32 v250, v131, v234
	ds_bpermute_b32 v251, v131, v235
	s_waitcnt lgkmcnt(7)
	v_add_f32_e32 v228, v228, v244
	s_waitcnt lgkmcnt(6)
	v_add_f32_e32 v229, v229, v245
	s_waitcnt lgkmcnt(5)
	v_add_f32_e32 v230, v230, v246
	s_waitcnt lgkmcnt(4)
	v_add_f32_e32 v231, v231, v247
	s_waitcnt lgkmcnt(3)
	v_add_f32_e32 v232, v232, v248
	s_waitcnt lgkmcnt(2)
	v_add_f32_e32 v233, v233, v249
	s_waitcnt lgkmcnt(1)
	v_add_f32_e32 v234, v234, v250
	s_waitcnt lgkmcnt(0)
	v_add_f32_e32 v235, v235, v251
	s_and_saveexec_b64 s[4:5], s[0:1]
	ds_write_b32 v1, v220
	ds_write_b32 v1, v221 offset:16
	ds_write_b32 v165, v222
	ds_write_b32 v165, v223 offset:16
	ds_write_b32 v169, v224
	ds_write_b32 v169, v225 offset:16
	ds_write_b32 v173, v226
	ds_write_b32 v173, v227 offset:16
	ds_write_b32 v218, v228
	ds_write_b32 v218, v229 offset:16
	ds_write_b32 v183, v230
	ds_write_b32 v183, v231 offset:16
	ds_write_b32 v188, v232
	ds_write_b32 v188, v233 offset:16
	ds_write_b32 v190, v234
	ds_write_b32 v190, v235 offset:16
	s_or_b64 exec, exec, s[4:5]
	s_waitcnt lgkmcnt(0)
	s_barrier
	s_waitcnt lgkmcnt(0)
	ds_read_b128 v[130:133], v159
	ds_read_b128 v[134:137], v159 offset:16
	s_cmp_gt_i32 s22, 15
	s_cselect_b64 s[4:5], -1, 0
	v_cndmask_b32_e64 v179, 1.0, v199, s[4:5]
	s_waitcnt lgkmcnt(0)
	v_mov_b32_e32 v150, v131
	v_mov_b32_e32 v151, v132
	v_mov_b32_e32 v131, v133
	v_pk_add_f32 v[130:131], v[150:151], v[130:131]
	v_readlane_b32 s60, v254, 12
	v_add_f32_e32 v130, v130, v131
	v_fmamk_f32 v130, v130, 0x3c000000, v195
	v_mul_f32_e32 v131, 0x4f800000, v130
	v_cmp_gt_f32_e32 vcc, s76, v130
	v_readlane_b32 s61, v254, 13
	v_readlane_b32 s64, v254, 16
	v_cndmask_b32_e32 v130, v130, v131, vcc
	v_sqrt_f32_e32 v131, v130
	v_readlane_b32 s65, v254, 17
	v_readlane_b32 s66, v254, 18
	v_readlane_b32 s67, v254, 19
	v_add_u32_e32 v132, -1, v131
	v_fma_f32 v133, -v132, v131, v130
	v_cmp_ge_f32_e64 s[4:5], 0, v133
	v_add_u32_e32 v133, 1, v131
	v_readlane_b32 s70, v254, 22
	v_cndmask_b32_e64 v132, v131, v132, s[4:5]
	v_fma_f32 v131, -v133, v131, v130
	v_cmp_lt_f32_e64 s[4:5], 0, v131
	v_readlane_b32 s71, v254, 23
	s_cmp_lt_i32 s22, 8
	v_cndmask_b32_e64 v131, v132, v133, s[4:5]
	v_mul_f32_e32 v132, 0x37800000, v131
	v_cndmask_b32_e32 v131, v131, v132, vcc
	v_cmp_class_f32_e32 vcc, v130, v196
	s_mov_b64 s[60:61], s[64:65]
	s_mov_b64 s[66:67], s[70:71]
	v_cndmask_b32_e32 v132, v131, v130, vcc
	v_div_scale_f32 v133, s[4:5], v132, v132, v179
	v_rcp_f32_e32 v150, v133
	v_mov_b32_e32 v131, v136
	v_div_scale_f32 v151, vcc, v179, v132, v179
	v_fma_f32 v130, -v133, v150, 1.0
	v_fmac_f32_e32 v150, v130, v150
	v_mov_b32_e32 v130, v135
	v_mov_b32_e32 v135, v137
	v_pk_add_f32 v[130:131], v[130:131], v[134:135]
	v_mul_f32_e32 v152, v151, v150
	v_add_f32_e32 v130, v130, v131
	v_fmamk_f32 v130, v130, 0x3c000000, v195
	v_mul_f32_e32 v131, 0x4f800000, v130
	v_cmp_gt_f32_e64 s[4:5], s76, v130
	v_fma_f32 v134, -v133, v152, v151
	v_fmac_f32_e32 v152, v134, v150
	v_cndmask_b32_e64 v130, v130, v131, s[4:5]
	v_sqrt_f32_e32 v131, v130
	v_fma_f32 v133, -v133, v152, v151
	ds_read_b128 v[200:203], v189
	v_readlane_b32 s62, v254, 14
	v_add_u32_e32 v134, -1, v131
	v_fma_f32 v135, -v134, v131, v130
	v_cmp_ge_f32_e64 s[8:9], 0, v135
	v_add_u32_e32 v135, 1, v131
	v_readlane_b32 s63, v254, 15
	v_cndmask_b32_e64 v134, v131, v134, s[8:9]
	v_fma_f32 v131, -v135, v131, v130
	v_cmp_lt_f32_e64 s[8:9], 0, v131
	v_readlane_b32 s68, v254, 20
	v_readlane_b32 s69, v254, 21
	v_cndmask_b32_e64 v131, v134, v135, s[8:9]
	v_mul_f32_e32 v134, 0x37800000, v131
	v_cndmask_b32_e64 v131, v131, v134, s[4:5]
	v_cmp_class_f32_e64 s[4:5], v130, v196
	ds_read_b128 v[134:137], v163 offset:16
	v_readlane_b32 s72, v254, 24
	v_cndmask_b32_e64 v153, v131, v130, s[4:5]
	v_div_scale_f32 v154, s[4:5], v153, v153, v179
	v_rcp_f32_e32 v156, v154
	v_div_fmas_f32 v130, v133, v150, v152
	v_div_fixup_f32 v178, v130, v132, v179
	v_div_scale_f32 v152, vcc, v179, v153, v179
	v_fma_f32 v130, -v154, v156, 1.0
	v_fmac_f32_e32 v156, v130, v156
	ds_read_b128 v[130:133], v163
	v_mul_f32_e32 v158, v152, v156
	v_readlane_b32 s73, v254, 25
	v_readlane_b32 s74, v254, 26
	v_readlane_b32 s75, v254, 27
	s_waitcnt lgkmcnt(0)
	v_mov_b32_e32 v150, v131
	v_mov_b32_e32 v151, v132
	v_mov_b32_e32 v131, v133
	v_pk_add_f32 v[130:131], v[150:151], v[130:131]
	v_fma_f32 v132, -v154, v158, v152
	v_add_f32_e32 v130, v130, v131
	v_fmamk_f32 v130, v130, 0x3c000000, v195
	v_mul_f32_e32 v131, 0x4f800000, v130
	v_cmp_gt_f32_e64 s[4:5], s76, v130
	v_fmac_f32_e32 v158, v132, v156
	v_fma_f32 v132, -v154, v158, v152
	v_cndmask_b32_e64 v130, v130, v131, s[4:5]
	v_sqrt_f32_e32 v131, v130
	s_nop 0
	v_add_u32_e32 v133, -1, v131
	v_fma_f32 v150, -v133, v131, v130
	v_cmp_ge_f32_e64 s[8:9], 0, v150
	v_add_u32_e32 v150, 1, v131
	s_nop 0
	v_cndmask_b32_e64 v133, v131, v133, s[8:9]
	v_fma_f32 v131, -v150, v131, v130
	v_cmp_lt_f32_e64 s[8:9], 0, v131
	s_nop 1
	v_cndmask_b32_e64 v131, v133, v150, s[8:9]
	v_mul_f32_e32 v133, 0x37800000, v131
	v_cndmask_b32_e64 v131, v131, v133, s[4:5]
	v_cmp_class_f32_e64 s[4:5], v130, v196
	s_nop 1
	v_cndmask_b32_e64 v133, v131, v130, s[4:5]
	v_div_scale_f32 v150, s[4:5], v133, v133, v179
	v_rcp_f32_e32 v151, v150
	v_div_fmas_f32 v130, v132, v156, v158
	v_div_fixup_f32 v176, v130, v153, v179
	v_mov_b32_e32 v131, v136
	v_fma_f32 v130, -v150, v151, 1.0
	v_fmac_f32_e32 v151, v130, v151
	v_mov_b32_e32 v130, v135
	v_mov_b32_e32 v135, v137
	v_pk_add_f32 v[130:131], v[130:131], v[134:135]
	v_div_scale_f32 v132, vcc, v179, v133, v179
	v_add_f32_e32 v130, v130, v131
	v_fmamk_f32 v130, v130, 0x3c000000, v195
	v_mul_f32_e32 v131, 0x4f800000, v130
	v_cmp_gt_f32_e64 s[4:5], s76, v130
	v_mul_f32_e32 v152, v132, v151
	v_fma_f32 v134, -v150, v152, v132
	v_cndmask_b32_e64 v130, v130, v131, s[4:5]
	v_sqrt_f32_e32 v131, v130
	v_fmac_f32_e32 v152, v134, v151
	v_fma_f32 v132, -v150, v152, v132
	v_add_u32_e32 v134, -1, v131
	v_fma_f32 v135, -v134, v131, v130
	v_cmp_ge_f32_e64 s[8:9], 0, v135
	v_add_u32_e32 v135, 1, v131
	s_nop 0
	v_cndmask_b32_e64 v134, v131, v134, s[8:9]
	v_fma_f32 v131, -v135, v131, v130
	v_cmp_lt_f32_e64 s[8:9], 0, v131
	s_nop 1
	v_cndmask_b32_e64 v131, v134, v135, s[8:9]
	v_mul_f32_e32 v134, 0x37800000, v131
	v_cndmask_b32_e64 v131, v131, v134, s[4:5]
	v_cmp_class_f32_e64 s[4:5], v130, v196
	ds_read_b128 v[134:137], v167 offset:16
	s_nop 0
	v_cndmask_b32_e64 v153, v131, v130, s[4:5]
	v_div_scale_f32 v154, s[4:5], v153, v153, v179
	v_rcp_f32_e32 v156, v154
	v_div_fmas_f32 v130, v132, v151, v152
	v_div_fixup_f32 v174, v130, v133, v179
	v_div_scale_f32 v152, vcc, v179, v153, v179
	v_fma_f32 v130, -v154, v156, 1.0
	v_fmac_f32_e32 v156, v130, v156
	ds_read_b128 v[130:133], v167
	v_mul_f32_e32 v158, v152, v156
	s_waitcnt lgkmcnt(0)
	v_mov_b32_e32 v150, v131
	v_mov_b32_e32 v151, v132
	v_mov_b32_e32 v131, v133
	v_pk_add_f32 v[130:131], v[150:151], v[130:131]
	v_fma_f32 v132, -v154, v158, v152
	v_add_f32_e32 v130, v130, v131
	v_fmamk_f32 v130, v130, 0x3c000000, v195
	v_mul_f32_e32 v131, 0x4f800000, v130
	v_cmp_gt_f32_e64 s[4:5], s76, v130
	v_fmac_f32_e32 v158, v132, v156
	v_fma_f32 v132, -v154, v158, v152
	v_cndmask_b32_e64 v130, v130, v131, s[4:5]
	v_sqrt_f32_e32 v131, v130
	s_nop 0
	v_add_u32_e32 v133, -1, v131
	v_fma_f32 v150, -v133, v131, v130
	v_cmp_ge_f32_e64 s[8:9], 0, v150
	v_add_u32_e32 v150, 1, v131
	s_nop 0
	v_cndmask_b32_e64 v133, v131, v133, s[8:9]
	v_fma_f32 v131, -v150, v131, v130
	v_cmp_lt_f32_e64 s[8:9], 0, v131
	s_nop 1
	v_cndmask_b32_e64 v131, v133, v150, s[8:9]
	v_mul_f32_e32 v133, 0x37800000, v131
	v_cndmask_b32_e64 v131, v131, v133, s[4:5]
	v_cmp_class_f32_e64 s[4:5], v130, v196
	s_nop 1
	v_cndmask_b32_e64 v133, v131, v130, s[4:5]
	v_div_scale_f32 v150, s[4:5], v133, v133, v179
	v_rcp_f32_e32 v151, v150
	v_div_fmas_f32 v130, v132, v156, v158
	v_div_fixup_f32 v172, v130, v153, v179
	v_mov_b32_e32 v131, v136
	v_fma_f32 v130, -v150, v151, 1.0
	v_fmac_f32_e32 v151, v130, v151
	v_mov_b32_e32 v130, v135
	v_mov_b32_e32 v135, v137
	v_pk_add_f32 v[130:131], v[130:131], v[134:135]
	v_div_scale_f32 v132, vcc, v179, v133, v179
	v_add_f32_e32 v130, v130, v131
	v_fmamk_f32 v130, v130, 0x3c000000, v195
	v_mul_f32_e32 v131, 0x4f800000, v130
	v_cmp_gt_f32_e64 s[4:5], s76, v130
	v_mul_f32_e32 v152, v132, v151
	v_fma_f32 v134, -v150, v152, v132
	v_cndmask_b32_e64 v130, v130, v131, s[4:5]
	v_sqrt_f32_e32 v131, v130
	v_fmac_f32_e32 v152, v134, v151
	v_fma_f32 v132, -v150, v152, v132
	v_add_u32_e32 v134, -1, v131
	v_fma_f32 v135, -v134, v131, v130
	v_cmp_ge_f32_e64 s[8:9], 0, v135
	v_add_u32_e32 v135, 1, v131
	s_nop 0
	v_cndmask_b32_e64 v134, v131, v134, s[8:9]
	v_fma_f32 v131, -v135, v131, v130
	v_cmp_lt_f32_e64 s[8:9], 0, v131
	s_nop 1
	v_cndmask_b32_e64 v131, v134, v135, s[8:9]
	v_mul_f32_e32 v134, 0x37800000, v131
	v_cndmask_b32_e64 v131, v131, v134, s[4:5]
	v_cmp_class_f32_e64 s[4:5], v130, v196
	ds_read_b128 v[134:137], v171 offset:16
	s_nop 0
	v_cndmask_b32_e64 v153, v131, v130, s[4:5]
	v_div_scale_f32 v154, s[4:5], v153, v153, v179
	v_rcp_f32_e32 v156, v154
	v_div_fmas_f32 v130, v132, v151, v152
	v_div_fixup_f32 v170, v130, v133, v179
	v_div_scale_f32 v152, vcc, v179, v153, v179
	v_fma_f32 v130, -v154, v156, 1.0
	v_fmac_f32_e32 v156, v130, v156
	ds_read_b128 v[130:133], v171
	v_mul_f32_e32 v158, v152, v156
	s_waitcnt lgkmcnt(0)
	v_mov_b32_e32 v150, v131
	v_mov_b32_e32 v151, v132
	v_mov_b32_e32 v131, v133
	v_pk_add_f32 v[130:131], v[150:151], v[130:131]
	v_fma_f32 v132, -v154, v158, v152
	v_add_f32_e32 v130, v130, v131
	v_fmamk_f32 v130, v130, 0x3c000000, v195
	v_mul_f32_e32 v131, 0x4f800000, v130
	v_cmp_gt_f32_e64 s[4:5], s76, v130
	v_fmac_f32_e32 v158, v132, v156
	v_fma_f32 v132, -v154, v158, v152
	v_cndmask_b32_e64 v130, v130, v131, s[4:5]
	v_sqrt_f32_e32 v131, v130
	s_nop 0
	v_add_u32_e32 v133, -1, v131
	v_fma_f32 v150, -v133, v131, v130
	v_cmp_ge_f32_e64 s[8:9], 0, v150
	v_add_u32_e32 v150, 1, v131
	s_nop 0
	v_cndmask_b32_e64 v133, v131, v133, s[8:9]
	v_fma_f32 v131, -v150, v131, v130
	v_cmp_lt_f32_e64 s[8:9], 0, v131
	s_nop 1
	v_cndmask_b32_e64 v131, v133, v150, s[8:9]
	v_mul_f32_e32 v133, 0x37800000, v131
	v_cndmask_b32_e64 v131, v131, v133, s[4:5]
	v_cmp_class_f32_e64 s[4:5], v130, v196
	s_nop 1
	v_cndmask_b32_e64 v133, v131, v130, s[4:5]
	v_div_scale_f32 v150, s[4:5], v133, v133, v179
	v_rcp_f32_e32 v151, v150
	v_div_fmas_f32 v130, v132, v156, v158
	v_div_fixup_f32 v168, v130, v153, v179
	v_mov_b32_e32 v131, v136
	v_fma_f32 v130, -v150, v151, 1.0
	v_fmac_f32_e32 v151, v130, v151
	v_mov_b32_e32 v130, v135
	v_mov_b32_e32 v135, v137
	v_pk_add_f32 v[130:131], v[130:131], v[134:135]
	v_div_scale_f32 v132, vcc, v179, v133, v179
	v_add_f32_e32 v130, v130, v131
	v_fmamk_f32 v130, v130, 0x3c000000, v195
	v_mul_f32_e32 v131, 0x4f800000, v130
	v_cmp_gt_f32_e64 s[4:5], s76, v130
	v_mul_f32_e32 v152, v132, v151
	v_fma_f32 v134, -v150, v152, v132
	v_cndmask_b32_e64 v130, v130, v131, s[4:5]
	v_sqrt_f32_e32 v131, v130
	v_fmac_f32_e32 v152, v134, v151
	v_fma_f32 v132, -v150, v152, v132
	v_add_u32_e32 v134, -1, v131
	v_fma_f32 v135, -v134, v131, v130
	v_cmp_ge_f32_e64 s[8:9], 0, v135
	v_add_u32_e32 v135, 1, v131
	s_nop 0
	v_cndmask_b32_e64 v134, v131, v134, s[8:9]
	v_fma_f32 v131, -v135, v131, v130
	v_cmp_lt_f32_e64 s[8:9], 0, v131
	s_nop 1
	v_cndmask_b32_e64 v131, v134, v135, s[8:9]
	v_mul_f32_e32 v134, 0x37800000, v131
	v_cndmask_b32_e64 v131, v131, v134, s[4:5]
	v_cmp_class_f32_e64 s[4:5], v130, v196
	ds_read_b128 v[134:137], v175 offset:16
	s_nop 0
	v_cndmask_b32_e64 v153, v131, v130, s[4:5]
	v_div_scale_f32 v154, s[4:5], v153, v153, v179
	v_rcp_f32_e32 v156, v154
	v_div_fmas_f32 v130, v132, v151, v152
	v_div_fixup_f32 v166, v130, v133, v179
	v_div_scale_f32 v152, vcc, v179, v153, v179
	v_fma_f32 v130, -v154, v156, 1.0
	v_fmac_f32_e32 v156, v130, v156
	ds_read_b128 v[130:133], v175
	v_mul_f32_e32 v158, v152, v156
	s_waitcnt lgkmcnt(0)
	v_mov_b32_e32 v150, v131
	v_mov_b32_e32 v151, v132
	v_mov_b32_e32 v131, v133
	v_pk_add_f32 v[130:131], v[150:151], v[130:131]
	v_fma_f32 v132, -v154, v158, v152
	v_add_f32_e32 v130, v130, v131
	v_fmamk_f32 v130, v130, 0x3c000000, v195
	v_mul_f32_e32 v131, 0x4f800000, v130
	v_cmp_gt_f32_e64 s[4:5], s76, v130
	v_fmac_f32_e32 v158, v132, v156
	v_fma_f32 v132, -v154, v158, v152
	v_cndmask_b32_e64 v130, v130, v131, s[4:5]
	v_sqrt_f32_e32 v131, v130
	s_nop 0
	v_add_u32_e32 v133, -1, v131
	v_fma_f32 v150, -v133, v131, v130
	v_cmp_ge_f32_e64 s[8:9], 0, v150
	v_add_u32_e32 v150, 1, v131
	s_nop 0
	v_cndmask_b32_e64 v133, v131, v133, s[8:9]
	v_fma_f32 v131, -v150, v131, v130
	v_cmp_lt_f32_e64 s[8:9], 0, v131
	s_nop 1
	v_cndmask_b32_e64 v131, v133, v150, s[8:9]
	v_mul_f32_e32 v133, 0x37800000, v131
	v_cndmask_b32_e64 v131, v131, v133, s[4:5]
	v_cmp_class_f32_e64 s[4:5], v130, v196
	s_nop 1
	v_cndmask_b32_e64 v133, v131, v130, s[4:5]
	v_div_scale_f32 v150, s[4:5], v133, v133, v179
	v_rcp_f32_e32 v151, v150
	v_div_fmas_f32 v130, v132, v156, v158
	v_div_fixup_f32 v164, v130, v153, v179
	v_mov_b32_e32 v131, v136
	v_fma_f32 v130, -v150, v151, 1.0
	v_fmac_f32_e32 v151, v130, v151
	v_mov_b32_e32 v130, v135
	v_mov_b32_e32 v135, v137
	v_pk_add_f32 v[130:131], v[130:131], v[134:135]
	v_div_scale_f32 v132, vcc, v179, v133, v179
	v_add_f32_e32 v130, v130, v131
	v_fmamk_f32 v130, v130, 0x3c000000, v195
	v_mul_f32_e32 v131, 0x4f800000, v130
	v_cmp_gt_f32_e64 s[4:5], s76, v130
	v_mul_f32_e32 v152, v132, v151
	v_fma_f32 v134, -v150, v152, v132
	v_cndmask_b32_e64 v130, v130, v131, s[4:5]
	v_sqrt_f32_e32 v131, v130
	v_fmac_f32_e32 v152, v134, v151
	v_fma_f32 v132, -v150, v152, v132
	v_add_u32_e32 v134, -1, v131
	v_fma_f32 v135, -v134, v131, v130
	v_cmp_ge_f32_e64 s[8:9], 0, v135
	v_add_u32_e32 v135, 1, v131
	s_nop 0
	v_cndmask_b32_e64 v134, v131, v134, s[8:9]
	v_fma_f32 v131, -v135, v131, v130
	v_cmp_lt_f32_e64 s[8:9], 0, v131
	s_nop 1
	v_cndmask_b32_e64 v131, v134, v135, s[8:9]
	v_mul_f32_e32 v134, 0x37800000, v131
	v_cndmask_b32_e64 v131, v131, v134, s[4:5]
	v_cmp_class_f32_e64 s[4:5], v130, v196
	ds_read_b128 v[134:137], v181 offset:16
	s_nop 0
	v_cndmask_b32_e64 v153, v131, v130, s[4:5]
	v_div_scale_f32 v154, s[4:5], v153, v153, v179
	v_rcp_f32_e32 v156, v154
	v_div_fmas_f32 v130, v132, v151, v152
	v_div_fixup_f32 v162, v130, v133, v179
	v_div_scale_f32 v152, vcc, v179, v153, v179
	v_fma_f32 v130, -v154, v156, 1.0
	v_fmac_f32_e32 v156, v130, v156
	ds_read_b128 v[130:133], v181
	v_mul_f32_e32 v158, v152, v156
	s_waitcnt lgkmcnt(0)
	v_mov_b32_e32 v150, v131
	v_mov_b32_e32 v151, v132
	v_mov_b32_e32 v131, v133
	v_pk_add_f32 v[130:131], v[150:151], v[130:131]
	v_fma_f32 v132, -v154, v158, v152
	v_add_f32_e32 v130, v130, v131
	v_fmamk_f32 v130, v130, 0x3c000000, v195
	v_mul_f32_e32 v131, 0x4f800000, v130
	v_cmp_gt_f32_e64 s[4:5], s76, v130
	v_fmac_f32_e32 v158, v132, v156
	v_fma_f32 v132, -v154, v158, v152
	v_cndmask_b32_e64 v130, v130, v131, s[4:5]
	v_sqrt_f32_e32 v131, v130
	s_nop 0
	v_add_u32_e32 v133, -1, v131
	v_fma_f32 v150, -v133, v131, v130
	v_cmp_ge_f32_e64 s[8:9], 0, v150
	v_add_u32_e32 v150, 1, v131
	s_nop 0
	v_cndmask_b32_e64 v133, v131, v133, s[8:9]
	v_fma_f32 v131, -v150, v131, v130
	v_cmp_lt_f32_e64 s[8:9], 0, v131
	s_nop 1
	v_cndmask_b32_e64 v131, v133, v150, s[8:9]
	v_mul_f32_e32 v133, 0x37800000, v131
	v_cndmask_b32_e64 v131, v131, v133, s[4:5]
	v_cmp_class_f32_e64 s[4:5], v130, v196
	s_nop 1
	v_cndmask_b32_e64 v133, v131, v130, s[4:5]
	v_div_scale_f32 v150, s[4:5], v133, v133, v179
	v_rcp_f32_e32 v151, v150
	v_div_fmas_f32 v130, v132, v156, v158
	v_div_fixup_f32 v160, v130, v153, v179
	v_mov_b32_e32 v131, v136
	v_fma_f32 v130, -v150, v151, 1.0
	v_fmac_f32_e32 v151, v130, v151
	v_mov_b32_e32 v130, v135
	v_mov_b32_e32 v135, v137
	v_pk_add_f32 v[130:131], v[130:131], v[134:135]
	v_div_scale_f32 v132, vcc, v179, v133, v179
	v_add_f32_e32 v130, v130, v131
	v_fmamk_f32 v130, v130, 0x3c000000, v195
	v_mul_f32_e32 v131, 0x4f800000, v130
	v_cmp_gt_f32_e64 s[4:5], s76, v130
	v_mul_f32_e32 v152, v132, v151
	v_fma_f32 v134, -v150, v152, v132
	v_cndmask_b32_e64 v130, v130, v131, s[4:5]
	v_sqrt_f32_e32 v131, v130
	v_fmac_f32_e32 v152, v134, v151
	v_fma_f32 v132, -v150, v152, v132
	v_add_u32_e32 v134, -1, v131
	v_fma_f32 v135, -v134, v131, v130
	v_cmp_ge_f32_e64 s[8:9], 0, v135
	v_add_u32_e32 v135, 1, v131
	s_nop 0
	v_cndmask_b32_e64 v134, v131, v134, s[8:9]
	v_fma_f32 v131, -v135, v131, v130
	v_cmp_lt_f32_e64 s[8:9], 0, v131
	s_nop 1
	v_cndmask_b32_e64 v131, v134, v135, s[8:9]
	v_mul_f32_e32 v134, 0x37800000, v131
	v_cndmask_b32_e64 v131, v131, v134, s[4:5]
	v_cmp_class_f32_e64 s[4:5], v130, v196
	ds_read_b128 v[134:137], v185 offset:16
	s_nop 0
	v_cndmask_b32_e64 v153, v131, v130, s[4:5]
	v_div_scale_f32 v154, s[4:5], v153, v153, v179
	v_rcp_f32_e32 v156, v154
	v_div_fmas_f32 v130, v132, v151, v152
	v_div_fixup_f32 v158, v130, v133, v179
	v_div_scale_f32 v152, vcc, v179, v153, v179
	v_fma_f32 v130, -v154, v156, 1.0
	v_fmac_f32_e32 v156, v130, v156
	ds_read_b128 v[130:133], v185
	v_mul_f32_e32 v161, v152, v156
	s_waitcnt lgkmcnt(0)
	v_mov_b32_e32 v150, v131
	v_mov_b32_e32 v151, v132
	v_mov_b32_e32 v131, v133
	v_pk_add_f32 v[130:131], v[150:151], v[130:131]
	v_fma_f32 v132, -v154, v161, v152
	v_add_f32_e32 v130, v130, v131
	v_fmamk_f32 v130, v130, 0x3c000000, v195
	v_mul_f32_e32 v131, 0x4f800000, v130
	v_cmp_gt_f32_e64 s[4:5], s76, v130
	v_fmac_f32_e32 v161, v132, v156
	v_fma_f32 v132, -v154, v161, v152
	v_cndmask_b32_e64 v130, v130, v131, s[4:5]
	v_sqrt_f32_e32 v131, v130
	s_nop 0
	v_add_u32_e32 v133, -1, v131
	v_fma_f32 v150, -v133, v131, v130
	v_cmp_ge_f32_e64 s[8:9], 0, v150
	v_add_u32_e32 v150, 1, v131
	s_nop 0
	v_cndmask_b32_e64 v133, v131, v133, s[8:9]
	v_fma_f32 v131, -v150, v131, v130
	v_cmp_lt_f32_e64 s[8:9], 0, v131
	s_nop 1
	v_cndmask_b32_e64 v131, v133, v150, s[8:9]
	v_mul_f32_e32 v133, 0x37800000, v131
	v_cndmask_b32_e64 v131, v131, v133, s[4:5]
	v_cmp_class_f32_e64 s[4:5], v130, v196
	s_nop 1
	v_cndmask_b32_e64 v133, v131, v130, s[4:5]
	v_div_scale_f32 v150, s[4:5], v133, v133, v179
	v_rcp_f32_e32 v151, v150
	v_div_fmas_f32 v130, v132, v156, v161
	v_div_fixup_f32 v156, v130, v153, v179
	v_mov_b32_e32 v131, v136
	v_fma_f32 v130, -v150, v151, 1.0
	v_fmac_f32_e32 v151, v130, v151
	v_mov_b32_e32 v130, v135
	v_mov_b32_e32 v135, v137
	v_pk_add_f32 v[130:131], v[130:131], v[134:135]
	v_div_scale_f32 v132, vcc, v179, v133, v179
	v_add_f32_e32 v130, v130, v131
	v_fmamk_f32 v130, v130, 0x3c000000, v195
	v_mul_f32_e32 v131, 0x4f800000, v130
	v_cmp_gt_f32_e64 s[4:5], s76, v130
	v_mul_f32_e32 v152, v132, v151
	v_fma_f32 v134, -v150, v152, v132
	v_cndmask_b32_e64 v130, v130, v131, s[4:5]
	v_sqrt_f32_e32 v131, v130
	v_fmac_f32_e32 v152, v134, v151
	v_fma_f32 v132, -v150, v152, v132
	v_mov_b32_e32 v150, v201
	v_add_u32_e32 v134, -1, v131
	v_fma_f32 v135, -v134, v131, v130
	v_cmp_ge_f32_e64 s[8:9], 0, v135
	v_add_u32_e32 v135, 1, v131
	v_mov_b32_e32 v201, v203
	v_cndmask_b32_e64 v134, v131, v134, s[8:9]
	v_fma_f32 v131, -v135, v131, v130
	v_cmp_lt_f32_e64 s[8:9], 0, v131
	s_nop 1
	v_cndmask_b32_e64 v131, v134, v135, s[8:9]
	v_mul_f32_e32 v134, 0x37800000, v131
	v_cndmask_b32_e64 v131, v131, v134, s[4:5]
	v_cmp_class_f32_e64 s[4:5], v130, v196
	s_nop 1
	v_cndmask_b32_e64 v153, v131, v130, s[4:5]
	v_div_scale_f32 v161, s[4:5], v153, v153, v179
	v_rcp_f32_e32 v177, v161
	s_cselect_b32 s4, s60, s66
	v_div_fmas_f32 v130, v132, v151, v152
	s_cselect_b32 s5, s61, s67
	s_add_u32 s4, s4, s77
	v_div_fixup_f32 v154, v130, v133, v179
	v_fma_f32 v130, -v161, v177, 1.0
	s_addc_u32 s5, s5, 0
	v_fmac_f32_e32 v177, v130, v177
	global_load_dwordx4 v[134:137], v197, s[4:5]
	global_load_dwordx4 v[130:133], v197, s[4:5] offset:16
	v_mov_b32_e32 v151, v202
	v_pk_add_f32 v[150:151], v[150:151], v[200:201]
	v_div_scale_f32 v152, vcc, v179, v153, v179
	v_add_f32_e32 v150, v150, v151
	v_fmamk_f32 v150, v150, 0x3c000000, v195
	v_mul_f32_e32 v151, 0x4f800000, v150
	v_cmp_gt_f32_e64 s[4:5], s76, v150
	v_mul_f32_e32 v180, v152, v177
	v_fma_f32 v182, -v161, v180, v152
	v_cndmask_b32_e64 v150, v150, v151, s[4:5]
	v_sqrt_f32_e32 v151, v150
	v_fmac_f32_e32 v180, v182, v177
	v_fma_f32 v152, -v161, v180, v152
	ds_read_b128 v[204:207], v189 offset:16
	v_add_u32_e32 v161, -1, v151
	v_fma_f32 v182, -v161, v151, v150
	v_cmp_ge_f32_e64 s[8:9], 0, v182
	v_add_u32_e32 v182, 1, v151
	s_nop 0
	v_cndmask_b32_e64 v161, v151, v161, s[8:9]
	v_fma_f32 v151, -v182, v151, v150
	v_cmp_lt_f32_e64 s[8:9], 0, v151
	s_nop 1
	v_cndmask_b32_e64 v151, v161, v182, s[8:9]
	v_mul_f32_e32 v161, 0x37800000, v151
	v_cndmask_b32_e64 v151, v151, v161, s[4:5]
	v_cmp_class_f32_e64 s[4:5], v150, v196
	s_nop 1
	v_cndmask_b32_e64 v161, v151, v150, s[4:5]
	v_div_scale_f32 v182, s[4:5], v161, v161, v179
	v_rcp_f32_e32 v186, v182
	v_div_fmas_f32 v150, v152, v177, v180
	v_div_fixup_f32 v184, v150, v153, v179
	s_waitcnt lgkmcnt(0)
	v_mov_b32_e32 v151, v206
	v_fma_f32 v150, -v182, v186, 1.0
	v_fmac_f32_e32 v186, v150, v186
	v_mov_b32_e32 v150, v205
	v_mov_b32_e32 v205, v207
	v_pk_add_f32 v[150:151], v[150:151], v[204:205]
	v_div_scale_f32 v152, vcc, v179, v161, v179
	v_add_f32_e32 v150, v150, v151
	v_fmamk_f32 v150, v150, 0x3c000000, v195
	v_mul_f32_e32 v151, 0x4f800000, v150
	v_cmp_gt_f32_e64 s[4:5], s76, v150
	v_mul_f32_e32 v153, v152, v186
	v_fma_f32 v177, -v182, v153, v152
	v_cndmask_b32_e64 v150, v150, v151, s[4:5]
	v_sqrt_f32_e32 v151, v150
	v_fmac_f32_e32 v153, v177, v186
	v_fma_f32 v152, -v182, v153, v152
	v_div_fmas_f32 v152, v152, v186, v153
	v_add_u32_e32 v177, -1, v151
	v_fma_f32 v180, -v177, v151, v150
	v_cmp_ge_f32_e64 s[8:9], 0, v180
	v_add_u32_e32 v180, 1, v151
	v_div_fixup_f32 v182, v152, v161, v179
	v_cndmask_b32_e64 v177, v151, v177, s[8:9]
	v_fma_f32 v151, -v180, v151, v150
	v_cmp_lt_f32_e64 s[8:9], 0, v151
	s_nop 1
	v_cndmask_b32_e64 v151, v177, v180, s[8:9]
	v_mul_f32_e32 v177, 0x37800000, v151
	v_cndmask_b32_e64 v151, v151, v177, s[4:5]
	v_cmp_class_f32_e64 s[4:5], v150, v196
	s_nop 1
	v_cndmask_b32_e64 v150, v151, v150, s[4:5]
	v_div_scale_f32 v151, s[4:5], v150, v150, v179
	v_rcp_f32_e32 v177, v151
	s_nop 0
	v_fma_f32 v152, -v151, v177, 1.0
	v_fmac_f32_e32 v177, v152, v177
	v_div_scale_f32 v152, vcc, v179, v150, v179
	v_mul_f32_e32 v153, v152, v177
	v_fma_f32 v161, -v151, v153, v152
	v_fmac_f32_e32 v153, v161, v177
	v_fma_f32 v151, -v151, v153, v152
	v_div_fmas_f32 v151, v151, v177, v153
	v_div_fixup_f32 v180, v151, v150, v179

.LBB0_1238:
	s_ashr_i32 s21, s20, 31
	v_cmp_lt_i64_e32 vcc, s[22:23], v[138:139]
	s_lshl_b64 s[22:23], s[20:21], 20
	s_add_u32 s22, s4, s22
	s_addc_u32 s23, s5, s23
	s_and_b64 s[24:25], vcc, exec
	s_cselect_b32 s21, s23, s57
	s_cselect_b32 s71, s22, s56
	s_ashr_i32 s19, s18, 31
	s_lshl_b64 s[24:25], s[18:19], 20
	v_readlane_b32 s60, v254, 32
	v_readlane_b32 s61, v254, 33
	s_add_u32 s24, s60, s24
	s_addc_u32 s25, s61, s25
	s_and_b64 s[60:61], vcc, exec
	s_cselect_b32 s19, s25, s59
	s_cselect_b32 s72, s24, s58
	s_add_u32 s56, s56, 0x80080
	s_addc_u32 s57, s57, 0
	s_add_u32 s73, s58, 0x100
	v_mov_b32_e32 v2, 0
	s_addc_u32 s74, s59, 0
	s_mov_b32 s75, -2
	ds_read_b128 v[150:153], v147
	ds_read_b128 v[154:157], v147 offset:1024
	ds_read_b128 v[158:161], v147 offset:2048
	ds_read_b128 v[162:165], v147 offset:3072
	s_add_u32 s58, s56, 0xfff80080
	s_addc_u32 s59, s57, -1
	s_cmp_eq_u32 s75, 28
	s_cselect_b32 s61, s21, s59
	s_cselect_b32 s60, s71, s58
	s_cselect_b32 s59, s19, s74
	s_cselect_b32 s58, s72, s73
	v_lshl_add_u64 v[142:143], s[56:57], 0, v[134:135]
	s_add_i32 m0, s33, 0xc000
	ds_read_b128 v[166:169], v148
	ds_read_b128 v[170:173], v148 offset:1024
	ds_read_b128 v[174:177], v148 offset:2048
	ds_read_b128 v[178:181], v148 offset:3072
	ds_read_b128 v[182:185], v148 offset:4096
	ds_read_b128 v[186:189], v148 offset:5120
	ds_read_b128 v[190:193], v148 offset:6144
	ds_read_b128 v[194:197], v148 offset:7168
	global_load_lds_dwordx4 v[142:143], off
	v_lshl_add_u64 v[142:143], s[56:57], 0, v[136:137]
	s_add_i32 m0, s33, 0xe000
	s_nop 0
	global_load_lds_dwordx4 v[142:143], off
	s_waitcnt lgkmcnt(8)
	s_barrier
	s_waitcnt lgkmcnt(0)
	s_setprio 1
	s_waitcnt lgkmcnt(0)
	v_mfma_f32_16x16x32_bf16 v[126:129], v[150:153], v[166:169], 0
	v_mfma_f32_16x16x32_bf16 v[122:125], v[158:161], v[166:169], 0
	v_mfma_f32_16x16x32_bf16 v[118:121], v[150:153], v[174:177], 0
	v_mfma_f32_16x16x32_bf16 v[114:117], v[158:161], v[174:177], 0
	v_mfma_f32_16x16x32_bf16 v[94:97], v[150:153], v[182:185], 0
	v_mfma_f32_16x16x32_bf16 v[90:93], v[158:161], v[182:185], 0
	v_mfma_f32_16x16x32_bf16 v[86:89], v[150:153], v[190:193], 0
	v_mfma_f32_16x16x32_bf16 v[82:85], v[158:161], v[190:193], 0
	v_mfma_f32_16x16x32_bf16 v[126:129], v[154:157], v[170:173], v[126:129]
	v_mfma_f32_16x16x32_bf16 v[122:125], v[162:165], v[170:173], v[122:125]
	v_mfma_f32_16x16x32_bf16 v[118:121], v[154:157], v[178:181], v[118:121]
	v_mfma_f32_16x16x32_bf16 v[114:117], v[162:165], v[178:181], v[114:117]
	v_mfma_f32_16x16x32_bf16 v[94:97], v[154:157], v[186:189], v[94:97]
	v_mfma_f32_16x16x32_bf16 v[90:93], v[162:165], v[186:189], v[90:93]
	v_mfma_f32_16x16x32_bf16 v[86:89], v[154:157], v[194:197], v[86:89]
	v_mfma_f32_16x16x32_bf16 v[82:85], v[162:165], v[194:197], v[82:85]
	s_setprio 0
	s_barrier
	s_add_i32 s76, s64, s26
	v_lshl_add_u64 v[142:143], s[58:59], 0, v[130:131]
	s_mov_b32 m0, s76
	ds_read_b128 v[198:201], v149
	ds_read_b128 v[202:205], v149 offset:1024
	ds_read_b128 v[206:209], v149 offset:2048
	ds_read_b128 v[210:213], v149 offset:3072
	global_load_lds_dwordx4 v[142:143], off
	v_lshl_add_u64 v[214:215], s[58:59], 0, v[132:133]
	s_add_i32 m0, s76, 0x2000
	s_nop 0
	global_load_lds_dwordx4 v[214:215], off
	s_barrier
	s_waitcnt lgkmcnt(0)
	s_setprio 1
	s_waitcnt lgkmcnt(0)
	v_mfma_f32_16x16x32_bf16 v[110:113], v[198:201], v[166:169], 0
	v_mfma_f32_16x16x32_bf16 v[106:109], v[206:209], v[166:169], 0
	v_mfma_f32_16x16x32_bf16 v[102:105], v[198:201], v[174:177], 0
	v_mfma_f32_16x16x32_bf16 v[98:101], v[206:209], v[174:177], 0
	v_mfma_f32_16x16x32_bf16 v[78:81], v[198:201], v[182:185], 0
	v_mfma_f32_16x16x32_bf16 v[74:77], v[206:209], v[182:185], 0
	v_mfma_f32_16x16x32_bf16 v[70:73], v[198:201], v[190:193], 0
	v_mfma_f32_16x16x32_bf16 v[66:69], v[206:209], v[190:193], 0
	v_mfma_f32_16x16x32_bf16 v[110:113], v[202:205], v[170:173], v[110:113]
	v_mfma_f32_16x16x32_bf16 v[106:109], v[210:213], v[170:173], v[106:109]
	v_mfma_f32_16x16x32_bf16 v[102:105], v[202:205], v[178:181], v[102:105]
	v_mfma_f32_16x16x32_bf16 v[98:101], v[210:213], v[178:181], v[98:101]
	v_mfma_f32_16x16x32_bf16 v[78:81], v[202:205], v[186:189], v[78:81]
	v_mfma_f32_16x16x32_bf16 v[74:77], v[210:213], v[186:189], v[74:77]
	v_mfma_f32_16x16x32_bf16 v[70:73], v[202:205], v[194:197], v[70:73]
	v_mfma_f32_16x16x32_bf16 v[66:69], v[210:213], v[194:197], v[66:69]
	s_setprio 0
	s_mov_b32 m0, s33
	v_lshl_add_u64 v[216:217], s[60:61], 0, v[130:131]
	s_barrier
	ds_read_b128 v[166:169], v148 offset:16384
	ds_read_b128 v[170:173], v148 offset:17408
	ds_read_b128 v[174:177], v148 offset:18432
	ds_read_b128 v[178:181], v148 offset:19456
	ds_read_b128 v[182:185], v148 offset:20480
	ds_read_b128 v[186:189], v148 offset:21504
	ds_read_b128 v[190:193], v148 offset:22528
	ds_read_b128 v[194:197], v148 offset:23552
	global_load_lds_dwordx4 v[216:217], off
	v_lshl_add_u64 v[220:221], s[60:61], 0, v[132:133]
	s_mov_b32 m0, s34
	s_nop 0
	global_load_lds_dwordx4 v[220:221], off
	s_barrier
	s_waitcnt lgkmcnt(0)
	s_setprio 1
	s_waitcnt lgkmcnt(0)
	v_mfma_f32_16x16x32_bf16 v[62:65], v[150:153], v[166:169], 0
	v_mfma_f32_16x16x32_bf16 v[58:61], v[158:161], v[166:169], 0
	v_mfma_f32_16x16x32_bf16 v[54:57], v[150:153], v[174:177], 0
	v_mfma_f32_16x16x32_bf16 v[50:53], v[158:161], v[174:177], 0
	v_mfma_f32_16x16x32_bf16 v[30:33], v[150:153], v[182:185], 0
	v_mfma_f32_16x16x32_bf16 v[26:29], v[158:161], v[182:185], 0
	v_mfma_f32_16x16x32_bf16 v[22:25], v[150:153], v[190:193], 0
	v_mfma_f32_16x16x32_bf16 v[14:17], v[158:161], v[190:193], 0
	v_mfma_f32_16x16x32_bf16 v[62:65], v[154:157], v[170:173], v[62:65]
	v_mfma_f32_16x16x32_bf16 v[58:61], v[162:165], v[170:173], v[58:61]
	v_mfma_f32_16x16x32_bf16 v[54:57], v[154:157], v[178:181], v[54:57]
	v_mfma_f32_16x16x32_bf16 v[50:53], v[162:165], v[178:181], v[50:53]
	v_mfma_f32_16x16x32_bf16 v[30:33], v[154:157], v[186:189], v[30:33]
	v_mfma_f32_16x16x32_bf16 v[26:29], v[162:165], v[186:189], v[26:29]
	v_mfma_f32_16x16x32_bf16 v[22:25], v[154:157], v[194:197], v[22:25]
	v_mfma_f32_16x16x32_bf16 v[14:17], v[162:165], v[194:197], v[14:17]
	s_setprio 0
	s_barrier
	s_add_u32 s76, s58, 0x80000
	s_addc_u32 s77, s59, 0
	s_add_i32 s78, s65, s26
	v_lshl_add_u64 v[150:151], s[76:77], 0, v[130:131]
	s_mov_b32 m0, s78
	s_nop 0
	global_load_lds_dwordx4 v[150:151], off
	v_lshl_add_u64 v[150:151], s[76:77], 0, v[132:133]
	s_add_i32 m0, s78, 0x2000
	s_nop 0
	global_load_lds_dwordx4 v[150:151], off
	s_waitcnt vmcnt(6)
	s_barrier
	s_setprio 1
	v_mfma_f32_16x16x32_bf16 v[46:49], v[198:201], v[166:169], 0
	v_mfma_f32_16x16x32_bf16 v[42:45], v[206:209], v[166:169], 0
	v_mfma_f32_16x16x32_bf16 v[38:41], v[198:201], v[174:177], 0
	v_mfma_f32_16x16x32_bf16 v[34:37], v[206:209], v[174:177], 0
	v_mfma_f32_16x16x32_bf16 v[18:21], v[198:201], v[182:185], 0
	v_mfma_f32_16x16x32_bf16 v[10:13], v[206:209], v[182:185], 0
	v_mfma_f32_16x16x32_bf16 v[6:9], v[198:201], v[190:193], 0
	v_mfma_f32_16x16x32_bf16 v[2:5], v[206:209], v[190:193], 0
	v_mfma_f32_16x16x32_bf16 v[46:49], v[202:205], v[170:173], v[46:49]
	v_mfma_f32_16x16x32_bf16 v[42:45], v[210:213], v[170:173], v[42:45]
	v_mfma_f32_16x16x32_bf16 v[38:41], v[202:205], v[178:181], v[38:41]
	v_mfma_f32_16x16x32_bf16 v[34:37], v[210:213], v[178:181], v[34:37]
	v_mfma_f32_16x16x32_bf16 v[18:21], v[202:205], v[186:189], v[18:21]
	v_mfma_f32_16x16x32_bf16 v[10:13], v[210:213], v[186:189], v[10:13]
	v_mfma_f32_16x16x32_bf16 v[6:9], v[202:205], v[194:197], v[6:9]
	v_mfma_f32_16x16x32_bf16 v[2:5], v[210:213], v[194:197], v[2:5]
	s_setprio 0
	s_add_i32 s76, 0, 0x18000
	v_add_u32_e32 v1, s76, v145
	s_barrier
	ds_read_b128 v[150:153], v1
	ds_read_b128 v[154:157], v1 offset:1024
	ds_read_b128 v[158:161], v1 offset:2048
	ds_read_b128 v[162:165], v1 offset:3072
	s_add_u32 s60, s60, 0x80000
	s_addc_u32 s61, s61, 0
	s_mov_b32 m0, s35
	v_lshl_add_u64 v[198:199], s[60:61], 0, v[130:131]
	ds_read_b128 v[166:169], v148 offset:32768
	ds_read_b128 v[170:173], v148 offset:33792
	ds_read_b128 v[174:177], v148 offset:34816
	ds_read_b128 v[178:181], v148 offset:35840
	ds_read_b128 v[182:185], v148 offset:36864
	ds_read_b128 v[186:189], v148 offset:37888
	ds_read_b128 v[190:193], v148 offset:38912
	ds_read_b128 v[194:197], v148 offset:39936
	global_load_lds_dwordx4 v[198:199], off
	v_lshl_add_u64 v[198:199], s[60:61], 0, v[132:133]
	s_mov_b32 m0, s40
	s_nop 0
	global_load_lds_dwordx4 v[198:199], off
	s_waitcnt lgkmcnt(8)
	s_barrier
	s_waitcnt lgkmcnt(0)
	s_setprio 1
	s_waitcnt lgkmcnt(0)
	v_mfma_f32_16x16x32_bf16 v[126:129], v[150:153], v[166:169], v[126:129]
	v_mfma_f32_16x16x32_bf16 v[122:125], v[158:161], v[166:169], v[122:125]
	v_mfma_f32_16x16x32_bf16 v[118:121], v[150:153], v[174:177], v[118:121]
	v_mfma_f32_16x16x32_bf16 v[114:117], v[158:161], v[174:177], v[114:117]
	v_mfma_f32_16x16x32_bf16 v[94:97], v[150:153], v[182:185], v[94:97]
	v_mfma_f32_16x16x32_bf16 v[90:93], v[158:161], v[182:185], v[90:93]
	v_mfma_f32_16x16x32_bf16 v[86:89], v[150:153], v[190:193], v[86:89]
	v_mfma_f32_16x16x32_bf16 v[82:85], v[158:161], v[190:193], v[82:85]
	v_mfma_f32_16x16x32_bf16 v[126:129], v[154:157], v[170:173], v[126:129]
	v_mfma_f32_16x16x32_bf16 v[122:125], v[162:165], v[170:173], v[122:125]
	v_mfma_f32_16x16x32_bf16 v[118:121], v[154:157], v[178:181], v[118:121]
	v_mfma_f32_16x16x32_bf16 v[114:117], v[162:165], v[178:181], v[114:117]
	v_mfma_f32_16x16x32_bf16 v[94:97], v[154:157], v[186:189], v[94:97]
	v_mfma_f32_16x16x32_bf16 v[90:93], v[162:165], v[186:189], v[90:93]
	v_mfma_f32_16x16x32_bf16 v[86:89], v[154:157], v[194:197], v[86:89]
	v_mfma_f32_16x16x32_bf16 v[82:85], v[162:165], v[194:197], v[82:85]
	s_setprio 0
	s_barrier
	s_add_i32 s60, 0, 0x1c000
	s_add_i32 s61, s76, s26
	v_add_u32_e32 v1, s60, v145
	v_lshl_add_u64 v[142:143], v[142:143], 0, s[8:9]
	s_mov_b32 m0, s61
	ds_read_b128 v[198:201], v1
	ds_read_b128 v[202:205], v1 offset:1024
	ds_read_b128 v[206:209], v1 offset:2048
	ds_read_b128 v[210:213], v1 offset:3072
	global_load_lds_dwordx4 v[142:143], off
	v_lshl_add_u64 v[142:143], v[214:215], 0, s[8:9]
	s_add_i32 m0, s61, 0x2000
	s_nop 0
	global_load_lds_dwordx4 v[142:143], off
	s_barrier
	s_waitcnt lgkmcnt(0)
	s_setprio 1
	s_waitcnt lgkmcnt(0)
	v_mfma_f32_16x16x32_bf16 v[110:113], v[198:201], v[166:169], v[110:113]
	v_mfma_f32_16x16x32_bf16 v[106:109], v[206:209], v[166:169], v[106:109]
	v_mfma_f32_16x16x32_bf16 v[102:105], v[198:201], v[174:177], v[102:105]
	v_mfma_f32_16x16x32_bf16 v[98:101], v[206:209], v[174:177], v[98:101]
	v_mfma_f32_16x16x32_bf16 v[78:81], v[198:201], v[182:185], v[78:81]
	v_mfma_f32_16x16x32_bf16 v[74:77], v[206:209], v[182:185], v[74:77]
	v_mfma_f32_16x16x32_bf16 v[70:73], v[198:201], v[190:193], v[70:73]
	v_mfma_f32_16x16x32_bf16 v[66:69], v[206:209], v[190:193], v[66:69]
	v_mfma_f32_16x16x32_bf16 v[110:113], v[202:205], v[170:173], v[110:113]
	v_mfma_f32_16x16x32_bf16 v[106:109], v[210:213], v[170:173], v[106:109]
	v_mfma_f32_16x16x32_bf16 v[102:105], v[202:205], v[178:181], v[102:105]
	v_mfma_f32_16x16x32_bf16 v[98:101], v[210:213], v[178:181], v[98:101]
	v_mfma_f32_16x16x32_bf16 v[78:81], v[202:205], v[186:189], v[78:81]
	v_mfma_f32_16x16x32_bf16 v[74:77], v[210:213], v[186:189], v[74:77]
	v_mfma_f32_16x16x32_bf16 v[70:73], v[202:205], v[194:197], v[70:73]
	v_mfma_f32_16x16x32_bf16 v[66:69], v[210:213], v[194:197], v[66:69]
	s_setprio 0
	s_mov_b32 m0, s55
	v_lshl_add_u64 v[142:143], v[216:217], 0, s[8:9]
	s_barrier
	ds_read_b128 v[166:169], v148 offset:49152
	ds_read_b128 v[170:173], v148 offset:50176
	ds_read_b128 v[174:177], v148 offset:51200
	ds_read_b128 v[178:181], v148 offset:52224
	ds_read_b128 v[182:185], v148 offset:53248
	ds_read_b128 v[186:189], v148 offset:54272
	ds_read_b128 v[190:193], v148 offset:55296
	ds_read_b128 v[194:197], v148 offset:56320
	global_load_lds_dwordx4 v[142:143], off
	v_lshl_add_u64 v[142:143], v[220:221], 0, s[8:9]
	s_mov_b32 m0, s62
	s_nop 0
	global_load_lds_dwordx4 v[142:143], off
	s_barrier
	s_waitcnt lgkmcnt(0)
	s_setprio 1
	s_waitcnt lgkmcnt(0)
	v_mfma_f32_16x16x32_bf16 v[62:65], v[150:153], v[166:169], v[62:65]
	v_mfma_f32_16x16x32_bf16 v[58:61], v[158:161], v[166:169], v[58:61]
	v_mfma_f32_16x16x32_bf16 v[54:57], v[150:153], v[174:177], v[54:57]
	v_mfma_f32_16x16x32_bf16 v[50:53], v[158:161], v[174:177], v[50:53]
	v_mfma_f32_16x16x32_bf16 v[30:33], v[150:153], v[182:185], v[30:33]
	v_mfma_f32_16x16x32_bf16 v[26:29], v[158:161], v[182:185], v[26:29]
	v_mfma_f32_16x16x32_bf16 v[22:25], v[150:153], v[190:193], v[22:25]
	v_mfma_f32_16x16x32_bf16 v[14:17], v[158:161], v[190:193], v[14:17]
	v_mfma_f32_16x16x32_bf16 v[62:65], v[154:157], v[170:173], v[62:65]
	v_mfma_f32_16x16x32_bf16 v[58:61], v[162:165], v[170:173], v[58:61]
	v_mfma_f32_16x16x32_bf16 v[54:57], v[154:157], v[178:181], v[54:57]
	v_mfma_f32_16x16x32_bf16 v[50:53], v[162:165], v[178:181], v[50:53]
	v_mfma_f32_16x16x32_bf16 v[30:33], v[154:157], v[186:189], v[30:33]
	v_mfma_f32_16x16x32_bf16 v[26:29], v[162:165], v[186:189], v[26:29]
	v_mfma_f32_16x16x32_bf16 v[22:25], v[154:157], v[194:197], v[22:25]
	v_mfma_f32_16x16x32_bf16 v[14:17], v[162:165], v[194:197], v[14:17]
	s_setprio 0
	s_barrier
	s_add_u32 s58, s58, 0x80080
	s_addc_u32 s59, s59, 0
	s_add_i32 s60, s60, s26
	v_lshl_add_u64 v[142:143], s[58:59], 0, v[130:131]
	s_mov_b32 m0, s60
	s_nop 0
	global_load_lds_dwordx4 v[142:143], off
	v_lshl_add_u64 v[142:143], s[58:59], 0, v[132:133]
	s_add_i32 m0, s60, 0x2000
	s_nop 0
	global_load_lds_dwordx4 v[142:143], off
	s_waitcnt vmcnt(6)
	s_barrier
	s_setprio 1
	v_mfma_f32_16x16x32_bf16 v[46:49], v[198:201], v[166:169], v[46:49]
	v_mfma_f32_16x16x32_bf16 v[42:45], v[206:209], v[166:169], v[42:45]
	v_mfma_f32_16x16x32_bf16 v[38:41], v[198:201], v[174:177], v[38:41]
	v_mfma_f32_16x16x32_bf16 v[34:37], v[206:209], v[174:177], v[34:37]
	v_mfma_f32_16x16x32_bf16 v[18:21], v[198:201], v[182:185], v[18:21]
	v_mfma_f32_16x16x32_bf16 v[10:13], v[206:209], v[182:185], v[10:13]
	v_mfma_f32_16x16x32_bf16 v[6:9], v[198:201], v[190:193], v[6:9]
	v_mfma_f32_16x16x32_bf16 v[2:5], v[206:209], v[190:193], v[2:5]
	v_mfma_f32_16x16x32_bf16 v[46:49], v[202:205], v[170:173], v[46:49]
	v_mfma_f32_16x16x32_bf16 v[42:45], v[210:213], v[170:173], v[42:45]
	v_mfma_f32_16x16x32_bf16 v[38:41], v[202:205], v[178:181], v[38:41]
	v_mfma_f32_16x16x32_bf16 v[34:37], v[210:213], v[178:181], v[34:37]
	v_mfma_f32_16x16x32_bf16 v[18:21], v[202:205], v[186:189], v[18:21]
	v_mfma_f32_16x16x32_bf16 v[10:13], v[210:213], v[186:189], v[10:13]
	v_mfma_f32_16x16x32_bf16 v[6:9], v[202:205], v[194:197], v[6:9]
	v_mfma_f32_16x16x32_bf16 v[2:5], v[210:213], v[194:197], v[2:5]
	s_setprio 0
	s_add_i32 s75, s75, 2
	s_add_u32 s56, s56, 0x100
	s_addc_u32 s57, s57, 0
	s_add_u32 s73, s73, 0x100
	s_addc_u32 s74, s74, 0
	s_cmp_gt_u32 s75, 29
	s_barrier
	s_cbranch_scc1 .Lpeel_1239_after

.Lpeel_1239_after:
	v_lshl_add_u32 v182, s54, 8, v144
	v_lshl_or_b32 v142, s70, 8, v146
	v_or_b32_e32 v166, 16, v182
	v_ashrrev_i32_e32 v143, 31, v142
	v_ashrrev_i32_e32 v183, 31, v182
	v_ashrrev_i32_e32 v167, 31, v166
	v_lshl_add_u64 v[184:185], v[142:143], 2, s[50:51]
	v_lshlrev_b64 v[142:143], 13, v[182:183]
	v_lshlrev_b64 v[166:167], 13, v[166:167]
	v_lshl_add_u64 v[142:143], v[184:185], 0, v[142:143]
	v_lshl_add_u64 v[186:187], v[184:185], 0, v[166:167]
	global_load_dwordx4 v[150:153], v[142:143], off
	global_load_dwordx4 v[154:157], v[142:143], off offset:64
	global_load_dwordx4 v[158:161], v[142:143], off offset:512
	global_load_dwordx4 v[162:165], v[142:143], off offset:576
	global_load_dwordx4 v[166:169], v[186:187], off
	global_load_dwordx4 v[170:173], v[186:187], off offset:64
	global_load_dwordx4 v[174:177], v[186:187], off offset:512
	global_load_dwordx4 v[178:181], v[186:187], off offset:576
	s_mov_b32 s70, s18
	s_mov_b32 s54, s20
	s_mov_b64 s[58:59], s[24:25]
	s_mov_b64 s[56:57], s[22:23]
	s_waitcnt vmcnt(0)
	v_pk_add_f32 v[128:129], v[128:129], v[152:153]
	v_pk_add_f32 v[126:127], v[126:127], v[150:151]
	v_pk_add_f32 v[124:125], v[124:125], v[156:157]
	v_pk_add_f32 v[108:109], v[108:109], v[164:165]
	v_pk_add_f32 v[100:101], v[100:101], v[180:181]
	v_pk_add_f32 v[98:99], v[98:99], v[178:179]
	v_pk_add_f32 v[106:107], v[106:107], v[162:163]
	global_store_dwordx4 v[186:187], v[98:101], off offset:576
	global_store_dwordx4 v[142:143], v[106:109], off offset:576
	v_pk_add_f32 v[122:123], v[122:123], v[154:155]
	v_or_b32_e32 v98, 32, v182
	v_pk_add_f32 v[108:109], v[120:121], v[168:169]
	v_pk_add_f32 v[106:107], v[118:119], v[166:167]
	v_ashrrev_i32_e32 v99, 31, v98
	v_pk_add_f32 v[112:113], v[112:113], v[160:161]
	v_pk_add_f32 v[110:111], v[110:111], v[158:159]
	global_store_dwordx4 v[186:187], v[106:109], off
	v_pk_add_f32 v[104:105], v[104:105], v[176:177]
	v_pk_add_f32 v[102:103], v[102:103], v[174:175]
	v_pk_add_f32 v[108:109], v[116:117], v[172:173]
	v_pk_add_f32 v[106:107], v[114:115], v[170:171]
	v_lshlrev_b64 v[98:99], 13, v[98:99]
	v_or_b32_e32 v114, 48, v182
	global_store_dwordx4 v[142:143], v[126:129], off
	global_store_dwordx4 v[142:143], v[122:125], off offset:64
	global_store_dwordx4 v[142:143], v[110:113], off offset:512
	global_store_dwordx4 v[186:187], v[106:109], off offset:64
	global_store_dwordx4 v[186:187], v[102:105], off offset:512
	v_lshl_add_u64 v[150:151], v[184:185], 0, v[98:99]
	v_ashrrev_i32_e32 v115, 31, v114
	global_load_dwordx4 v[98:101], v[150:151], off
	global_load_dwordx4 v[102:105], v[150:151], off offset:64
	global_load_dwordx4 v[106:109], v[150:151], off offset:512
	global_load_dwordx4 v[110:113], v[150:151], off offset:576
	v_lshlrev_b64 v[114:115], 13, v[114:115]
	v_lshl_add_u64 v[152:153], v[184:185], 0, v[114:115]
	global_load_dwordx4 v[114:117], v[152:153], off
	global_load_dwordx4 v[118:121], v[152:153], off offset:64
	global_load_dwordx4 v[122:125], v[152:153], off offset:512
	global_load_dwordx4 v[126:129], v[152:153], off offset:576
	s_waitcnt vmcnt(0)
	v_pk_add_f32 v[96:97], v[96:97], v[100:101]
	v_pk_add_f32 v[94:95], v[94:95], v[98:99]
	v_pk_add_f32 v[92:93], v[92:93], v[104:105]
	v_pk_add_f32 v[76:77], v[76:77], v[112:113]
	v_pk_add_f32 v[74:75], v[74:75], v[110:111]
	global_store_dwordx4 v[150:151], v[74:77], off offset:576
	v_pk_add_f32 v[90:91], v[90:91], v[102:103]
	v_pk_add_f32 v[80:81], v[80:81], v[108:109]
	v_pk_add_f32 v[76:77], v[88:89], v[116:117]
	v_pk_add_f32 v[74:75], v[86:87], v[114:115]
	v_pk_add_f32 v[78:79], v[78:79], v[106:107]
	global_store_dwordx4 v[152:153], v[74:77], off
	v_pk_add_f32 v[72:73], v[72:73], v[124:125]
	v_pk_add_f32 v[70:71], v[70:71], v[122:123]
	v_pk_add_f32 v[76:77], v[84:85], v[120:121]
	v_pk_add_f32 v[74:75], v[82:83], v[118:119]
	v_pk_add_f32 v[68:69], v[68:69], v[128:129]
	v_pk_add_f32 v[66:67], v[66:67], v[126:127]
	v_add_co_u32_e32 v100, vcc, s66, v142
	global_store_dwordx4 v[150:151], v[94:97], off
	global_store_dwordx4 v[150:151], v[90:93], off offset:64
	global_store_dwordx4 v[150:151], v[78:81], off offset:512
	global_store_dwordx4 v[152:153], v[74:77], off offset:64
	global_store_dwordx4 v[152:153], v[70:73], off offset:512
	global_store_dwordx4 v[152:153], v[66:69], off offset:576
	v_addc_co_u32_e32 v101, vcc, 0, v143, vcc
	v_lshl_add_u64 v[98:99], v[142:143], 0, s[10:11]
	global_load_dwordx4 v[66:69], v[100:101], off
	global_load_dwordx4 v[70:73], v[98:99], off offset:64
	global_load_dwordx4 v[74:77], v[98:99], off offset:512
	global_load_dwordx4 v[78:81], v[98:99], off offset:576
	v_add_co_u32_e32 v104, vcc, s67, v142
	v_lshl_add_u64 v[102:103], v[142:143], 0, s[12:13]
	s_nop 0
	v_addc_co_u32_e32 v105, vcc, 0, v143, vcc
	global_load_dwordx4 v[82:85], v[104:105], off
	global_load_dwordx4 v[86:89], v[102:103], off offset:64
	global_load_dwordx4 v[90:93], v[102:103], off offset:512
	global_load_dwordx4 v[94:97], v[102:103], off offset:576
	s_waitcnt vmcnt(0)
	v_pk_add_f32 v[64:65], v[64:65], v[68:69]
	v_pk_add_f32 v[62:63], v[62:63], v[66:67]
	v_pk_add_f32 v[48:49], v[48:49], v[76:77]
	v_pk_add_f32 v[44:45], v[44:45], v[80:81]
	v_pk_add_f32 v[42:43], v[42:43], v[78:79]
	v_pk_add_f32 v[46:47], v[46:47], v[74:75]
	global_store_dwordx4 v[98:99], v[42:45], off offset:576
	v_pk_add_f32 v[60:61], v[60:61], v[72:73]
	v_pk_add_f32 v[58:59], v[58:59], v[70:71]
	v_pk_add_f32 v[44:45], v[56:57], v[84:85]
	v_pk_add_f32 v[42:43], v[54:55], v[82:83]
	global_store_dwordx4 v[98:99], v[46:49], off offset:512
	global_store_dwordx4 v[104:105], v[42:45], off
	v_pk_add_f32 v[40:41], v[40:41], v[92:93]
	v_pk_add_f32 v[38:39], v[38:39], v[90:91]
	v_pk_add_f32 v[44:45], v[52:53], v[88:89]
	v_pk_add_f32 v[42:43], v[50:51], v[86:87]
	v_pk_add_f32 v[36:37], v[36:37], v[96:97]
	v_pk_add_f32 v[34:35], v[34:35], v[94:95]
	v_add_co_u32_e32 v46, vcc, s68, v142
	global_store_dwordx4 v[100:101], v[62:65], off
	global_store_dwordx4 v[98:99], v[58:61], off offset:64
	global_store_dwordx4 v[102:103], v[42:45], off offset:64
	global_store_dwordx4 v[102:103], v[38:41], off offset:512
	global_store_dwordx4 v[102:103], v[34:37], off offset:576
	v_addc_co_u32_e32 v47, vcc, 0, v143, vcc
	v_lshl_add_u64 v[42:43], v[142:143], 0, s[14:15]
	global_load_dwordx4 v[50:53], v[46:47], off
	global_load_dwordx4 v[54:57], v[42:43], off offset:64
	global_load_dwordx4 v[58:61], v[42:43], off offset:512
	global_load_dwordx4 v[62:65], v[42:43], off offset:576
	v_add_co_u32_e32 v48, vcc, s69, v142
	v_lshl_add_u64 v[44:45], v[142:143], 0, s[16:17]
	s_nop 0
	v_addc_co_u32_e32 v49, vcc, 0, v143, vcc
	global_load_dwordx4 v[66:69], v[48:49], off
	global_load_dwordx4 v[70:73], v[44:45], off offset:64
	global_load_dwordx4 v[38:41], v[44:45], off offset:512
	global_load_dwordx4 v[34:37], v[44:45], off offset:576
	s_and_b64 vcc, exec, s[0:1]
	s_waitcnt vmcnt(0)
	v_pk_add_f32 v[32:33], v[32:33], v[52:53]
	v_pk_add_f32 v[30:31], v[30:31], v[50:51]
	v_pk_add_f32 v[28:29], v[28:29], v[56:57]
	v_pk_add_f32 v[12:13], v[12:13], v[64:65]
	v_pk_add_f32 v[10:11], v[10:11], v[62:63]
	global_store_dwordx4 v[42:43], v[10:13], off offset:576
	v_pk_add_f32 v[26:27], v[26:27], v[54:55]
	v_pk_add_f32 v[20:21], v[20:21], v[60:61]
	v_pk_add_f32 v[12:13], v[24:25], v[68:69]
	v_pk_add_f32 v[10:11], v[22:23], v[66:67]
	v_pk_add_f32 v[18:19], v[18:19], v[58:59]
	global_store_dwordx4 v[48:49], v[10:13], off
	v_pk_add_f32 v[8:9], v[8:9], v[40:41]
	v_pk_add_f32 v[6:7], v[6:7], v[38:39]
	v_pk_add_f32 v[12:13], v[16:17], v[72:73]
	v_pk_add_f32 v[10:11], v[14:15], v[70:71]
	v_pk_add_f32 v[4:5], v[4:5], v[36:37]
	v_pk_add_f32 v[2:3], v[2:3], v[34:35]
	global_store_dwordx4 v[46:47], v[30:33], off
	global_store_dwordx4 v[42:43], v[26:29], off offset:64
	global_store_dwordx4 v[42:43], v[18:21], off offset:512
	global_store_dwordx4 v[44:45], v[10:13], off offset:64
	global_store_dwordx4 v[44:45], v[6:9], off offset:512
	global_store_dwordx4 v[44:45], v[2:5], off offset:576
	s_cbranch_vccz .LBB0_1232
	s_waitcnt vmcnt(0)
	s_cmpk_gt_u32 s2, 0xff
	s_cbranch_scc1 .LBB0_1243
	s_barrier

.LBB0_1521:
	s_ashr_i32 s9, s8, 31
	s_lshl_b64 s[10:11], s[8:9], 20
	s_add_u32 s10, s25, s10
	s_addc_u32 s11, s26, s11
	s_and_b64 s[14:15], s[14:15], exec
	s_cselect_b32 s9, s11, s13
	s_cselect_b32 s58, s10, s12
	v_mov_b32_e32 v139, v135
	v_mov_b32_e32 v141, v135
	s_add_u32 s59, s12, 0x100
	v_mov_b32_e32 v2, 0
	v_lshl_add_u64 v[142:143], s[6:7], 0, v[140:141]
	v_lshl_add_u64 v[144:145], s[6:7], 0, v[138:139]
	s_addc_u32 s60, s13, 0
	s_mov_b32 s61, -2
	s_mov_b64 s[12:13], 0
	s_add_u32 s14, s28, s12
	s_addc_u32 s15, s29, s13
	s_add_u32 s16, s14, 0x2a300100
	ds_read_b128 v[158:161], v151
	ds_read_b128 v[162:165], v151 offset:1024
	ds_read_b128 v[166:169], v151 offset:2048
	ds_read_b128 v[170:173], v151 offset:3072
	s_addc_u32 s17, s15, 0
	s_add_u32 s62, s59, s12
	s_addc_u32 s63, s60, s13
	s_cmpk_eq_i32 s12, 0xf00
	s_cselect_b64 vcc, -1, 0
	s_and_b64 s[14:15], vcc, exec
	v_cndmask_b32_e32 v134, v137, v154, vcc
	v_cndmask_b32_e32 v222, v136, v155, vcc
	v_cndmask_b32_e32 v139, v138, v156, vcc
	v_cndmask_b32_e32 v141, v140, v157, vcc
	s_cselect_b32 s17, s37, s17
	s_cselect_b32 s16, s36, s16
	s_cselect_b32 s15, s9, s63
	s_cselect_b32 s14, s58, s62
	v_lshl_add_u64 v[206:207], v[144:145], 0, s[12:13]
	s_add_i32 m0, s34, 0xc000
	ds_read_b128 v[174:177], v152
	ds_read_b128 v[178:181], v152 offset:1024
	ds_read_b128 v[182:185], v152 offset:2048
	ds_read_b128 v[186:189], v152 offset:3072
	ds_read_b128 v[190:193], v152 offset:4096
	ds_read_b128 v[194:197], v152 offset:5120
	ds_read_b128 v[198:201], v152 offset:6144
	ds_read_b128 v[202:205], v152 offset:7168
	global_load_lds_dwordx4 v[206:207], off
	v_lshl_add_u64 v[206:207], v[142:143], 0, s[12:13]
	s_add_i32 m0, s34, 0xe000
	s_nop 0
	global_load_lds_dwordx4 v[206:207], off
	s_waitcnt lgkmcnt(8)
	s_barrier
	s_waitcnt lgkmcnt(0)
	s_setprio 1
	s_waitcnt lgkmcnt(0)
	v_mfma_f32_16x16x32_bf16 v[126:129], v[158:161], v[174:177], 0
	v_mfma_f32_16x16x32_bf16 v[122:125], v[166:169], v[174:177], 0
	v_mfma_f32_16x16x32_bf16 v[110:113], v[158:161], v[182:185], 0
	v_mfma_f32_16x16x32_bf16 v[106:109], v[166:169], v[182:185], 0
	v_mfma_f32_16x16x32_bf16 v[94:97], v[158:161], v[190:193], 0
	v_mfma_f32_16x16x32_bf16 v[90:93], v[166:169], v[190:193], 0
	v_mfma_f32_16x16x32_bf16 v[78:81], v[158:161], v[198:201], 0
	v_mfma_f32_16x16x32_bf16 v[74:77], v[166:169], v[198:201], 0
	v_mfma_f32_16x16x32_bf16 v[126:129], v[162:165], v[178:181], v[126:129]
	v_mfma_f32_16x16x32_bf16 v[122:125], v[170:173], v[178:181], v[122:125]
	v_mfma_f32_16x16x32_bf16 v[110:113], v[162:165], v[186:189], v[110:113]
	v_mfma_f32_16x16x32_bf16 v[106:109], v[170:173], v[186:189], v[106:109]
	v_mfma_f32_16x16x32_bf16 v[94:97], v[162:165], v[194:197], v[94:97]
	v_mfma_f32_16x16x32_bf16 v[90:93], v[170:173], v[194:197], v[90:93]
	v_mfma_f32_16x16x32_bf16 v[78:81], v[162:165], v[202:205], v[78:81]
	v_mfma_f32_16x16x32_bf16 v[74:77], v[170:173], v[202:205], v[74:77]
	s_setprio 0
	s_barrier
	s_add_i32 s62, s42, s33
	v_lshl_add_u64 v[224:225], s[14:15], 0, v[132:133]
	s_mov_b32 m0, s62
	ds_read_b128 v[206:209], v153
	ds_read_b128 v[210:213], v153 offset:1024
	ds_read_b128 v[214:217], v153 offset:2048
	ds_read_b128 v[218:221], v153 offset:3072
	global_load_lds_dwordx4 v[224:225], off
	v_lshl_add_u64 v[226:227], s[14:15], 0, v[130:131]
	s_add_i32 m0, s62, 0x2000
	s_nop 0
	global_load_lds_dwordx4 v[226:227], off
	s_barrier
	s_waitcnt lgkmcnt(0)
	s_setprio 1
	s_waitcnt lgkmcnt(0)
	v_mfma_f32_16x16x32_bf16 v[118:121], v[206:209], v[174:177], 0
	v_mfma_f32_16x16x32_bf16 v[114:117], v[214:217], v[174:177], 0
	v_mfma_f32_16x16x32_bf16 v[102:105], v[206:209], v[182:185], 0
	v_mfma_f32_16x16x32_bf16 v[98:101], v[214:217], v[182:185], 0
	v_mfma_f32_16x16x32_bf16 v[86:89], v[206:209], v[190:193], 0
	v_mfma_f32_16x16x32_bf16 v[82:85], v[214:217], v[190:193], 0
	v_mfma_f32_16x16x32_bf16 v[70:73], v[206:209], v[198:201], 0
	v_mfma_f32_16x16x32_bf16 v[66:69], v[214:217], v[198:201], 0
	v_mfma_f32_16x16x32_bf16 v[118:121], v[210:213], v[178:181], v[118:121]
	v_mfma_f32_16x16x32_bf16 v[114:117], v[218:221], v[178:181], v[114:117]
	v_mfma_f32_16x16x32_bf16 v[102:105], v[210:213], v[186:189], v[102:105]
	v_mfma_f32_16x16x32_bf16 v[98:101], v[218:221], v[186:189], v[98:101]
	v_mfma_f32_16x16x32_bf16 v[86:89], v[210:213], v[194:197], v[86:89]
	v_mfma_f32_16x16x32_bf16 v[82:85], v[218:221], v[194:197], v[82:85]
	v_mfma_f32_16x16x32_bf16 v[70:73], v[210:213], v[202:205], v[70:73]
	v_mfma_f32_16x16x32_bf16 v[66:69], v[218:221], v[202:205], v[66:69]
	s_setprio 0
	s_mov_b32 m0, s34
	s_barrier
	ds_read_b128 v[174:177], v152 offset:16384
	ds_read_b128 v[178:181], v152 offset:17408
	ds_read_b128 v[182:185], v152 offset:18432
	ds_read_b128 v[186:189], v152 offset:19456
	ds_read_b128 v[190:193], v152 offset:20480
	ds_read_b128 v[194:197], v152 offset:21504
	ds_read_b128 v[198:201], v152 offset:22528
	ds_read_b128 v[202:205], v152 offset:23552
	global_load_lds_dwordx4 v134, s[16:17]
	s_mov_b32 m0, s35
	v_mov_b32_e32 v223, v135
	global_load_lds_dwordx4 v222, s[16:17]
	s_barrier
	s_waitcnt lgkmcnt(0)
	v_lshl_add_u64 v[228:229], s[16:17], 0, v[134:135]
	v_lshl_add_u64 v[222:223], s[16:17], 0, v[222:223]
	s_setprio 1
	s_waitcnt lgkmcnt(0)
	v_mfma_f32_16x16x32_bf16 v[62:65], v[158:161], v[174:177], 0
	v_mfma_f32_16x16x32_bf16 v[58:61], v[166:169], v[174:177], 0
	v_mfma_f32_16x16x32_bf16 v[46:49], v[158:161], v[182:185], 0
	v_mfma_f32_16x16x32_bf16 v[42:45], v[166:169], v[182:185], 0
	v_mfma_f32_16x16x32_bf16 v[30:33], v[158:161], v[190:193], 0
	v_mfma_f32_16x16x32_bf16 v[26:29], v[166:169], v[190:193], 0
	v_mfma_f32_16x16x32_bf16 v[14:17], v[158:161], v[198:201], 0
	v_mfma_f32_16x16x32_bf16 v[10:13], v[166:169], v[198:201], 0
	v_mfma_f32_16x16x32_bf16 v[62:65], v[162:165], v[178:181], v[62:65]
	v_mfma_f32_16x16x32_bf16 v[58:61], v[170:173], v[178:181], v[58:61]
	v_mfma_f32_16x16x32_bf16 v[46:49], v[162:165], v[186:189], v[46:49]
	v_mfma_f32_16x16x32_bf16 v[42:45], v[170:173], v[186:189], v[42:45]
	v_mfma_f32_16x16x32_bf16 v[30:33], v[162:165], v[194:197], v[30:33]
	v_mfma_f32_16x16x32_bf16 v[26:29], v[170:173], v[194:197], v[26:29]
	v_mfma_f32_16x16x32_bf16 v[14:17], v[162:165], v[202:205], v[14:17]
	v_mfma_f32_16x16x32_bf16 v[10:13], v[170:173], v[202:205], v[10:13]
	s_setprio 0
	s_barrier
	s_add_u32 s62, s14, 0x80000
	s_addc_u32 s63, s15, 0
	s_add_i32 s64, s43, s33
	v_lshl_add_u64 v[158:159], s[62:63], 0, v[132:133]
	s_mov_b32 m0, s64
	s_nop 0
	global_load_lds_dwordx4 v[158:159], off
	v_lshl_add_u64 v[158:159], s[62:63], 0, v[130:131]
	s_add_i32 m0, s64, 0x2000
	s_nop 0
	global_load_lds_dwordx4 v[158:159], off
	s_waitcnt vmcnt(6)
	s_barrier
	s_setprio 1
	v_mfma_f32_16x16x32_bf16 v[54:57], v[206:209], v[174:177], 0
	v_mfma_f32_16x16x32_bf16 v[50:53], v[214:217], v[174:177], 0
	v_mfma_f32_16x16x32_bf16 v[38:41], v[206:209], v[182:185], 0
	v_mfma_f32_16x16x32_bf16 v[34:37], v[214:217], v[182:185], 0
	v_mfma_f32_16x16x32_bf16 v[22:25], v[206:209], v[190:193], 0
	v_mfma_f32_16x16x32_bf16 v[18:21], v[214:217], v[190:193], 0
	v_mfma_f32_16x16x32_bf16 v[6:9], v[206:209], v[198:201], 0
	v_mfma_f32_16x16x32_bf16 v[2:5], v[214:217], v[198:201], 0
	v_mfma_f32_16x16x32_bf16 v[54:57], v[210:213], v[178:181], v[54:57]
	v_mfma_f32_16x16x32_bf16 v[50:53], v[218:221], v[178:181], v[50:53]
	v_mfma_f32_16x16x32_bf16 v[38:41], v[210:213], v[186:189], v[38:41]
	v_mfma_f32_16x16x32_bf16 v[34:37], v[218:221], v[186:189], v[34:37]
	v_mfma_f32_16x16x32_bf16 v[22:25], v[210:213], v[194:197], v[22:25]
	v_mfma_f32_16x16x32_bf16 v[18:21], v[218:221], v[194:197], v[18:21]
	v_mfma_f32_16x16x32_bf16 v[6:9], v[210:213], v[202:205], v[6:9]
	v_mfma_f32_16x16x32_bf16 v[2:5], v[218:221], v[202:205], v[2:5]
	s_setprio 0
	s_add_i32 s62, 0, 0x18000
	v_add_u32_e32 v134, s62, v149
	s_barrier
	ds_read_b128 v[158:161], v134
	ds_read_b128 v[162:165], v134 offset:1024
	ds_read_b128 v[166:169], v134 offset:2048
	ds_read_b128 v[170:173], v134 offset:3072
	s_mov_b32 m0, s38
	ds_read_b128 v[174:177], v152 offset:32768
	ds_read_b128 v[178:181], v152 offset:33792
	ds_read_b128 v[182:185], v152 offset:34816
	ds_read_b128 v[186:189], v152 offset:35840
	ds_read_b128 v[190:193], v152 offset:36864
	ds_read_b128 v[194:197], v152 offset:37888
	ds_read_b128 v[198:201], v152 offset:38912
	ds_read_b128 v[202:205], v152 offset:39936
	global_load_lds_dwordx4 v139, s[16:17]
	s_mov_b32 m0, s39
	s_nop 0
	global_load_lds_dwordx4 v141, s[16:17]
	s_waitcnt lgkmcnt(8)
	s_barrier
	s_waitcnt lgkmcnt(0)
	s_setprio 1
	s_waitcnt lgkmcnt(0)
	v_mfma_f32_16x16x32_bf16 v[126:129], v[158:161], v[174:177], v[126:129]
	v_mfma_f32_16x16x32_bf16 v[122:125], v[166:169], v[174:177], v[122:125]
	v_mfma_f32_16x16x32_bf16 v[110:113], v[158:161], v[182:185], v[110:113]
	v_mfma_f32_16x16x32_bf16 v[106:109], v[166:169], v[182:185], v[106:109]
	v_mfma_f32_16x16x32_bf16 v[94:97], v[158:161], v[190:193], v[94:97]
	v_mfma_f32_16x16x32_bf16 v[90:93], v[166:169], v[190:193], v[90:93]
	v_mfma_f32_16x16x32_bf16 v[78:81], v[158:161], v[198:201], v[78:81]
	v_mfma_f32_16x16x32_bf16 v[74:77], v[166:169], v[198:201], v[74:77]
	v_mfma_f32_16x16x32_bf16 v[126:129], v[162:165], v[178:181], v[126:129]
	v_mfma_f32_16x16x32_bf16 v[122:125], v[170:173], v[178:181], v[122:125]
	v_mfma_f32_16x16x32_bf16 v[110:113], v[162:165], v[186:189], v[110:113]
	v_mfma_f32_16x16x32_bf16 v[106:109], v[170:173], v[186:189], v[106:109]
	v_mfma_f32_16x16x32_bf16 v[94:97], v[162:165], v[194:197], v[94:97]
	v_mfma_f32_16x16x32_bf16 v[90:93], v[170:173], v[194:197], v[90:93]
	v_mfma_f32_16x16x32_bf16 v[78:81], v[162:165], v[202:205], v[78:81]
	v_mfma_f32_16x16x32_bf16 v[74:77], v[170:173], v[202:205], v[74:77]
	s_setprio 0
	s_barrier
	s_add_i32 s16, 0, 0x1c000
	s_add_i32 s17, s62, s33
	v_add_u32_e32 v134, s16, v149
	v_lshl_add_u64 v[224:225], v[224:225], 0, s[0:1]
	s_mov_b32 m0, s17
	ds_read_b128 v[206:209], v134
	ds_read_b128 v[210:213], v134 offset:1024
	ds_read_b128 v[214:217], v134 offset:2048
	ds_read_b128 v[218:221], v134 offset:3072
	global_load_lds_dwordx4 v[224:225], off
	v_lshl_add_u64 v[224:225], v[226:227], 0, s[0:1]
	s_add_i32 m0, s17, 0x2000
	s_nop 0
	global_load_lds_dwordx4 v[224:225], off
	s_barrier
	s_waitcnt lgkmcnt(0)
	s_setprio 1
	s_waitcnt lgkmcnt(0)
	v_mfma_f32_16x16x32_bf16 v[118:121], v[206:209], v[174:177], v[118:121]
	v_mfma_f32_16x16x32_bf16 v[114:117], v[214:217], v[174:177], v[114:117]
	v_mfma_f32_16x16x32_bf16 v[102:105], v[206:209], v[182:185], v[102:105]
	v_mfma_f32_16x16x32_bf16 v[98:101], v[214:217], v[182:185], v[98:101]
	v_mfma_f32_16x16x32_bf16 v[86:89], v[206:209], v[190:193], v[86:89]
	v_mfma_f32_16x16x32_bf16 v[82:85], v[214:217], v[190:193], v[82:85]
	v_mfma_f32_16x16x32_bf16 v[70:73], v[206:209], v[198:201], v[70:73]
	v_mfma_f32_16x16x32_bf16 v[66:69], v[214:217], v[198:201], v[66:69]
	v_mfma_f32_16x16x32_bf16 v[118:121], v[210:213], v[178:181], v[118:121]
	v_mfma_f32_16x16x32_bf16 v[114:117], v[218:221], v[178:181], v[114:117]
	v_mfma_f32_16x16x32_bf16 v[102:105], v[210:213], v[186:189], v[102:105]
	v_mfma_f32_16x16x32_bf16 v[98:101], v[218:221], v[186:189], v[98:101]
	v_mfma_f32_16x16x32_bf16 v[86:89], v[210:213], v[194:197], v[86:89]
	v_mfma_f32_16x16x32_bf16 v[82:85], v[218:221], v[194:197], v[82:85]
	v_mfma_f32_16x16x32_bf16 v[70:73], v[210:213], v[202:205], v[70:73]
	v_mfma_f32_16x16x32_bf16 v[66:69], v[218:221], v[202:205], v[66:69]
	s_setprio 0
	s_mov_b32 m0, s40
	v_lshl_add_u64 v[224:225], v[228:229], 0, s[0:1]
	s_barrier
	ds_read_b128 v[174:177], v152 offset:49152
	ds_read_b128 v[178:181], v152 offset:50176
	ds_read_b128 v[182:185], v152 offset:51200
	ds_read_b128 v[186:189], v152 offset:52224
	ds_read_b128 v[190:193], v152 offset:53248
	ds_read_b128 v[194:197], v152 offset:54272
	ds_read_b128 v[198:201], v152 offset:55296
	ds_read_b128 v[202:205], v152 offset:56320
	global_load_lds_dwordx4 v[224:225], off
	v_lshl_add_u64 v[222:223], v[222:223], 0, s[0:1]
	s_mov_b32 m0, s41
	s_nop 0
	global_load_lds_dwordx4 v[222:223], off
	s_barrier
	s_waitcnt lgkmcnt(0)
	s_setprio 1
	s_waitcnt lgkmcnt(0)
	v_mfma_f32_16x16x32_bf16 v[62:65], v[158:161], v[174:177], v[62:65]
	v_mfma_f32_16x16x32_bf16 v[58:61], v[166:169], v[174:177], v[58:61]
	v_mfma_f32_16x16x32_bf16 v[46:49], v[158:161], v[182:185], v[46:49]
	v_mfma_f32_16x16x32_bf16 v[42:45], v[166:169], v[182:185], v[42:45]
	v_mfma_f32_16x16x32_bf16 v[30:33], v[158:161], v[190:193], v[30:33]
	v_mfma_f32_16x16x32_bf16 v[26:29], v[166:169], v[190:193], v[26:29]
	v_mfma_f32_16x16x32_bf16 v[14:17], v[158:161], v[198:201], v[14:17]
	v_mfma_f32_16x16x32_bf16 v[10:13], v[166:169], v[198:201], v[10:13]
	v_mfma_f32_16x16x32_bf16 v[62:65], v[162:165], v[178:181], v[62:65]
	v_mfma_f32_16x16x32_bf16 v[58:61], v[170:173], v[178:181], v[58:61]
	v_mfma_f32_16x16x32_bf16 v[46:49], v[162:165], v[186:189], v[46:49]
	v_mfma_f32_16x16x32_bf16 v[42:45], v[170:173], v[186:189], v[42:45]
	v_mfma_f32_16x16x32_bf16 v[30:33], v[162:165], v[194:197], v[30:33]
	v_mfma_f32_16x16x32_bf16 v[26:29], v[170:173], v[194:197], v[26:29]
	v_mfma_f32_16x16x32_bf16 v[14:17], v[162:165], v[202:205], v[14:17]
	v_mfma_f32_16x16x32_bf16 v[10:13], v[170:173], v[202:205], v[10:13]
	s_setprio 0
	s_barrier
	s_add_u32 s14, s14, 0x80080
	s_addc_u32 s15, s15, 0
	s_add_i32 s16, s16, s33
	v_lshl_add_u64 v[158:159], s[14:15], 0, v[132:133]
	s_mov_b32 m0, s16
	s_nop 0
	global_load_lds_dwordx4 v[158:159], off
	v_lshl_add_u64 v[158:159], s[14:15], 0, v[130:131]
	s_add_i32 m0, s16, 0x2000
	s_nop 0
	global_load_lds_dwordx4 v[158:159], off
	s_waitcnt vmcnt(6)
	s_barrier
	s_setprio 1
	v_mfma_f32_16x16x32_bf16 v[54:57], v[206:209], v[174:177], v[54:57]
	v_mfma_f32_16x16x32_bf16 v[50:53], v[214:217], v[174:177], v[50:53]
	v_mfma_f32_16x16x32_bf16 v[38:41], v[206:209], v[182:185], v[38:41]
	v_mfma_f32_16x16x32_bf16 v[34:37], v[214:217], v[182:185], v[34:37]
	v_mfma_f32_16x16x32_bf16 v[22:25], v[206:209], v[190:193], v[22:25]
	v_mfma_f32_16x16x32_bf16 v[18:21], v[214:217], v[190:193], v[18:21]
	v_mfma_f32_16x16x32_bf16 v[6:9], v[206:209], v[198:201], v[6:9]
	v_mfma_f32_16x16x32_bf16 v[2:5], v[214:217], v[198:201], v[2:5]
	v_mfma_f32_16x16x32_bf16 v[54:57], v[210:213], v[178:181], v[54:57]
	v_mfma_f32_16x16x32_bf16 v[50:53], v[218:221], v[178:181], v[50:53]
	v_mfma_f32_16x16x32_bf16 v[38:41], v[210:213], v[186:189], v[38:41]
	v_mfma_f32_16x16x32_bf16 v[34:37], v[218:221], v[186:189], v[34:37]
	v_mfma_f32_16x16x32_bf16 v[22:25], v[210:213], v[194:197], v[22:25]
	v_mfma_f32_16x16x32_bf16 v[18:21], v[218:221], v[194:197], v[18:21]
	v_mfma_f32_16x16x32_bf16 v[6:9], v[210:213], v[202:205], v[6:9]
	v_mfma_f32_16x16x32_bf16 v[2:5], v[218:221], v[202:205], v[2:5]
	s_setprio 0
	s_add_i32 s61, s61, 2
	s_add_u32 s12, s12, 0x100
	s_addc_u32 s13, s13, 0
	s_cmp_gt_u32 s61, 29
	s_barrier
	s_cbranch_scc1 .Lpeel_1522_after

.Lpeel_1522_after:
	v_mul_f32_e32 v136, 0xbfb8aa3b, v126
	v_exp_f32_e32 v136, v136
	v_mul_f32_e32 v137, 0xbfb8aa3b, v127
	v_exp_f32_e32 v137, v137
	v_lshl_or_b32 v138, s56, 7, v150
	v_add_f32_e32 v136, 1.0, v136
	v_rcp_f32_e32 v140, v136
	v_add_f32_e32 v136, 1.0, v137
	v_rcp_f32_e32 v141, v136
	v_lshl_add_u32 v134, s57, 8, v148
	v_ashrrev_i32_e32 v139, 31, v138
	v_mov_b64_e32 v[136:137], s[44:45]
	v_pk_mul_f32 v[126:127], v[126:127], v[140:141]
	v_mul_f32_e32 v140, 0xbfb8aa3b, v128
	v_mul_f32_e32 v141, 0xbfb8aa3b, v129
	v_exp_f32_e32 v140, v140
	v_exp_f32_e32 v141, v141
	v_pk_mul_f32 v[118:119], v[126:127], v[118:119]
	v_mad_i64_i32 v[142:143], s[12:13], v134, s52, v[136:137]
	v_add_f32_e32 v126, 1.0, v140
	v_add_f32_e32 v127, 1.0, v141
	v_mul_f32_e32 v140, 0xbfb8aa3b, v122
	v_mul_f32_e32 v141, 0xbfb8aa3b, v123
	v_rcp_f32_e32 v126, v126
	v_rcp_f32_e32 v127, v127
	v_exp_f32_e32 v140, v140
	v_exp_f32_e32 v141, v141
	s_cmp_eq_u32 s53, s20
	v_pk_mul_f32 v[126:127], v[128:129], v[126:127]
	v_add_f32_e32 v128, 1.0, v140
	v_add_f32_e32 v129, 1.0, v141
	v_mul_f32_e32 v140, 0xbfb8aa3b, v124
	v_mul_f32_e32 v141, 0xbfb8aa3b, v125
	v_exp_f32_e32 v140, v140
	v_exp_f32_e32 v141, v141
	v_rcp_f32_e32 v128, v128
	v_rcp_f32_e32 v129, v129
	v_add_f32_e32 v140, 1.0, v140
	v_add_f32_e32 v141, 1.0, v141
	v_rcp_f32_e32 v140, v140
	v_rcp_f32_e32 v141, v141
	v_pk_mul_f32 v[122:123], v[122:123], v[128:129]
	v_pk_mul_f32 v[120:121], v[126:127], v[120:121]
	v_pk_mul_f32 v[122:123], v[122:123], v[114:115]
	v_pk_mul_f32 v[114:115], v[124:125], v[140:141]
	v_mov_b32_e32 v140, v157
	v_pk_mul_f32 v[124:125], v[114:115], v[116:117]
	v_cvt_pk_bf16_f32 v117, v120, v121
	v_mul_f32_e32 v120, 0xbfb8aa3b, v110
	v_mul_f32_e32 v121, 0xbfb8aa3b, v111
	v_exp_f32_e32 v120, v120
	v_exp_f32_e32 v121, v121
	v_lshlrev_b64 v[114:115], 1, v[138:139]
	v_lshl_add_u64 v[126:127], v[142:143], 0, v[114:115]
	v_cvt_pk_bf16_f32 v116, v118, v119
	v_cvt_pk_bf16_f32 v118, v122, v123
	v_cvt_pk_bf16_f32 v119, v124, v125
	global_store_dwordx4 v[126:127], v[116:119], off
	v_mov_b32_e32 v138, v156
	s_mov_b32 s56, s55
	v_add_f32_e32 v116, 1.0, v120
	v_add_f32_e32 v117, 1.0, v121
	v_rcp_f32_e32 v116, v116
	v_rcp_f32_e32 v117, v117
	v_or_b32_e32 v118, 16, v134
	v_mad_i64_i32 v[118:119], s[12:13], v118, s52, v[136:137]
	v_pk_mul_f32 v[110:111], v[110:111], v[116:117]
	v_mul_f32_e32 v116, 0xbfb8aa3b, v112
	v_mul_f32_e32 v117, 0xbfb8aa3b, v113
	v_exp_f32_e32 v116, v116
	v_exp_f32_e32 v117, v117
	v_pk_mul_f32 v[102:103], v[110:111], v[102:103]
	s_mov_b32 s57, s54
	v_add_f32_e32 v110, 1.0, v116
	v_add_f32_e32 v111, 1.0, v117
	v_mul_f32_e32 v116, 0xbfb8aa3b, v106
	v_mul_f32_e32 v117, 0xbfb8aa3b, v107
	v_rcp_f32_e32 v110, v110
	v_rcp_f32_e32 v111, v111
	v_exp_f32_e32 v116, v116
	v_exp_f32_e32 v117, v117
	v_pk_mul_f32 v[110:111], v[112:113], v[110:111]
	v_add_f32_e32 v112, 1.0, v116
	v_add_f32_e32 v113, 1.0, v117
	v_mul_f32_e32 v116, 0xbfb8aa3b, v108
	v_mul_f32_e32 v117, 0xbfb8aa3b, v109
	v_exp_f32_e32 v116, v116
	v_exp_f32_e32 v117, v117
	v_rcp_f32_e32 v112, v112
	v_rcp_f32_e32 v113, v113
	v_add_f32_e32 v116, 1.0, v116
	v_add_f32_e32 v117, 1.0, v117
	v_rcp_f32_e32 v116, v116
	v_rcp_f32_e32 v117, v117
	v_pk_mul_f32 v[106:107], v[106:107], v[112:113]
	v_pk_mul_f32 v[104:105], v[110:111], v[104:105]
	v_pk_mul_f32 v[106:107], v[106:107], v[98:99]
	v_pk_mul_f32 v[98:99], v[108:109], v[116:117]
	v_lshl_add_u64 v[110:111], v[118:119], 0, v[114:115]
	v_pk_mul_f32 v[108:109], v[98:99], v[100:101]
	v_cvt_pk_bf16_f32 v98, v102, v103
	v_mul_f32_e32 v102, 0xbfb8aa3b, v94
	v_mul_f32_e32 v103, 0xbfb8aa3b, v95
	v_exp_f32_e32 v102, v102
	v_exp_f32_e32 v103, v103
	v_cvt_pk_bf16_f32 v99, v104, v105
	v_cvt_pk_bf16_f32 v100, v106, v107
	v_cvt_pk_bf16_f32 v101, v108, v109
	global_store_dwordx4 v[110:111], v[98:101], off
	s_nop 1
	v_add_f32_e32 v98, 1.0, v102
	v_add_f32_e32 v99, 1.0, v103
	v_rcp_f32_e32 v98, v98
	v_rcp_f32_e32 v99, v99
	v_or_b32_e32 v100, 32, v134
	v_mad_i64_i32 v[100:101], s[12:13], v100, s52, v[136:137]
	v_pk_mul_f32 v[94:95], v[94:95], v[98:99]
	v_mul_f32_e32 v98, 0xbfb8aa3b, v96
	v_mul_f32_e32 v99, 0xbfb8aa3b, v97
	v_exp_f32_e32 v98, v98
	v_exp_f32_e32 v99, v99
	v_pk_mul_f32 v[86:87], v[94:95], v[86:87]
	v_add_f32_e32 v94, 1.0, v98
	v_add_f32_e32 v95, 1.0, v99
	v_mul_f32_e32 v98, 0xbfb8aa3b, v90
	v_mul_f32_e32 v99, 0xbfb8aa3b, v91
	v_rcp_f32_e32 v94, v94
	v_rcp_f32_e32 v95, v95
	v_exp_f32_e32 v98, v98
	v_exp_f32_e32 v99, v99
	v_pk_mul_f32 v[94:95], v[96:97], v[94:95]
	v_add_f32_e32 v96, 1.0, v98
	v_add_f32_e32 v97, 1.0, v99
	v_mul_f32_e32 v98, 0xbfb8aa3b, v92
	v_mul_f32_e32 v99, 0xbfb8aa3b, v93
	v_exp_f32_e32 v98, v98
	v_exp_f32_e32 v99, v99
	v_rcp_f32_e32 v96, v96
	v_rcp_f32_e32 v97, v97
	v_add_f32_e32 v98, 1.0, v98
	v_add_f32_e32 v99, 1.0, v99
	v_rcp_f32_e32 v98, v98
	v_rcp_f32_e32 v99, v99
	v_pk_mul_f32 v[90:91], v[90:91], v[96:97]
	v_pk_mul_f32 v[88:89], v[94:95], v[88:89]
	v_pk_mul_f32 v[90:91], v[90:91], v[82:83]
	v_pk_mul_f32 v[82:83], v[92:93], v[98:99]
	v_lshl_add_u64 v[94:95], v[100:101], 0, v[114:115]
	v_pk_mul_f32 v[92:93], v[82:83], v[84:85]
	v_cvt_pk_bf16_f32 v82, v86, v87
	v_mul_f32_e32 v86, 0xbfb8aa3b, v78
	v_mul_f32_e32 v87, 0xbfb8aa3b, v79
	v_exp_f32_e32 v86, v86
	v_exp_f32_e32 v87, v87
	v_cvt_pk_bf16_f32 v83, v88, v89
	v_cvt_pk_bf16_f32 v84, v90, v91
	v_cvt_pk_bf16_f32 v85, v92, v93
	global_store_dwordx4 v[94:95], v[82:85], off
	s_nop 1
	v_add_f32_e32 v82, 1.0, v86
	v_add_f32_e32 v83, 1.0, v87
	v_rcp_f32_e32 v82, v82
	v_rcp_f32_e32 v83, v83
	v_or_b32_e32 v84, 48, v134
	v_mad_i64_i32 v[84:85], s[12:13], v84, s52, v[136:137]
	v_pk_mul_f32 v[78:79], v[78:79], v[82:83]
	v_mul_f32_e32 v82, 0xbfb8aa3b, v80
	v_mul_f32_e32 v83, 0xbfb8aa3b, v81
	v_exp_f32_e32 v82, v82
	v_exp_f32_e32 v83, v83
	v_pk_mul_f32 v[70:71], v[78:79], v[70:71]
	v_add_f32_e32 v78, 1.0, v82
	v_add_f32_e32 v79, 1.0, v83
	v_mul_f32_e32 v82, 0xbfb8aa3b, v74
	v_mul_f32_e32 v83, 0xbfb8aa3b, v75
	v_rcp_f32_e32 v78, v78
	v_rcp_f32_e32 v79, v79
	v_exp_f32_e32 v82, v82
	v_exp_f32_e32 v83, v83
	v_pk_mul_f32 v[78:79], v[80:81], v[78:79]
	v_add_f32_e32 v80, 1.0, v82
	v_add_f32_e32 v81, 1.0, v83
	v_mul_f32_e32 v82, 0xbfb8aa3b, v76
	v_mul_f32_e32 v83, 0xbfb8aa3b, v77
	v_exp_f32_e32 v82, v82
	v_exp_f32_e32 v83, v83
	v_rcp_f32_e32 v80, v80
	v_rcp_f32_e32 v81, v81
	v_add_f32_e32 v82, 1.0, v82
	v_add_f32_e32 v83, 1.0, v83
	v_rcp_f32_e32 v82, v82
	v_rcp_f32_e32 v83, v83
	v_pk_mul_f32 v[74:75], v[74:75], v[80:81]
	v_pk_mul_f32 v[72:73], v[78:79], v[72:73]
	v_pk_mul_f32 v[74:75], v[74:75], v[66:67]
	v_pk_mul_f32 v[66:67], v[76:77], v[82:83]
	v_lshl_add_u64 v[78:79], v[84:85], 0, v[114:115]
	v_pk_mul_f32 v[76:77], v[66:67], v[68:69]
	v_cvt_pk_bf16_f32 v66, v70, v71
	v_mul_f32_e32 v70, 0xbfb8aa3b, v62
	v_mul_f32_e32 v71, 0xbfb8aa3b, v63
	v_exp_f32_e32 v70, v70
	v_exp_f32_e32 v71, v71
	v_cvt_pk_bf16_f32 v67, v72, v73
	v_cvt_pk_bf16_f32 v68, v74, v75
	v_cvt_pk_bf16_f32 v69, v76, v77
	global_store_dwordx4 v[78:79], v[66:69], off
	s_nop 1
	v_add_f32_e32 v66, 1.0, v70
	v_add_f32_e32 v67, 1.0, v71
	v_rcp_f32_e32 v66, v66
	v_rcp_f32_e32 v67, v67
	v_add_u32_e32 v68, 0x80, v134
	v_mad_i64_i32 v[68:69], s[12:13], v68, s52, v[136:137]
	v_pk_mul_f32 v[62:63], v[62:63], v[66:67]
	v_mul_f32_e32 v66, 0xbfb8aa3b, v64
	v_mul_f32_e32 v67, 0xbfb8aa3b, v65
	v_exp_f32_e32 v66, v66
	v_exp_f32_e32 v67, v67
	v_pk_mul_f32 v[54:55], v[62:63], v[54:55]
	v_add_f32_e32 v62, 1.0, v66
	v_add_f32_e32 v63, 1.0, v67
	v_mul_f32_e32 v66, 0xbfb8aa3b, v58
	v_mul_f32_e32 v67, 0xbfb8aa3b, v59
	v_rcp_f32_e32 v62, v62
	v_rcp_f32_e32 v63, v63
	v_exp_f32_e32 v66, v66
	v_exp_f32_e32 v67, v67
	v_pk_mul_f32 v[62:63], v[64:65], v[62:63]
	v_add_f32_e32 v64, 1.0, v66
	v_add_f32_e32 v65, 1.0, v67
	v_mul_f32_e32 v66, 0xbfb8aa3b, v60
	v_mul_f32_e32 v67, 0xbfb8aa3b, v61
	v_exp_f32_e32 v66, v66
	v_exp_f32_e32 v67, v67
	v_rcp_f32_e32 v64, v64
	v_rcp_f32_e32 v65, v65
	v_add_f32_e32 v66, 1.0, v66
	v_add_f32_e32 v67, 1.0, v67
	v_rcp_f32_e32 v66, v66
	v_rcp_f32_e32 v67, v67
	v_pk_mul_f32 v[58:59], v[58:59], v[64:65]
	v_pk_mul_f32 v[56:57], v[62:63], v[56:57]
	v_pk_mul_f32 v[58:59], v[58:59], v[50:51]
	v_pk_mul_f32 v[50:51], v[60:61], v[66:67]
	v_lshl_add_u64 v[62:63], v[68:69], 0, v[114:115]
	v_pk_mul_f32 v[60:61], v[50:51], v[52:53]
	v_cvt_pk_bf16_f32 v50, v54, v55
	v_mul_f32_e32 v54, 0xbfb8aa3b, v46
	v_mul_f32_e32 v55, 0xbfb8aa3b, v47
	v_exp_f32_e32 v54, v54
	v_exp_f32_e32 v55, v55
	v_cvt_pk_bf16_f32 v51, v56, v57
	v_cvt_pk_bf16_f32 v52, v58, v59
	v_cvt_pk_bf16_f32 v53, v60, v61
	global_store_dwordx4 v[62:63], v[50:53], off
	s_nop 1
	v_add_f32_e32 v50, 1.0, v54
	v_add_f32_e32 v51, 1.0, v55
	v_rcp_f32_e32 v50, v50
	v_rcp_f32_e32 v51, v51
	v_add_u32_e32 v52, 0x90, v134
	v_mad_i64_i32 v[52:53], s[12:13], v52, s52, v[136:137]
	v_pk_mul_f32 v[46:47], v[46:47], v[50:51]
	v_mul_f32_e32 v50, 0xbfb8aa3b, v48
	v_mul_f32_e32 v51, 0xbfb8aa3b, v49
	v_exp_f32_e32 v50, v50
	v_exp_f32_e32 v51, v51
	v_pk_mul_f32 v[38:39], v[46:47], v[38:39]
	v_add_f32_e32 v46, 1.0, v50
	v_add_f32_e32 v47, 1.0, v51
	v_mul_f32_e32 v50, 0xbfb8aa3b, v42
	v_mul_f32_e32 v51, 0xbfb8aa3b, v43
	v_rcp_f32_e32 v46, v46
	v_rcp_f32_e32 v47, v47
	v_exp_f32_e32 v50, v50
	v_exp_f32_e32 v51, v51
	v_pk_mul_f32 v[46:47], v[48:49], v[46:47]
	v_add_f32_e32 v48, 1.0, v50
	v_add_f32_e32 v49, 1.0, v51
	v_mul_f32_e32 v50, 0xbfb8aa3b, v44
	v_mul_f32_e32 v51, 0xbfb8aa3b, v45
	v_exp_f32_e32 v50, v50
	v_exp_f32_e32 v51, v51
	v_rcp_f32_e32 v48, v48
	v_rcp_f32_e32 v49, v49
	v_add_f32_e32 v50, 1.0, v50
	v_add_f32_e32 v51, 1.0, v51
	v_rcp_f32_e32 v50, v50
	v_rcp_f32_e32 v51, v51
	v_pk_mul_f32 v[42:43], v[42:43], v[48:49]
	v_pk_mul_f32 v[40:41], v[46:47], v[40:41]
	v_pk_mul_f32 v[42:43], v[42:43], v[34:35]
	v_pk_mul_f32 v[34:35], v[44:45], v[50:51]
	v_lshl_add_u64 v[46:47], v[52:53], 0, v[114:115]
	v_pk_mul_f32 v[44:45], v[34:35], v[36:37]
	v_cvt_pk_bf16_f32 v34, v38, v39
	v_mul_f32_e32 v38, 0xbfb8aa3b, v30
	v_mul_f32_e32 v39, 0xbfb8aa3b, v31
	v_exp_f32_e32 v38, v38
	v_exp_f32_e32 v39, v39
	v_cvt_pk_bf16_f32 v35, v40, v41
	v_cvt_pk_bf16_f32 v36, v42, v43
	v_cvt_pk_bf16_f32 v37, v44, v45
	global_store_dwordx4 v[46:47], v[34:37], off
	s_nop 1
	v_add_f32_e32 v34, 1.0, v38
	v_add_f32_e32 v35, 1.0, v39
	v_rcp_f32_e32 v34, v34
	v_rcp_f32_e32 v35, v35
	v_add_u32_e32 v36, 0xa0, v134
	v_mad_i64_i32 v[36:37], s[12:13], v36, s52, v[136:137]
	v_pk_mul_f32 v[30:31], v[30:31], v[34:35]
	v_mul_f32_e32 v34, 0xbfb8aa3b, v32
	v_mul_f32_e32 v35, 0xbfb8aa3b, v33
	v_exp_f32_e32 v34, v34
	v_exp_f32_e32 v35, v35
	v_pk_mul_f32 v[22:23], v[30:31], v[22:23]
	v_add_f32_e32 v30, 1.0, v34
	v_add_f32_e32 v31, 1.0, v35
	v_mul_f32_e32 v34, 0xbfb8aa3b, v26
	v_mul_f32_e32 v35, 0xbfb8aa3b, v27
	v_rcp_f32_e32 v30, v30
	v_rcp_f32_e32 v31, v31
	v_exp_f32_e32 v34, v34
	v_exp_f32_e32 v35, v35
	v_pk_mul_f32 v[30:31], v[32:33], v[30:31]
	v_add_f32_e32 v32, 1.0, v34
	v_add_f32_e32 v33, 1.0, v35
	v_mul_f32_e32 v34, 0xbfb8aa3b, v28
	v_mul_f32_e32 v35, 0xbfb8aa3b, v29
	v_exp_f32_e32 v34, v34
	v_exp_f32_e32 v35, v35
	v_rcp_f32_e32 v32, v32
	v_rcp_f32_e32 v33, v33
	v_add_f32_e32 v34, 1.0, v34
	v_add_f32_e32 v35, 1.0, v35
	v_rcp_f32_e32 v34, v34
	v_rcp_f32_e32 v35, v35
	v_pk_mul_f32 v[26:27], v[26:27], v[32:33]
	v_pk_mul_f32 v[24:25], v[30:31], v[24:25]
	v_pk_mul_f32 v[26:27], v[26:27], v[18:19]
	v_pk_mul_f32 v[18:19], v[28:29], v[34:35]
	v_lshl_add_u64 v[30:31], v[36:37], 0, v[114:115]
	v_pk_mul_f32 v[28:29], v[18:19], v[20:21]
	v_cvt_pk_bf16_f32 v18, v22, v23
	v_mul_f32_e32 v22, 0xbfb8aa3b, v14
	v_mul_f32_e32 v23, 0xbfb8aa3b, v15
	v_exp_f32_e32 v22, v22
	v_exp_f32_e32 v23, v23
	v_cvt_pk_bf16_f32 v19, v24, v25
	v_cvt_pk_bf16_f32 v20, v26, v27
	v_cvt_pk_bf16_f32 v21, v28, v29
	global_store_dwordx4 v[30:31], v[18:21], off
	s_nop 1
	v_add_f32_e32 v18, 1.0, v22
	v_add_f32_e32 v19, 1.0, v23
	v_rcp_f32_e32 v18, v18
	v_rcp_f32_e32 v19, v19
	v_add_u32_e32 v20, 0xb0, v134
	v_mad_i64_i32 v[20:21], s[12:13], v20, s52, v[136:137]
	v_pk_mul_f32 v[14:15], v[14:15], v[18:19]
	v_mul_f32_e32 v18, 0xbfb8aa3b, v16
	v_mul_f32_e32 v19, 0xbfb8aa3b, v17
	v_exp_f32_e32 v18, v18
	v_exp_f32_e32 v19, v19
	v_pk_mul_f32 v[6:7], v[14:15], v[6:7]
	v_mov_b32_e32 v137, v154
	v_add_f32_e32 v14, 1.0, v18
	v_add_f32_e32 v15, 1.0, v19
	v_mul_f32_e32 v18, 0xbfb8aa3b, v10
	v_mul_f32_e32 v19, 0xbfb8aa3b, v11
	v_rcp_f32_e32 v14, v14
	v_rcp_f32_e32 v15, v15
	v_exp_f32_e32 v18, v18
	v_exp_f32_e32 v19, v19
	v_mov_b32_e32 v136, v155
	v_pk_mul_f32 v[14:15], v[16:17], v[14:15]
	v_add_f32_e32 v16, 1.0, v18
	v_add_f32_e32 v17, 1.0, v19
	v_mul_f32_e32 v18, 0xbfb8aa3b, v12
	v_mul_f32_e32 v19, 0xbfb8aa3b, v13
	v_exp_f32_e32 v18, v18
	v_exp_f32_e32 v19, v19
	v_rcp_f32_e32 v16, v16
	v_rcp_f32_e32 v17, v17
	v_add_f32_e32 v18, 1.0, v18
	v_add_f32_e32 v19, 1.0, v19
	v_rcp_f32_e32 v18, v18
	v_rcp_f32_e32 v19, v19
	v_pk_mul_f32 v[10:11], v[10:11], v[16:17]
	v_pk_mul_f32 v[8:9], v[14:15], v[8:9]
	v_pk_mul_f32 v[10:11], v[10:11], v[2:3]
	v_pk_mul_f32 v[2:3], v[12:13], v[18:19]
	v_lshl_add_u64 v[14:15], v[20:21], 0, v[114:115]
	v_pk_mul_f32 v[12:13], v[2:3], v[4:5]
	v_cvt_pk_bf16_f32 v2, v6, v7
	v_cvt_pk_bf16_f32 v3, v8, v9
	v_cvt_pk_bf16_f32 v4, v10, v11
	v_cvt_pk_bf16_f32 v5, v12, v13
	s_mov_b64 s[12:13], s[10:11]
	s_mov_b32 s10, s53
	global_store_dwordx4 v[14:15], v[2:5], off
	s_cbranch_scc0 .LBB0_1497
	s_waitcnt vmcnt(0)
	s_cmpk_gt_u32 s24, 0xff
	v_readlane_b32 s93, v254, 9
	s_cbranch_scc1 .LBB0_1526
	s_barrier

.LBB0_1626:
	s_add_u32 s18, s18, 0x30080
	s_addc_u32 s19, s19, 0
	s_add_u32 s64, s20, 0x100
	v_mov_b32_e32 v2, 0
	s_addc_u32 s65, s21, 0
	s_mov_b32 s66, -2
	ds_read_b128 v[148:151], v144
	ds_read_b128 v[152:155], v144 offset:1024
	ds_read_b128 v[156:159], v144 offset:2048
	ds_read_b128 v[160:163], v144 offset:3072
	s_add_u32 s20, s18, 0xfffd0080
	s_addc_u32 s21, s19, -1
	s_cmp_eq_u32 s66, 8
	s_cselect_b32 s23, s17, s21
	s_cselect_b32 s22, s16, s20
	s_cselect_b32 s21, s1, s65
	s_cselect_b32 s20, s0, s64
	v_lshl_add_u64 v[196:197], s[18:19], 0, v[138:139]
	s_add_i32 m0, s40, 0xc000
	ds_read_b128 v[164:167], v145
	ds_read_b128 v[168:171], v145 offset:1024
	ds_read_b128 v[172:175], v145 offset:2048
	ds_read_b128 v[176:179], v145 offset:3072
	ds_read_b128 v[180:183], v145 offset:4096
	ds_read_b128 v[184:187], v145 offset:5120
	ds_read_b128 v[188:191], v145 offset:6144
	ds_read_b128 v[192:195], v145 offset:7168
	global_load_lds_dwordx4 v[196:197], off
	v_lshl_add_u64 v[196:197], s[18:19], 0, v[140:141]
	s_add_i32 m0, s40, 0xe000
	s_nop 0
	global_load_lds_dwordx4 v[196:197], off
	s_waitcnt lgkmcnt(8)
	s_barrier
	s_waitcnt lgkmcnt(0)
	s_setprio 1
	s_waitcnt lgkmcnt(0)
	v_mfma_f32_16x16x32_bf16 v[126:129], v[148:151], v[164:167], 0
	v_mfma_f32_16x16x32_bf16 v[122:125], v[156:159], v[164:167], 0
	v_mfma_f32_16x16x32_bf16 v[118:121], v[148:151], v[172:175], 0
	v_mfma_f32_16x16x32_bf16 v[114:117], v[156:159], v[172:175], 0
	v_mfma_f32_16x16x32_bf16 v[102:105], v[148:151], v[180:183], 0
	v_mfma_f32_16x16x32_bf16 v[98:101], v[156:159], v[180:183], 0
	v_mfma_f32_16x16x32_bf16 v[86:89], v[148:151], v[188:191], 0
	v_mfma_f32_16x16x32_bf16 v[82:85], v[156:159], v[188:191], 0
	v_mfma_f32_16x16x32_bf16 v[126:129], v[152:155], v[168:171], v[126:129]
	v_mfma_f32_16x16x32_bf16 v[122:125], v[160:163], v[168:171], v[122:125]
	v_mfma_f32_16x16x32_bf16 v[118:121], v[152:155], v[176:179], v[118:121]
	v_mfma_f32_16x16x32_bf16 v[114:117], v[160:163], v[176:179], v[114:117]
	v_mfma_f32_16x16x32_bf16 v[102:105], v[152:155], v[184:187], v[102:105]
	v_mfma_f32_16x16x32_bf16 v[98:101], v[160:163], v[184:187], v[98:101]
	v_mfma_f32_16x16x32_bf16 v[86:89], v[152:155], v[192:195], v[86:89]
	v_mfma_f32_16x16x32_bf16 v[82:85], v[160:163], v[192:195], v[82:85]
	s_setprio 0
	s_barrier
	s_add_i32 s67, s52, s39
	v_lshl_add_u64 v[212:213], s[20:21], 0, v[134:135]
	s_mov_b32 m0, s67
	ds_read_b128 v[196:199], v146
	ds_read_b128 v[200:203], v146 offset:1024
	ds_read_b128 v[204:207], v146 offset:2048
	ds_read_b128 v[208:211], v146 offset:3072
	global_load_lds_dwordx4 v[212:213], off
	v_lshl_add_u64 v[214:215], s[20:21], 0, v[130:131]
	s_add_i32 m0, s67, 0x2000
	s_nop 0
	global_load_lds_dwordx4 v[214:215], off
	s_barrier
	s_waitcnt lgkmcnt(0)
	s_setprio 1
	s_waitcnt lgkmcnt(0)
	v_mfma_f32_16x16x32_bf16 v[110:113], v[196:199], v[164:167], 0
	v_mfma_f32_16x16x32_bf16 v[106:109], v[204:207], v[164:167], 0
	v_mfma_f32_16x16x32_bf16 v[94:97], v[196:199], v[172:175], 0
	v_mfma_f32_16x16x32_bf16 v[90:93], v[204:207], v[172:175], 0
	v_mfma_f32_16x16x32_bf16 v[78:81], v[196:199], v[180:183], 0
	v_mfma_f32_16x16x32_bf16 v[74:77], v[204:207], v[180:183], 0
	v_mfma_f32_16x16x32_bf16 v[70:73], v[196:199], v[188:191], 0
	v_mfma_f32_16x16x32_bf16 v[66:69], v[204:207], v[188:191], 0
	v_mfma_f32_16x16x32_bf16 v[110:113], v[200:203], v[168:171], v[110:113]
	v_mfma_f32_16x16x32_bf16 v[106:109], v[208:211], v[168:171], v[106:109]
	v_mfma_f32_16x16x32_bf16 v[94:97], v[200:203], v[176:179], v[94:97]
	v_mfma_f32_16x16x32_bf16 v[90:93], v[208:211], v[176:179], v[90:93]
	v_mfma_f32_16x16x32_bf16 v[78:81], v[200:203], v[184:187], v[78:81]
	v_mfma_f32_16x16x32_bf16 v[74:77], v[208:211], v[184:187], v[74:77]
	v_mfma_f32_16x16x32_bf16 v[70:73], v[200:203], v[192:195], v[70:73]
	v_mfma_f32_16x16x32_bf16 v[66:69], v[208:211], v[192:195], v[66:69]
	s_setprio 0
	s_mov_b32 m0, s40
	v_lshl_add_u64 v[216:217], s[22:23], 0, v[136:137]
	s_barrier
	ds_read_b128 v[164:167], v145 offset:16384
	ds_read_b128 v[168:171], v145 offset:17408
	ds_read_b128 v[172:175], v145 offset:18432
	ds_read_b128 v[176:179], v145 offset:19456
	ds_read_b128 v[180:183], v145 offset:20480
	ds_read_b128 v[184:187], v145 offset:21504
	ds_read_b128 v[188:191], v145 offset:22528
	ds_read_b128 v[192:195], v145 offset:23552
	global_load_lds_dwordx4 v[216:217], off
	v_lshl_add_u64 v[218:219], s[22:23], 0, v[132:133]
	s_mov_b32 m0, s41
	s_nop 0
	global_load_lds_dwordx4 v[218:219], off
	s_barrier
	s_waitcnt lgkmcnt(0)
	s_setprio 1
	s_waitcnt lgkmcnt(0)
	v_mfma_f32_16x16x32_bf16 v[62:65], v[148:151], v[164:167], 0
	v_mfma_f32_16x16x32_bf16 v[58:61], v[156:159], v[164:167], 0
	v_mfma_f32_16x16x32_bf16 v[54:57], v[148:151], v[172:175], 0
	v_mfma_f32_16x16x32_bf16 v[50:53], v[156:159], v[172:175], 0
	v_mfma_f32_16x16x32_bf16 v[38:41], v[148:151], v[180:183], 0
	v_mfma_f32_16x16x32_bf16 v[34:37], v[156:159], v[180:183], 0
	v_mfma_f32_16x16x32_bf16 v[22:25], v[148:151], v[188:191], 0
	v_mfma_f32_16x16x32_bf16 v[18:21], v[156:159], v[188:191], 0
	v_mfma_f32_16x16x32_bf16 v[62:65], v[152:155], v[168:171], v[62:65]
	v_mfma_f32_16x16x32_bf16 v[58:61], v[160:163], v[168:171], v[58:61]
	v_mfma_f32_16x16x32_bf16 v[54:57], v[152:155], v[176:179], v[54:57]
	v_mfma_f32_16x16x32_bf16 v[50:53], v[160:163], v[176:179], v[50:53]
	v_mfma_f32_16x16x32_bf16 v[38:41], v[152:155], v[184:187], v[38:41]
	v_mfma_f32_16x16x32_bf16 v[34:37], v[160:163], v[184:187], v[34:37]
	v_mfma_f32_16x16x32_bf16 v[22:25], v[152:155], v[192:195], v[22:25]
	v_mfma_f32_16x16x32_bf16 v[18:21], v[160:163], v[192:195], v[18:21]
	s_setprio 0
	s_barrier
	s_add_u32 s68, s20, 0x30000
	s_addc_u32 s69, s21, 0
	s_add_i32 s67, s53, s39
	v_lshl_add_u64 v[148:149], s[68:69], 0, v[134:135]
	s_mov_b32 m0, s67
	s_nop 0
	global_load_lds_dwordx4 v[148:149], off
	v_lshl_add_u64 v[148:149], s[68:69], 0, v[130:131]
	s_add_i32 m0, s67, 0x2000
	s_nop 0
	global_load_lds_dwordx4 v[148:149], off
	s_waitcnt vmcnt(6)
	s_barrier
	s_setprio 1
	v_mfma_f32_16x16x32_bf16 v[46:49], v[196:199], v[164:167], 0
	v_mfma_f32_16x16x32_bf16 v[42:45], v[204:207], v[164:167], 0
	v_mfma_f32_16x16x32_bf16 v[30:33], v[196:199], v[172:175], 0
	v_mfma_f32_16x16x32_bf16 v[26:29], v[204:207], v[172:175], 0
	v_mfma_f32_16x16x32_bf16 v[14:17], v[196:199], v[180:183], 0
	v_mfma_f32_16x16x32_bf16 v[10:13], v[204:207], v[180:183], 0
	v_mfma_f32_16x16x32_bf16 v[6:9], v[196:199], v[188:191], 0
	v_mfma_f32_16x16x32_bf16 v[2:5], v[204:207], v[188:191], 0
	v_mfma_f32_16x16x32_bf16 v[46:49], v[200:203], v[168:171], v[46:49]
	v_mfma_f32_16x16x32_bf16 v[42:45], v[208:211], v[168:171], v[42:45]
	v_mfma_f32_16x16x32_bf16 v[30:33], v[200:203], v[176:179], v[30:33]
	v_mfma_f32_16x16x32_bf16 v[26:29], v[208:211], v[176:179], v[26:29]
	v_mfma_f32_16x16x32_bf16 v[14:17], v[200:203], v[184:187], v[14:17]
	v_mfma_f32_16x16x32_bf16 v[10:13], v[208:211], v[184:187], v[10:13]
	v_mfma_f32_16x16x32_bf16 v[6:9], v[200:203], v[192:195], v[6:9]
	v_mfma_f32_16x16x32_bf16 v[2:5], v[208:211], v[192:195], v[2:5]
	s_setprio 0
	s_add_i32 s67, 0, 0x18000
	v_add_u32_e32 v147, s67, v1
	s_barrier
	ds_read_b128 v[148:151], v147
	ds_read_b128 v[152:155], v147 offset:1024
	ds_read_b128 v[156:159], v147 offset:2048
	ds_read_b128 v[160:163], v147 offset:3072
	s_add_u32 s22, s22, 0x30000
	s_addc_u32 s23, s23, 0
	s_mov_b32 m0, s42
	v_lshl_add_u64 v[196:197], s[22:23], 0, v[136:137]
	ds_read_b128 v[164:167], v145 offset:32768
	ds_read_b128 v[168:171], v145 offset:33792
	ds_read_b128 v[172:175], v145 offset:34816
	ds_read_b128 v[176:179], v145 offset:35840
	ds_read_b128 v[180:183], v145 offset:36864
	ds_read_b128 v[184:187], v145 offset:37888
	ds_read_b128 v[188:191], v145 offset:38912
	ds_read_b128 v[192:195], v145 offset:39936
	global_load_lds_dwordx4 v[196:197], off
	v_lshl_add_u64 v[196:197], s[22:23], 0, v[132:133]
	s_mov_b32 m0, s43
	s_nop 0
	global_load_lds_dwordx4 v[196:197], off
	s_waitcnt lgkmcnt(8)
	s_barrier
	s_waitcnt lgkmcnt(0)
	s_setprio 1
	s_waitcnt lgkmcnt(0)
	v_mfma_f32_16x16x32_bf16 v[126:129], v[148:151], v[164:167], v[126:129]
	v_mfma_f32_16x16x32_bf16 v[122:125], v[156:159], v[164:167], v[122:125]
	v_mfma_f32_16x16x32_bf16 v[118:121], v[148:151], v[172:175], v[118:121]
	v_mfma_f32_16x16x32_bf16 v[114:117], v[156:159], v[172:175], v[114:117]
	v_mfma_f32_16x16x32_bf16 v[102:105], v[148:151], v[180:183], v[102:105]
	v_mfma_f32_16x16x32_bf16 v[98:101], v[156:159], v[180:183], v[98:101]
	v_mfma_f32_16x16x32_bf16 v[86:89], v[148:151], v[188:191], v[86:89]
	v_mfma_f32_16x16x32_bf16 v[82:85], v[156:159], v[188:191], v[82:85]
	v_mfma_f32_16x16x32_bf16 v[126:129], v[152:155], v[168:171], v[126:129]
	v_mfma_f32_16x16x32_bf16 v[122:125], v[160:163], v[168:171], v[122:125]
	v_mfma_f32_16x16x32_bf16 v[118:121], v[152:155], v[176:179], v[118:121]
	v_mfma_f32_16x16x32_bf16 v[114:117], v[160:163], v[176:179], v[114:117]
	v_mfma_f32_16x16x32_bf16 v[102:105], v[152:155], v[184:187], v[102:105]
	v_mfma_f32_16x16x32_bf16 v[98:101], v[160:163], v[184:187], v[98:101]
	v_mfma_f32_16x16x32_bf16 v[86:89], v[152:155], v[192:195], v[86:89]
	v_mfma_f32_16x16x32_bf16 v[82:85], v[160:163], v[192:195], v[82:85]
	s_setprio 0
	s_barrier
	s_add_i32 s22, 0, 0x1c000
	s_add_i32 s23, s67, s39
	v_add_u32_e32 v147, s22, v1
	v_lshl_add_u64 v[212:213], v[212:213], 0, s[6:7]
	s_mov_b32 m0, s23
	ds_read_b128 v[196:199], v147
	ds_read_b128 v[200:203], v147 offset:1024
	ds_read_b128 v[204:207], v147 offset:2048
	ds_read_b128 v[208:211], v147 offset:3072
	global_load_lds_dwordx4 v[212:213], off
	v_lshl_add_u64 v[212:213], v[214:215], 0, s[6:7]
	s_add_i32 m0, s23, 0x2000
	s_nop 0
	global_load_lds_dwordx4 v[212:213], off
	s_barrier
	s_waitcnt lgkmcnt(0)
	s_setprio 1
	s_waitcnt lgkmcnt(0)
	v_mfma_f32_16x16x32_bf16 v[110:113], v[196:199], v[164:167], v[110:113]
	v_mfma_f32_16x16x32_bf16 v[106:109], v[204:207], v[164:167], v[106:109]
	v_mfma_f32_16x16x32_bf16 v[94:97], v[196:199], v[172:175], v[94:97]
	v_mfma_f32_16x16x32_bf16 v[90:93], v[204:207], v[172:175], v[90:93]
	v_mfma_f32_16x16x32_bf16 v[78:81], v[196:199], v[180:183], v[78:81]
	v_mfma_f32_16x16x32_bf16 v[74:77], v[204:207], v[180:183], v[74:77]
	v_mfma_f32_16x16x32_bf16 v[70:73], v[196:199], v[188:191], v[70:73]
	v_mfma_f32_16x16x32_bf16 v[66:69], v[204:207], v[188:191], v[66:69]
	v_mfma_f32_16x16x32_bf16 v[110:113], v[200:203], v[168:171], v[110:113]
	v_mfma_f32_16x16x32_bf16 v[106:109], v[208:211], v[168:171], v[106:109]
	v_mfma_f32_16x16x32_bf16 v[94:97], v[200:203], v[176:179], v[94:97]
	v_mfma_f32_16x16x32_bf16 v[90:93], v[208:211], v[176:179], v[90:93]
	v_mfma_f32_16x16x32_bf16 v[78:81], v[200:203], v[184:187], v[78:81]
	v_mfma_f32_16x16x32_bf16 v[74:77], v[208:211], v[184:187], v[74:77]
	v_mfma_f32_16x16x32_bf16 v[70:73], v[200:203], v[192:195], v[70:73]
	v_mfma_f32_16x16x32_bf16 v[66:69], v[208:211], v[192:195], v[66:69]
	s_setprio 0
	s_mov_b32 m0, s46
	v_lshl_add_u64 v[212:213], v[216:217], 0, s[6:7]
	s_barrier
	ds_read_b128 v[164:167], v145 offset:49152
	ds_read_b128 v[168:171], v145 offset:50176
	ds_read_b128 v[172:175], v145 offset:51200
	ds_read_b128 v[176:179], v145 offset:52224
	ds_read_b128 v[180:183], v145 offset:53248
	ds_read_b128 v[184:187], v145 offset:54272
	ds_read_b128 v[188:191], v145 offset:55296
	ds_read_b128 v[192:195], v145 offset:56320
	global_load_lds_dwordx4 v[212:213], off
	v_lshl_add_u64 v[212:213], v[218:219], 0, s[6:7]
	s_mov_b32 m0, s47
	s_nop 0
	global_load_lds_dwordx4 v[212:213], off
	s_barrier
	s_waitcnt lgkmcnt(0)
	s_setprio 1
	s_waitcnt lgkmcnt(0)
	v_mfma_f32_16x16x32_bf16 v[62:65], v[148:151], v[164:167], v[62:65]
	v_mfma_f32_16x16x32_bf16 v[58:61], v[156:159], v[164:167], v[58:61]
	v_mfma_f32_16x16x32_bf16 v[54:57], v[148:151], v[172:175], v[54:57]
	v_mfma_f32_16x16x32_bf16 v[50:53], v[156:159], v[172:175], v[50:53]
	v_mfma_f32_16x16x32_bf16 v[38:41], v[148:151], v[180:183], v[38:41]
	v_mfma_f32_16x16x32_bf16 v[34:37], v[156:159], v[180:183], v[34:37]
	v_mfma_f32_16x16x32_bf16 v[22:25], v[148:151], v[188:191], v[22:25]
	v_mfma_f32_16x16x32_bf16 v[18:21], v[156:159], v[188:191], v[18:21]
	v_mfma_f32_16x16x32_bf16 v[62:65], v[152:155], v[168:171], v[62:65]
	v_mfma_f32_16x16x32_bf16 v[58:61], v[160:163], v[168:171], v[58:61]
	v_mfma_f32_16x16x32_bf16 v[54:57], v[152:155], v[176:179], v[54:57]
	v_mfma_f32_16x16x32_bf16 v[50:53], v[160:163], v[176:179], v[50:53]
	v_mfma_f32_16x16x32_bf16 v[38:41], v[152:155], v[184:187], v[38:41]
	v_mfma_f32_16x16x32_bf16 v[34:37], v[160:163], v[184:187], v[34:37]
	v_mfma_f32_16x16x32_bf16 v[22:25], v[152:155], v[192:195], v[22:25]
	v_mfma_f32_16x16x32_bf16 v[18:21], v[160:163], v[192:195], v[18:21]
	s_setprio 0
	s_barrier
	s_add_u32 s20, s20, 0x30080
	s_addc_u32 s21, s21, 0
	s_add_i32 s22, s22, s39
	v_lshl_add_u64 v[148:149], s[20:21], 0, v[134:135]
	s_mov_b32 m0, s22
	s_nop 0
	global_load_lds_dwordx4 v[148:149], off
	v_lshl_add_u64 v[148:149], s[20:21], 0, v[130:131]
	s_add_i32 m0, s22, 0x2000
	s_nop 0
	global_load_lds_dwordx4 v[148:149], off
	s_waitcnt vmcnt(6)
	s_barrier
	s_setprio 1
	v_mfma_f32_16x16x32_bf16 v[46:49], v[196:199], v[164:167], v[46:49]
	v_mfma_f32_16x16x32_bf16 v[42:45], v[204:207], v[164:167], v[42:45]
	v_mfma_f32_16x16x32_bf16 v[30:33], v[196:199], v[172:175], v[30:33]
	v_mfma_f32_16x16x32_bf16 v[26:29], v[204:207], v[172:175], v[26:29]
	v_mfma_f32_16x16x32_bf16 v[14:17], v[196:199], v[180:183], v[14:17]
	v_mfma_f32_16x16x32_bf16 v[10:13], v[204:207], v[180:183], v[10:13]
	v_mfma_f32_16x16x32_bf16 v[6:9], v[196:199], v[188:191], v[6:9]
	v_mfma_f32_16x16x32_bf16 v[2:5], v[204:207], v[188:191], v[2:5]
	v_mfma_f32_16x16x32_bf16 v[46:49], v[200:203], v[168:171], v[46:49]
	v_mfma_f32_16x16x32_bf16 v[42:45], v[208:211], v[168:171], v[42:45]
	v_mfma_f32_16x16x32_bf16 v[30:33], v[200:203], v[176:179], v[30:33]
	v_mfma_f32_16x16x32_bf16 v[26:29], v[208:211], v[176:179], v[26:29]
	v_mfma_f32_16x16x32_bf16 v[14:17], v[200:203], v[184:187], v[14:17]
	v_mfma_f32_16x16x32_bf16 v[10:13], v[208:211], v[184:187], v[10:13]
	v_mfma_f32_16x16x32_bf16 v[6:9], v[200:203], v[192:195], v[6:9]
	v_mfma_f32_16x16x32_bf16 v[2:5], v[208:211], v[192:195], v[2:5]
	s_setprio 0
	s_add_i32 s66, s66, 2
	s_add_u32 s18, s18, 0x100
	s_addc_u32 s19, s19, 0
	s_add_u32 s64, s64, 0x100
	s_addc_u32 s65, s65, 0
	s_cmp_gt_u32 s66, 9
	s_barrier
	s_cbranch_scc1 .Lpeel_1627_after

.Lpeel_1627_after:
	v_lshl_add_u32 v148, s59, 8, v142
	v_lshl_or_b32 v150, s60, 8, v143
	v_ashrrev_i32_e32 v149, 31, v148
	v_ashrrev_i32_e32 v151, 31, v150
	v_lshlrev_b64 v[152:153], 12, v[148:149]
	v_lshl_add_u64 v[152:153], s[48:49], 0, v[152:153]
	v_lshlrev_b64 v[150:151], 1, v[150:151]
	v_lshl_add_u64 v[152:153], v[152:153], 0, v[150:151]
	v_cvt_pk_bf16_f32 v62, v62, v63
	v_cvt_pk_bf16_f32 v63, v64, v65
	v_cvt_pk_bf16_f32 v64, v58, v59
	v_add_co_u32_e32 v58, vcc, s54, v152
	v_cvt_pk_bf16_f32 v110, v110, v111
	v_cvt_pk_bf16_f32 v111, v112, v113
	v_cvt_pk_bf16_f32 v112, v106, v107
	v_or_b32_e32 v106, 16, v148
	v_cvt_pk_bf16_f32 v70, v70, v71
	v_cvt_pk_bf16_f32 v71, v72, v73
	v_cvt_pk_bf16_f32 v72, v66, v67
	v_lshl_add_u64 v[66:67], v[152:153], 0, s[8:9]
	v_addc_co_u32_e32 v59, vcc, 0, v153, vcc
	v_cvt_pk_bf16_f32 v46, v46, v47
	v_cvt_pk_bf16_f32 v47, v48, v49
	v_cvt_pk_bf16_f32 v48, v42, v43
	v_cvt_pk_bf16_f32 v49, v44, v45
	v_ashrrev_i32_e32 v107, 31, v106
	v_cvt_pk_bf16_f32 v94, v94, v95
	v_cvt_pk_bf16_f32 v95, v96, v97
	v_cvt_pk_bf16_f32 v96, v90, v91
	v_or_b32_e32 v90, 32, v148
	global_store_dwordx4 v[66:67], v[46:49], off offset:256
	v_lshlrev_b64 v[106:107], 12, v[106:107]
	v_ashrrev_i32_e32 v91, 31, v90
	v_add_co_u32_e32 v48, vcc, s55, v152
	v_cvt_pk_bf16_f32 v78, v78, v79
	v_cvt_pk_bf16_f32 v79, v80, v81
	v_cvt_pk_bf16_f32 v80, v74, v75
	v_or_b32_e32 v74, 48, v148
	v_lshl_add_u64 v[46:47], v[152:153], 0, s[10:11]
	v_addc_co_u32_e32 v49, vcc, 0, v153, vcc
	v_cvt_pk_bf16_f32 v30, v30, v31
	v_cvt_pk_bf16_f32 v31, v32, v33
	v_cvt_pk_bf16_f32 v32, v26, v27
	v_cvt_pk_bf16_f32 v33, v28, v29
	v_cvt_pk_bf16_f32 v113, v108, v109
	v_lshl_add_u64 v[106:107], s[48:49], 0, v[106:107]
	v_lshlrev_b64 v[90:91], 12, v[90:91]
	v_ashrrev_i32_e32 v75, 31, v74
	global_store_dwordx4 v[46:47], v[30:33], off offset:256
	global_store_dwordx4 v[152:153], v[110:113], off offset:256
	v_cvt_pk_bf16_f32 v97, v92, v93
	v_add_co_u32_e32 v32, vcc, s56, v152
	v_lshl_add_u64 v[110:111], v[106:107], 0, v[150:151]
	v_lshl_add_u64 v[90:91], s[48:49], 0, v[90:91]
	v_lshlrev_b64 v[74:75], 12, v[74:75]
	v_lshl_add_u64 v[30:31], v[152:153], 0, s[12:13]
	v_addc_co_u32_e32 v33, vcc, 0, v153, vcc
	v_cvt_pk_bf16_f32 v14, v14, v15
	v_cvt_pk_bf16_f32 v15, v16, v17
	v_cvt_pk_bf16_f32 v16, v10, v11
	v_cvt_pk_bf16_f32 v17, v12, v13
	global_store_dwordx4 v[110:111], v[94:97], off offset:256
	v_cvt_pk_bf16_f32 v81, v76, v77
	v_lshl_add_u64 v[74:75], s[48:49], 0, v[74:75]
	v_lshl_add_u64 v[94:95], v[90:91], 0, v[150:151]
	global_store_dwordx4 v[30:31], v[14:17], off offset:256
	v_cvt_pk_bf16_f32 v126, v126, v127
	v_cvt_pk_bf16_f32 v127, v128, v129
	v_add_co_u32_e32 v16, vcc, s57, v152
	v_cvt_pk_bf16_f32 v128, v122, v123
	v_cvt_pk_bf16_f32 v129, v124, v125
	v_cvt_pk_bf16_f32 v106, v118, v119
	v_cvt_pk_bf16_f32 v107, v120, v121
	v_cvt_pk_bf16_f32 v108, v114, v115
	v_cvt_pk_bf16_f32 v109, v116, v117
	v_cvt_pk_bf16_f32 v90, v102, v103
	v_cvt_pk_bf16_f32 v91, v104, v105
	v_cvt_pk_bf16_f32 v92, v98, v99
	v_cvt_pk_bf16_f32 v93, v100, v101
	global_store_dwordx4 v[94:95], v[78:81], off offset:256
	v_cvt_pk_bf16_f32 v76, v82, v83
	v_cvt_pk_bf16_f32 v77, v84, v85
	v_lshl_add_u64 v[78:79], v[74:75], 0, v[150:151]
	v_cvt_pk_bf16_f32 v74, v86, v87
	v_cvt_pk_bf16_f32 v75, v88, v89
	v_cvt_pk_bf16_f32 v73, v68, v69
	v_cvt_pk_bf16_f32 v65, v60, v61
	v_cvt_pk_bf16_f32 v42, v54, v55
	v_cvt_pk_bf16_f32 v43, v56, v57
	v_cvt_pk_bf16_f32 v44, v50, v51
	v_cvt_pk_bf16_f32 v45, v52, v53
	v_cvt_pk_bf16_f32 v26, v38, v39
	v_cvt_pk_bf16_f32 v27, v40, v41
	v_cvt_pk_bf16_f32 v28, v34, v35
	v_cvt_pk_bf16_f32 v29, v36, v37
	v_lshl_add_u64 v[14:15], v[152:153], 0, s[14:15]
	v_cvt_pk_bf16_f32 v10, v22, v23
	v_cvt_pk_bf16_f32 v11, v24, v25
	v_cvt_pk_bf16_f32 v12, v18, v19
	v_cvt_pk_bf16_f32 v13, v20, v21
	v_addc_co_u32_e32 v17, vcc, 0, v153, vcc
	v_cvt_pk_bf16_f32 v6, v6, v7
	v_cvt_pk_bf16_f32 v7, v8, v9
	v_cvt_pk_bf16_f32 v8, v2, v3
	v_cvt_pk_bf16_f32 v9, v4, v5
	s_cmp_eq_u32 s58, s33
	s_mov_b32 s60, s62
	s_mov_b32 s59, s61
	s_mov_b64 s[20:21], s[0:1]
	s_mov_b64 s[18:19], s[16:17]
	s_mov_b32 s22, s58
	global_store_dwordx4 v[152:153], v[126:129], off
	global_store_dwordx4 v[110:111], v[106:109], off
	global_store_dwordx4 v[94:95], v[90:93], off
	global_store_dwordx4 v[78:79], v[74:77], off
	global_store_dwordx4 v[78:79], v[70:73], off offset:256
	global_store_dwordx4 v[58:59], v[62:65], off
	global_store_dwordx4 v[48:49], v[42:45], off
	global_store_dwordx4 v[32:33], v[26:29], off
	global_store_dwordx4 v[16:17], v[10:13], off
	global_store_dwordx4 v[14:15], v[6:9], off offset:256
	s_cbranch_scc0 .LBB0_1600
	s_waitcnt vmcnt(0)
	s_cmpk_gt_u32 s36, 0xff
	v_readlane_b32 s93, v254, 9
	s_cbranch_scc1 .LBB0_1631
	s_barrier
